# P6 split into a U sweep (dots, gate weights kept in LDS) and a V sweep (axpy), rows issued three batches ahead into three rotating register buffers, dummy rows of partial batches skipped
# speedup vs baseline: 1.0215x; 1.0215x over previous
.LBB0_837:
	s_cmp_lt_u32 s2, 0x400001
	s_mov_b64 s[20:21], 0
	s_cselect_b64 s[22:23], -1, 0
	s_and_b64 vcc, exec, s[22:23]
	s_cbranch_vccz .LBB0_831
	s_branch .LBB0_836
.Lp6_tramp_1042:
	s_branch .LBB0_1042

.Lp6_tramp_423:
	s_branch .LBB0_423
.LBB0_838:
	s_or_b64 exec, exec, s[10:11]
	s_and_b64 s[10:11], s[12:13], exec

.LBB0_950:
	s_or_b64 exec, exec, s[0:1]
	s_waitcnt vmcnt(0)
	v_mov_b32_e32 v1, s85
	ds_read_b32 v1, v1 offset:4864
	s_or_b32 s96, s2, s33
	s_ashr_i32 s97, s96, 31
	v_readlane_b32 s22, v9, 63
	s_waitcnt lgkmcnt(0)
	v_readfirstlane_b32 s26, v1
	s_and_b32 s0, s26, 0x3ff
	s_bfe_u32 s1, s26, 0x4000a
	v_cmp_gt_u32_e32 vcc, s1, v182
	s_lshl_b32 s0, s0, 2
	s_add_i32 s0, s0, s85
	v_cndmask_b32_e32 v1, 0, v182, vcc
	v_lshl_add_u32 v1, v1, 2, s0
	ds_read_b32 v1, v1 offset:8192
	s_lshl_b64 s[0:1], s[96:97], 11
	s_lshr_b32 s23, s26, 3
	v_lshl_add_u64 v[142:143], v[76:77], 0, s[0:1]
	s_and_b32 s88, s23, 0x1ffff800
	s_waitcnt lgkmcnt(0)
	v_lshlrev_b32_e32 v1, 10, v1
	v_and_b32_e32 v1, 0x3fffc00, v1
	v_lshl_add_u64 v[12:13], v[142:143], 0, s[88:89]
	global_load_dwordx4 v[8:11], v[12:13], off
	global_load_dwordx4 v[4:7], v[12:13], off offset:16
	v_readlane_b32 s0, v1, 0
	v_readlane_b32 s1, v1, 1
	v_readlane_b32 s2, v1, 2
	v_readlane_b32 s3, v1, 3
	v_readlane_b32 s14, v1, 4
	v_readlane_b32 s15, v1, 5
	v_readlane_b32 s20, v1, 6
	v_readlane_b32 s21, v1, 7
	s_nop 4
	buffer_load_dwordx4 v[68:71], v181, s[8:11], s0 offen
	buffer_load_dwordx4 v[64:67], v181, s[8:11], s1 offen
	buffer_load_dwordx4 v[60:63], v181, s[8:11], s2 offen
	buffer_load_dwordx4 v[56:59], v181, s[8:11], s3 offen
	buffer_load_dwordx4 v[48:51], v181, s[8:11], s14 offen
	buffer_load_dwordx4 v[32:35], v181, s[8:11], s15 offen
	buffer_load_dwordx4 v[16:19], v181, s[8:11], s20 offen
	buffer_load_dwordx4 v[12:15], v181, s[8:11], s21 offen
	s_add_i32 s3, s22, -1
	s_min_i32 s2, s3, 1
	s_max_i32 s2, s2, 0
	s_lshl_b32 s2, s2, 2
	s_add_i32 s2, s85, s2
	v_mov_b32_e32 v1, s2
	ds_read_b32 v1, v1 offset:4864
	s_waitcnt lgkmcnt(0)
	v_readfirstlane_b32 s86, v1
	s_and_b32 s2, s86, 0x3ff
	s_bfe_u32 s3, s86, 0x4000a
	v_cmp_gt_u32_e32 vcc, s3, v182
	s_lshl_b32 s2, s2, 2
	s_add_i32 s2, s2, s85
	v_cndmask_b32_e32 v1, 0, v182, vcc
	v_lshl_add_u32 v1, v1, 2, s2
	ds_read_b32 v1, v1 offset:8192
	s_waitcnt lgkmcnt(0)
	v_lshlrev_b32_e32 v1, 10, v1
	v_and_b32_e32 v1, 0x3fffc00, v1
	s_nop 0
	v_readlane_b32 s44, v1, 0
	v_readlane_b32 s45, v1, 1
	v_readlane_b32 s46, v1, 2
	v_readlane_b32 s47, v1, 3
	v_readlane_b32 s48, v1, 4
	v_readlane_b32 s49, v1, 5
	v_readlane_b32 s50, v1, 6
	v_readlane_b32 s51, v1, 7
	s_nop 4
	buffer_load_dwordx4 v[72:75], v181, s[8:11], s44 offen
	buffer_load_dwordx4 v[52:55], v181, s[8:11], s45 offen
	buffer_load_dwordx4 v[44:47], v181, s[8:11], s46 offen
	buffer_load_dwordx4 v[40:43], v181, s[8:11], s47 offen
	buffer_load_dwordx4 v[36:39], v181, s[8:11], s48 offen
	buffer_load_dwordx4 v[28:31], v181, s[8:11], s49 offen
	buffer_load_dwordx4 v[24:27], v181, s[8:11], s50 offen
	buffer_load_dwordx4 v[20:23], v181, s[8:11], s51 offen
	s_add_i32 s3, s22, -1
	s_min_i32 s2, s3, 2
	s_max_i32 s2, s2, 0
	s_lshl_b32 s2, s2, 2
	s_add_i32 s2, s85, s2
	v_mov_b32_e32 v1, s2
	ds_read_b32 v1, v1 offset:4864
	s_waitcnt lgkmcnt(0)
	v_readfirstlane_b32 s27, v1
	s_and_b32 s2, s27, 0x3ff
	s_bfe_u32 s3, s27, 0x4000a
	v_cmp_gt_u32_e32 vcc, s3, v182
	s_lshl_b32 s2, s2, 2
	s_add_i32 s2, s2, s85
	v_cndmask_b32_e32 v1, 0, v182, vcc
	v_lshl_add_u32 v1, v1, 2, s2
	ds_read_b32 v1, v1 offset:8192
	s_waitcnt lgkmcnt(0)
	v_lshlrev_b32_e32 v1, 10, v1
	v_and_b32_e32 v1, 0x3fffc00, v1
	s_nop 0
	v_readlane_b32 s44, v1, 0
	v_readlane_b32 s45, v1, 1
	v_readlane_b32 s46, v1, 2
	v_readlane_b32 s47, v1, 3
	v_readlane_b32 s48, v1, 4
	v_readlane_b32 s49, v1, 5
	v_readlane_b32 s50, v1, 6
	v_readlane_b32 s51, v1, 7
	s_nop 4
	buffer_load_dwordx4 v[224:227], v181, s[8:11], s44 offen
	buffer_load_dwordx4 v[228:231], v181, s[8:11], s45 offen
	buffer_load_dwordx4 v[232:235], v181, s[8:11], s46 offen
	buffer_load_dwordx4 v[236:239], v181, s[8:11], s47 offen
	buffer_load_dwordx4 v[240:243], v181, s[8:11], s48 offen
	buffer_load_dwordx4 v[244:247], v181, s[8:11], s49 offen
	buffer_load_dwordx4 v[248:251], v181, s[8:11], s50 offen
	buffer_load_dwordx4 v[216:219], v181, s[8:11], s51 offen
	s_cmp_lt_i32 s22, 1
	s_cbranch_scc1 .LBB0_974
	v_mov_b32_e32 v84, 0
	s_mov_b32 s23, 0
	s_mov_b64 s[0:1], -1
	v_mov_b32_e32 v158, 0
	v_mov_b32_e32 v159, 0
	v_mov_b32_e32 v156, 0
	v_mov_b32_e32 v157, 0
	v_mov_b32_e32 v154, 0
	v_mov_b32_e32 v155, 0
	v_mov_b32_e32 v152, 0
	v_mov_b32_e32 v153, 0
	v_mov_b32_e32 v150, 0
	v_mov_b32_e32 v151, 0
	v_mov_b32_e32 v148, 0
	v_mov_b32_e32 v149, 0
	v_mov_b32_e32 v146, 0
	v_mov_b32_e32 v147, 0
	v_mov_b32_e32 v144, 0
	v_mov_b32_e32 v145, 0
	v_mov_b32_e32 v85, v84
	v_mov_b32_e32 v92, v84
	v_mov_b32_e32 v93, v84
	v_mov_b32_e32 v90, v84
	v_mov_b32_e32 v91, v84
	v_mov_b32_e32 v88, v84
	v_mov_b32_e32 v89, v84
	v_mov_b32_e32 v86, v84
	v_mov_b32_e32 v87, v84
	v_mov_b32_e32 v82, v84
	v_mov_b32_e32 v83, v84
	v_mov_b32_e32 v80, v84
	v_mov_b32_e32 v81, v84
	v_mov_b32_e32 v78, v84
	v_mov_b32_e32 v79, v84
	v_mov_b32_e32 v108, v84
	v_mov_b32_e32 v109, v84
	v_mov_b32_e32 v106, v84
	v_mov_b32_e32 v107, v84
	v_mov_b32_e32 v104, v84
	v_mov_b32_e32 v105, v84
	v_mov_b32_e32 v102, v84
	v_mov_b32_e32 v103, v84
	v_mov_b32_e32 v100, v84
	v_mov_b32_e32 v101, v84
	v_mov_b32_e32 v98, v84
	v_mov_b32_e32 v99, v84
	v_mov_b32_e32 v96, v84
	v_mov_b32_e32 v97, v84
	v_mov_b32_e32 v94, v84
	v_mov_b32_e32 v95, v84
	v_mov_b32_e32 v124, v84
	v_mov_b32_e32 v125, v84
	v_mov_b32_e32 v122, v84
	v_mov_b32_e32 v123, v84
	v_mov_b32_e32 v120, v84
	v_mov_b32_e32 v121, v84
	v_mov_b32_e32 v118, v84
	v_mov_b32_e32 v119, v84
	v_mov_b32_e32 v116, v84
	v_mov_b32_e32 v117, v84
	v_mov_b32_e32 v114, v84
	v_mov_b32_e32 v115, v84
	v_mov_b32_e32 v112, v84
	v_mov_b32_e32 v113, v84
	v_mov_b32_e32 v110, v84
	v_mov_b32_e32 v111, v84
	v_mov_b32_e32 v140, v84
	v_mov_b32_e32 v141, v84
	v_mov_b32_e32 v138, v84
	v_mov_b32_e32 v139, v84
	v_mov_b32_e32 v136, v84
	v_mov_b32_e32 v137, v84
	v_mov_b32_e32 v134, v84
	v_mov_b32_e32 v135, v84
	v_mov_b32_e32 v132, v84
	v_mov_b32_e32 v133, v84
	v_mov_b32_e32 v130, v84
	v_mov_b32_e32 v131, v84
	v_mov_b32_e32 v128, v84
	v_mov_b32_e32 v129, v84
	v_mov_b32_e32 v126, v84
	v_mov_b32_e32 v127, v84
.Lp6a0_top:
	s_add_i32 s23, s23, 1
	s_add_i32 s2, s23, 2
	s_add_i32 s3, s22, -1
	s_min_i32 s2, s2, s3
	s_lshl_b32 s2, s2, 2
	s_add_i32 s2, s85, s2
	v_mov_b32_e32 v1, s2
	ds_read_b32 v1, v1 offset:4864
	s_waitcnt lgkmcnt(0)
	v_readfirstlane_b32 s32, v1
	s_and_b32 s2, s32, 0x3ff
	s_bfe_u32 s3, s32, 0x4000a
	v_cmp_gt_u32_e32 vcc, s3, v182
	s_lshl_b32 s2, s2, 2
	s_add_i32 s2, s2, s85
	v_cndmask_b32_e32 v1, 0, v182, vcc
	v_lshl_add_u32 v1, v1, 2, s2
	ds_read_b32 v1, v1 offset:8192
	s_waitcnt vmcnt(16)
	s_andn2_b64 vcc, exec, s[0:1]
	s_waitcnt lgkmcnt(0)
	v_lshlrev_b32_e32 v1, 10, v1
	v_and_b32_e32 v1, 0x3fffc00, v1
	s_nop 0
	v_readlane_b32 s44, v1, 0
	v_readlane_b32 s45, v1, 1
	v_readlane_b32 s46, v1, 2
	v_readlane_b32 s47, v1, 3
	v_readlane_b32 s48, v1, 4
	v_readlane_b32 s49, v1, 5
	v_readlane_b32 s50, v1, 6
	v_readlane_b32 s51, v1, 7
	s_cbranch_vccnz .Lp6a0_954
	s_waitcnt vmcnt(8)
	v_lshlrev_b32_e32 v144, 16, v8
	v_and_b32_e32 v145, 0xffff0000, v8
	v_lshlrev_b32_e32 v146, 16, v9
	v_and_b32_e32 v147, 0xffff0000, v9
	v_lshlrev_b32_e32 v148, 16, v10
	v_and_b32_e32 v149, 0xffff0000, v10
	v_lshlrev_b32_e32 v150, 16, v11
	v_and_b32_e32 v151, 0xffff0000, v11
	v_lshlrev_b32_e32 v152, 16, v4
	v_and_b32_e32 v153, 0xffff0000, v4
	v_lshlrev_b32_e32 v154, 16, v5
	v_and_b32_e32 v155, 0xffff0000, v5
	v_lshlrev_b32_e32 v156, 16, v6
	v_and_b32_e32 v157, 0xffff0000, v6
	v_lshlrev_b32_e32 v158, 16, v7
	v_and_b32_e32 v159, 0xffff0000, v7

.Lp6a0_956:
	s_bfe_u32 s36, s26, 0x4000a
	v_cvt_pk_f32_fp8_e32 v[184:185], v68
	v_cvt_pk_f32_fp8_e32 v[192:193], v64
	v_cvt_pk_f32_fp8_sdwa v[186:187], v68 src0_sel:WORD_1
	v_cvt_pk_f32_fp8_sdwa v[194:195], v64 src0_sel:WORD_1
	v_pk_mul_f32 v[188:189], v[184:185], v[144:145]
	v_pk_mul_f32 v[222:223], v[192:193], v[144:145]
	v_pk_mul_f32 v[190:191], v[186:187], v[146:147]
	v_pk_mul_f32 v[176:177], v[194:195], v[146:147]
	v_cvt_pk_f32_fp8_e32 v[184:185], v69
	v_cvt_pk_f32_fp8_e32 v[192:193], v65
	v_cvt_pk_f32_fp8_sdwa v[186:187], v69 src0_sel:WORD_1
	v_cvt_pk_f32_fp8_sdwa v[194:195], v65 src0_sel:WORD_1
	v_pk_fma_f32 v[188:189], v[184:185], v[148:149], v[188:189]
	v_pk_fma_f32 v[222:223], v[192:193], v[148:149], v[222:223]
	v_pk_fma_f32 v[190:191], v[186:187], v[150:151], v[190:191]
	v_pk_fma_f32 v[176:177], v[194:195], v[150:151], v[176:177]
	v_cvt_pk_f32_fp8_e32 v[184:185], v70
	v_cvt_pk_f32_fp8_e32 v[192:193], v66
	v_cvt_pk_f32_fp8_sdwa v[186:187], v70 src0_sel:WORD_1
	v_cvt_pk_f32_fp8_sdwa v[194:195], v66 src0_sel:WORD_1
	v_pk_fma_f32 v[188:189], v[184:185], v[152:153], v[188:189]
	v_pk_fma_f32 v[222:223], v[192:193], v[152:153], v[222:223]
	v_pk_fma_f32 v[190:191], v[186:187], v[154:155], v[190:191]
	v_pk_fma_f32 v[176:177], v[194:195], v[154:155], v[176:177]
	v_cvt_pk_f32_fp8_e32 v[184:185], v71
	v_cvt_pk_f32_fp8_e32 v[192:193], v67
	v_cvt_pk_f32_fp8_sdwa v[186:187], v71 src0_sel:WORD_1
	v_cvt_pk_f32_fp8_sdwa v[194:195], v67 src0_sel:WORD_1
	v_pk_fma_f32 v[188:189], v[184:185], v[156:157], v[188:189]
	v_pk_fma_f32 v[222:223], v[192:193], v[156:157], v[222:223]
	v_pk_fma_f32 v[190:191], v[186:187], v[158:159], v[190:191]
	v_pk_fma_f32 v[176:177], v[194:195], v[158:159], v[176:177]
	v_pk_add_f32 v[188:189], v[188:189], v[190:191]
	v_pk_add_f32 v[222:223], v[222:223], v[176:177]
	v_add_f32_e32 v160, v188, v189
	v_add_f32_e32 v162, v222, v223
	s_cmp_le_u32 s36, 2
	s_cbranch_scc1 .Lp6a0_dotdone
	v_cvt_pk_f32_fp8_e32 v[184:185], v60
	v_cvt_pk_f32_fp8_e32 v[192:193], v56
	v_cvt_pk_f32_fp8_sdwa v[186:187], v60 src0_sel:WORD_1
	v_cvt_pk_f32_fp8_sdwa v[194:195], v56 src0_sel:WORD_1
	v_pk_mul_f32 v[188:189], v[184:185], v[144:145]
	v_pk_mul_f32 v[222:223], v[192:193], v[144:145]
	v_pk_mul_f32 v[190:191], v[186:187], v[146:147]
	v_pk_mul_f32 v[176:177], v[194:195], v[146:147]
	v_cvt_pk_f32_fp8_e32 v[184:185], v61
	v_cvt_pk_f32_fp8_e32 v[192:193], v57
	v_cvt_pk_f32_fp8_sdwa v[186:187], v61 src0_sel:WORD_1
	v_cvt_pk_f32_fp8_sdwa v[194:195], v57 src0_sel:WORD_1
	v_pk_fma_f32 v[188:189], v[184:185], v[148:149], v[188:189]
	v_pk_fma_f32 v[222:223], v[192:193], v[148:149], v[222:223]
	v_pk_fma_f32 v[190:191], v[186:187], v[150:151], v[190:191]
	v_pk_fma_f32 v[176:177], v[194:195], v[150:151], v[176:177]
	v_cvt_pk_f32_fp8_e32 v[184:185], v62
	v_cvt_pk_f32_fp8_e32 v[192:193], v58
	v_cvt_pk_f32_fp8_sdwa v[186:187], v62 src0_sel:WORD_1
	v_cvt_pk_f32_fp8_sdwa v[194:195], v58 src0_sel:WORD_1
	v_pk_fma_f32 v[188:189], v[184:185], v[152:153], v[188:189]
	v_pk_fma_f32 v[222:223], v[192:193], v[152:153], v[222:223]
	v_pk_fma_f32 v[190:191], v[186:187], v[154:155], v[190:191]
	v_pk_fma_f32 v[176:177], v[194:195], v[154:155], v[176:177]
	v_cvt_pk_f32_fp8_e32 v[184:185], v63
	v_cvt_pk_f32_fp8_e32 v[192:193], v59
	v_cvt_pk_f32_fp8_sdwa v[186:187], v63 src0_sel:WORD_1
	v_cvt_pk_f32_fp8_sdwa v[194:195], v59 src0_sel:WORD_1
	v_pk_fma_f32 v[188:189], v[184:185], v[156:157], v[188:189]
	v_pk_fma_f32 v[222:223], v[192:193], v[156:157], v[222:223]
	v_pk_fma_f32 v[190:191], v[186:187], v[158:159], v[190:191]
	v_pk_fma_f32 v[176:177], v[194:195], v[158:159], v[176:177]
	v_pk_add_f32 v[188:189], v[188:189], v[190:191]
	v_pk_add_f32 v[222:223], v[222:223], v[176:177]
	v_add_f32_e32 v164, v188, v189
	v_add_f32_e32 v166, v222, v223
	s_cmp_le_u32 s36, 4
	s_cbranch_scc1 .Lp6a0_dotdone
	v_cvt_pk_f32_fp8_e32 v[184:185], v48
	v_cvt_pk_f32_fp8_e32 v[192:193], v32
	v_cvt_pk_f32_fp8_sdwa v[186:187], v48 src0_sel:WORD_1
	v_cvt_pk_f32_fp8_sdwa v[194:195], v32 src0_sel:WORD_1
	v_pk_mul_f32 v[188:189], v[184:185], v[144:145]
	v_pk_mul_f32 v[222:223], v[192:193], v[144:145]
	v_pk_mul_f32 v[190:191], v[186:187], v[146:147]
	v_pk_mul_f32 v[176:177], v[194:195], v[146:147]
	v_cvt_pk_f32_fp8_e32 v[184:185], v49
	v_cvt_pk_f32_fp8_e32 v[192:193], v33
	v_cvt_pk_f32_fp8_sdwa v[186:187], v49 src0_sel:WORD_1
	v_cvt_pk_f32_fp8_sdwa v[194:195], v33 src0_sel:WORD_1
	v_pk_fma_f32 v[188:189], v[184:185], v[148:149], v[188:189]
	v_pk_fma_f32 v[222:223], v[192:193], v[148:149], v[222:223]
	v_pk_fma_f32 v[190:191], v[186:187], v[150:151], v[190:191]
	v_pk_fma_f32 v[176:177], v[194:195], v[150:151], v[176:177]
	v_cvt_pk_f32_fp8_e32 v[184:185], v50
	v_cvt_pk_f32_fp8_e32 v[192:193], v34
	v_cvt_pk_f32_fp8_sdwa v[186:187], v50 src0_sel:WORD_1
	v_cvt_pk_f32_fp8_sdwa v[194:195], v34 src0_sel:WORD_1
	v_pk_fma_f32 v[188:189], v[184:185], v[152:153], v[188:189]
	v_pk_fma_f32 v[222:223], v[192:193], v[152:153], v[222:223]
	v_pk_fma_f32 v[190:191], v[186:187], v[154:155], v[190:191]
	v_pk_fma_f32 v[176:177], v[194:195], v[154:155], v[176:177]
	v_cvt_pk_f32_fp8_e32 v[184:185], v51
	v_cvt_pk_f32_fp8_e32 v[192:193], v35
	v_cvt_pk_f32_fp8_sdwa v[186:187], v51 src0_sel:WORD_1
	v_cvt_pk_f32_fp8_sdwa v[194:195], v35 src0_sel:WORD_1
	v_pk_fma_f32 v[188:189], v[184:185], v[156:157], v[188:189]
	v_pk_fma_f32 v[222:223], v[192:193], v[156:157], v[222:223]
	v_pk_fma_f32 v[190:191], v[186:187], v[158:159], v[190:191]
	v_pk_fma_f32 v[176:177], v[194:195], v[158:159], v[176:177]
	v_pk_add_f32 v[188:189], v[188:189], v[190:191]
	v_pk_add_f32 v[222:223], v[222:223], v[176:177]
	v_add_f32_e32 v168, v188, v189
	v_add_f32_e32 v170, v222, v223
	s_cmp_le_u32 s36, 6
	s_cbranch_scc1 .Lp6a0_dotdone
	v_cvt_pk_f32_fp8_e32 v[184:185], v16
	v_cvt_pk_f32_fp8_e32 v[192:193], v12
	v_cvt_pk_f32_fp8_sdwa v[186:187], v16 src0_sel:WORD_1
	v_cvt_pk_f32_fp8_sdwa v[194:195], v12 src0_sel:WORD_1
	v_pk_mul_f32 v[188:189], v[184:185], v[144:145]
	v_pk_mul_f32 v[222:223], v[192:193], v[144:145]
	v_pk_mul_f32 v[190:191], v[186:187], v[146:147]
	v_pk_mul_f32 v[176:177], v[194:195], v[146:147]
	v_cvt_pk_f32_fp8_e32 v[184:185], v17
	v_cvt_pk_f32_fp8_e32 v[192:193], v13
	v_cvt_pk_f32_fp8_sdwa v[186:187], v17 src0_sel:WORD_1
	v_cvt_pk_f32_fp8_sdwa v[194:195], v13 src0_sel:WORD_1
	v_pk_fma_f32 v[188:189], v[184:185], v[148:149], v[188:189]
	v_pk_fma_f32 v[222:223], v[192:193], v[148:149], v[222:223]
	v_pk_fma_f32 v[190:191], v[186:187], v[150:151], v[190:191]
	v_pk_fma_f32 v[176:177], v[194:195], v[150:151], v[176:177]
	v_cvt_pk_f32_fp8_e32 v[184:185], v18
	v_cvt_pk_f32_fp8_e32 v[192:193], v14
	v_cvt_pk_f32_fp8_sdwa v[186:187], v18 src0_sel:WORD_1
	v_cvt_pk_f32_fp8_sdwa v[194:195], v14 src0_sel:WORD_1
	v_pk_fma_f32 v[188:189], v[184:185], v[152:153], v[188:189]
	v_pk_fma_f32 v[222:223], v[192:193], v[152:153], v[222:223]
	v_pk_fma_f32 v[190:191], v[186:187], v[154:155], v[190:191]
	v_pk_fma_f32 v[176:177], v[194:195], v[154:155], v[176:177]
	v_cvt_pk_f32_fp8_e32 v[184:185], v19
	v_cvt_pk_f32_fp8_e32 v[192:193], v15
	v_cvt_pk_f32_fp8_sdwa v[186:187], v19 src0_sel:WORD_1
	v_cvt_pk_f32_fp8_sdwa v[194:195], v15 src0_sel:WORD_1
	v_pk_fma_f32 v[188:189], v[184:185], v[156:157], v[188:189]
	v_pk_fma_f32 v[222:223], v[192:193], v[156:157], v[222:223]
	v_pk_fma_f32 v[190:191], v[186:187], v[158:159], v[190:191]
	v_pk_fma_f32 v[176:177], v[194:195], v[158:159], v[176:177]
	v_pk_add_f32 v[188:189], v[188:189], v[190:191]
	v_pk_add_f32 v[222:223], v[222:223], v[176:177]
	v_add_f32_e32 v172, v188, v189
	v_add_f32_e32 v174, v222, v223
.Lp6a0_dotdone:
	s_nop 4
	buffer_load_dwordx4 v[68:71], v181, s[8:11], s44 offen
	buffer_load_dwordx4 v[64:67], v181, s[8:11], s45 offen
	buffer_load_dwordx4 v[60:63], v181, s[8:11], s46 offen
	buffer_load_dwordx4 v[56:59], v181, s[8:11], s47 offen
	buffer_load_dwordx4 v[48:51], v181, s[8:11], s48 offen
	buffer_load_dwordx4 v[32:35], v181, s[8:11], s49 offen
	buffer_load_dwordx4 v[16:19], v181, s[8:11], s50 offen
	buffer_load_dwordx4 v[12:15], v181, s[8:11], s51 offen
	v_permlane32_swap_b32_e32 v160, v168
	v_permlane32_swap_b32_e32 v162, v170
	v_permlane32_swap_b32_e32 v164, v172
	v_permlane32_swap_b32_e32 v166, v174
	v_add_f32_e32 v1, v160, v168
	v_add_f32_e32 v2, v162, v170
	v_add_f32_e32 v160, v164, v172
	v_add_f32_e32 v161, v166, v174
	s_nop 0
	v_permlane16_swap_b32_e32 v1, v160
	v_permlane16_swap_b32_e32 v2, v161
	v_add_f32_e32 v1, v1, v160
	v_add_f32_e32 v2, v2, v161
	v_cndmask_b32_e64 v160, v1, v2, s[4:5]
	v_cndmask_b32_e64 v1, v2, v1, s[4:5]
	s_bfe_u32 s14, s26, 0x4000a
	v_cmp_gt_u32_e32 vcc, s14, v180
	v_add_f32_dpp v1, v160, v1 row_ror:8 row_mask:0xf bank_mask:0xf bound_ctrl:1
	s_nop 1
	v_add_f32_dpp v1, v1, v1 row_half_mirror row_mask:0xf bank_mask:0xf bound_ctrl:1
	s_nop 1
	v_add_f32_dpp v2, v1, v1 quad_perm:[1,0,3,2] row_mask:0xf bank_mask:0xf bound_ctrl:1
	v_mov_b32_e32 v1, 0
	s_nop 0
	v_mov_b32_dpp v160, v2 quad_perm:[2,3,0,1] row_mask:0xf bank_mask:0xf bound_ctrl:1
	s_and_saveexec_b64 s[14:15], vcc
	s_cbranch_execz .Lp6a0_958
	s_and_b32 s26, s26, 0x3ff
	v_add_u32_e32 v1, s26, v180
	v_lshl_add_u32 v1, v1, 2, s85
	v_mov_b32_e32 v185, v1
	v_add_f32_e32 v2, v2, v160
	ds_read2st64_b32 v[160:161], v1 offset1:48
	s_mov_b32 s26, 0x3e6d3388
	s_waitcnt lgkmcnt(0)
	v_mul_f32_e32 v1, v2, v160
	v_fma_f32 v2, |v1|, s26, 1.0
	v_rcp_f32_e32 v2, v2
	v_mov_b32_e32 v160, 0xbf3a00e3
	v_cmp_gt_f32_e32 vcc, 0, v1
	v_fmamk_f32 v160, v2, 0x3f07dc22, v160
	v_fmaak_f32 v160, v2, v160, 0x3f35f0e3
	v_fmaak_f32 v160, v2, v160, 0xbe11a98e
	v_fmaak_f32 v160, v2, v160, 0x3e027906
	v_mul_f32_e32 v2, v2, v160
	v_mul_f32_e32 v160, v1, v1
	v_mul_f32_e32 v160, 0xbf38aa3b, v160
	v_exp_f32_e32 v160, v160
	s_nop 0
	v_mul_f32_e32 v2, v160, v2
	v_mul_f32_e32 v160, v1, v2
	v_fma_f32 v1, -v1, v2, v1
	v_cndmask_b32_e32 v1, v1, v160, vcc
	v_mul_f32_e32 v1, v161, v1
	ds_write_b32 v185, v1 offset:12288
.Lp6a0_958:
	s_or_b64 exec, exec, s[14:15]
	s_mov_b32 s26, s86
	s_mov_b32 s86, s27
	s_mov_b32 s27, s32
	s_cmp_eq_u32 s22, s23
	s_cbranch_scc1 .Lp6_Adone

.Lp6a1_956:
	s_bfe_u32 s36, s26, 0x4000a
	v_cvt_pk_f32_fp8_e32 v[184:185], v72
	v_cvt_pk_f32_fp8_e32 v[192:193], v52
	v_cvt_pk_f32_fp8_sdwa v[186:187], v72 src0_sel:WORD_1
	v_cvt_pk_f32_fp8_sdwa v[194:195], v52 src0_sel:WORD_1
	v_pk_mul_f32 v[188:189], v[184:185], v[144:145]
	v_pk_mul_f32 v[222:223], v[192:193], v[144:145]
	v_pk_mul_f32 v[190:191], v[186:187], v[146:147]
	v_pk_mul_f32 v[176:177], v[194:195], v[146:147]
	v_cvt_pk_f32_fp8_e32 v[184:185], v73
	v_cvt_pk_f32_fp8_e32 v[192:193], v53
	v_cvt_pk_f32_fp8_sdwa v[186:187], v73 src0_sel:WORD_1
	v_cvt_pk_f32_fp8_sdwa v[194:195], v53 src0_sel:WORD_1
	v_pk_fma_f32 v[188:189], v[184:185], v[148:149], v[188:189]
	v_pk_fma_f32 v[222:223], v[192:193], v[148:149], v[222:223]
	v_pk_fma_f32 v[190:191], v[186:187], v[150:151], v[190:191]
	v_pk_fma_f32 v[176:177], v[194:195], v[150:151], v[176:177]
	v_cvt_pk_f32_fp8_e32 v[184:185], v74
	v_cvt_pk_f32_fp8_e32 v[192:193], v54
	v_cvt_pk_f32_fp8_sdwa v[186:187], v74 src0_sel:WORD_1
	v_cvt_pk_f32_fp8_sdwa v[194:195], v54 src0_sel:WORD_1
	v_pk_fma_f32 v[188:189], v[184:185], v[152:153], v[188:189]
	v_pk_fma_f32 v[222:223], v[192:193], v[152:153], v[222:223]
	v_pk_fma_f32 v[190:191], v[186:187], v[154:155], v[190:191]
	v_pk_fma_f32 v[176:177], v[194:195], v[154:155], v[176:177]
	v_cvt_pk_f32_fp8_e32 v[184:185], v75
	v_cvt_pk_f32_fp8_e32 v[192:193], v55
	v_cvt_pk_f32_fp8_sdwa v[186:187], v75 src0_sel:WORD_1
	v_cvt_pk_f32_fp8_sdwa v[194:195], v55 src0_sel:WORD_1
	v_pk_fma_f32 v[188:189], v[184:185], v[156:157], v[188:189]
	v_pk_fma_f32 v[222:223], v[192:193], v[156:157], v[222:223]
	v_pk_fma_f32 v[190:191], v[186:187], v[158:159], v[190:191]
	v_pk_fma_f32 v[176:177], v[194:195], v[158:159], v[176:177]
	v_pk_add_f32 v[188:189], v[188:189], v[190:191]
	v_pk_add_f32 v[222:223], v[222:223], v[176:177]
	v_add_f32_e32 v160, v188, v189
	v_add_f32_e32 v162, v222, v223
	s_cmp_le_u32 s36, 2
	s_cbranch_scc1 .Lp6a1_dotdone
	v_cvt_pk_f32_fp8_e32 v[184:185], v44
	v_cvt_pk_f32_fp8_e32 v[192:193], v40
	v_cvt_pk_f32_fp8_sdwa v[186:187], v44 src0_sel:WORD_1
	v_cvt_pk_f32_fp8_sdwa v[194:195], v40 src0_sel:WORD_1
	v_pk_mul_f32 v[188:189], v[184:185], v[144:145]
	v_pk_mul_f32 v[222:223], v[192:193], v[144:145]
	v_pk_mul_f32 v[190:191], v[186:187], v[146:147]
	v_pk_mul_f32 v[176:177], v[194:195], v[146:147]
	v_cvt_pk_f32_fp8_e32 v[184:185], v45
	v_cvt_pk_f32_fp8_e32 v[192:193], v41
	v_cvt_pk_f32_fp8_sdwa v[186:187], v45 src0_sel:WORD_1
	v_cvt_pk_f32_fp8_sdwa v[194:195], v41 src0_sel:WORD_1
	v_pk_fma_f32 v[188:189], v[184:185], v[148:149], v[188:189]
	v_pk_fma_f32 v[222:223], v[192:193], v[148:149], v[222:223]
	v_pk_fma_f32 v[190:191], v[186:187], v[150:151], v[190:191]
	v_pk_fma_f32 v[176:177], v[194:195], v[150:151], v[176:177]
	v_cvt_pk_f32_fp8_e32 v[184:185], v46
	v_cvt_pk_f32_fp8_e32 v[192:193], v42
	v_cvt_pk_f32_fp8_sdwa v[186:187], v46 src0_sel:WORD_1
	v_cvt_pk_f32_fp8_sdwa v[194:195], v42 src0_sel:WORD_1
	v_pk_fma_f32 v[188:189], v[184:185], v[152:153], v[188:189]
	v_pk_fma_f32 v[222:223], v[192:193], v[152:153], v[222:223]
	v_pk_fma_f32 v[190:191], v[186:187], v[154:155], v[190:191]
	v_pk_fma_f32 v[176:177], v[194:195], v[154:155], v[176:177]
	v_cvt_pk_f32_fp8_e32 v[184:185], v47
	v_cvt_pk_f32_fp8_e32 v[192:193], v43
	v_cvt_pk_f32_fp8_sdwa v[186:187], v47 src0_sel:WORD_1
	v_cvt_pk_f32_fp8_sdwa v[194:195], v43 src0_sel:WORD_1
	v_pk_fma_f32 v[188:189], v[184:185], v[156:157], v[188:189]
	v_pk_fma_f32 v[222:223], v[192:193], v[156:157], v[222:223]
	v_pk_fma_f32 v[190:191], v[186:187], v[158:159], v[190:191]
	v_pk_fma_f32 v[176:177], v[194:195], v[158:159], v[176:177]
	v_pk_add_f32 v[188:189], v[188:189], v[190:191]
	v_pk_add_f32 v[222:223], v[222:223], v[176:177]
	v_add_f32_e32 v164, v188, v189
	v_add_f32_e32 v166, v222, v223
	s_cmp_le_u32 s36, 4
	s_cbranch_scc1 .Lp6a1_dotdone
	v_cvt_pk_f32_fp8_e32 v[184:185], v36
	v_cvt_pk_f32_fp8_e32 v[192:193], v28
	v_cvt_pk_f32_fp8_sdwa v[186:187], v36 src0_sel:WORD_1
	v_cvt_pk_f32_fp8_sdwa v[194:195], v28 src0_sel:WORD_1
	v_pk_mul_f32 v[188:189], v[184:185], v[144:145]
	v_pk_mul_f32 v[222:223], v[192:193], v[144:145]
	v_pk_mul_f32 v[190:191], v[186:187], v[146:147]
	v_pk_mul_f32 v[176:177], v[194:195], v[146:147]
	v_cvt_pk_f32_fp8_e32 v[184:185], v37
	v_cvt_pk_f32_fp8_e32 v[192:193], v29
	v_cvt_pk_f32_fp8_sdwa v[186:187], v37 src0_sel:WORD_1
	v_cvt_pk_f32_fp8_sdwa v[194:195], v29 src0_sel:WORD_1
	v_pk_fma_f32 v[188:189], v[184:185], v[148:149], v[188:189]
	v_pk_fma_f32 v[222:223], v[192:193], v[148:149], v[222:223]
	v_pk_fma_f32 v[190:191], v[186:187], v[150:151], v[190:191]
	v_pk_fma_f32 v[176:177], v[194:195], v[150:151], v[176:177]
	v_cvt_pk_f32_fp8_e32 v[184:185], v38
	v_cvt_pk_f32_fp8_e32 v[192:193], v30
	v_cvt_pk_f32_fp8_sdwa v[186:187], v38 src0_sel:WORD_1
	v_cvt_pk_f32_fp8_sdwa v[194:195], v30 src0_sel:WORD_1
	v_pk_fma_f32 v[188:189], v[184:185], v[152:153], v[188:189]
	v_pk_fma_f32 v[222:223], v[192:193], v[152:153], v[222:223]
	v_pk_fma_f32 v[190:191], v[186:187], v[154:155], v[190:191]
	v_pk_fma_f32 v[176:177], v[194:195], v[154:155], v[176:177]
	v_cvt_pk_f32_fp8_e32 v[184:185], v39
	v_cvt_pk_f32_fp8_e32 v[192:193], v31
	v_cvt_pk_f32_fp8_sdwa v[186:187], v39 src0_sel:WORD_1
	v_cvt_pk_f32_fp8_sdwa v[194:195], v31 src0_sel:WORD_1
	v_pk_fma_f32 v[188:189], v[184:185], v[156:157], v[188:189]
	v_pk_fma_f32 v[222:223], v[192:193], v[156:157], v[222:223]
	v_pk_fma_f32 v[190:191], v[186:187], v[158:159], v[190:191]
	v_pk_fma_f32 v[176:177], v[194:195], v[158:159], v[176:177]
	v_pk_add_f32 v[188:189], v[188:189], v[190:191]
	v_pk_add_f32 v[222:223], v[222:223], v[176:177]
	v_add_f32_e32 v168, v188, v189
	v_add_f32_e32 v170, v222, v223
	s_cmp_le_u32 s36, 6
	s_cbranch_scc1 .Lp6a1_dotdone
	v_cvt_pk_f32_fp8_e32 v[184:185], v24
	v_cvt_pk_f32_fp8_e32 v[192:193], v20
	v_cvt_pk_f32_fp8_sdwa v[186:187], v24 src0_sel:WORD_1
	v_cvt_pk_f32_fp8_sdwa v[194:195], v20 src0_sel:WORD_1
	v_pk_mul_f32 v[188:189], v[184:185], v[144:145]
	v_pk_mul_f32 v[222:223], v[192:193], v[144:145]
	v_pk_mul_f32 v[190:191], v[186:187], v[146:147]
	v_pk_mul_f32 v[176:177], v[194:195], v[146:147]
	v_cvt_pk_f32_fp8_e32 v[184:185], v25
	v_cvt_pk_f32_fp8_e32 v[192:193], v21
	v_cvt_pk_f32_fp8_sdwa v[186:187], v25 src0_sel:WORD_1
	v_cvt_pk_f32_fp8_sdwa v[194:195], v21 src0_sel:WORD_1
	v_pk_fma_f32 v[188:189], v[184:185], v[148:149], v[188:189]
	v_pk_fma_f32 v[222:223], v[192:193], v[148:149], v[222:223]
	v_pk_fma_f32 v[190:191], v[186:187], v[150:151], v[190:191]
	v_pk_fma_f32 v[176:177], v[194:195], v[150:151], v[176:177]
	v_cvt_pk_f32_fp8_e32 v[184:185], v26
	v_cvt_pk_f32_fp8_e32 v[192:193], v22
	v_cvt_pk_f32_fp8_sdwa v[186:187], v26 src0_sel:WORD_1
	v_cvt_pk_f32_fp8_sdwa v[194:195], v22 src0_sel:WORD_1
	v_pk_fma_f32 v[188:189], v[184:185], v[152:153], v[188:189]
	v_pk_fma_f32 v[222:223], v[192:193], v[152:153], v[222:223]
	v_pk_fma_f32 v[190:191], v[186:187], v[154:155], v[190:191]
	v_pk_fma_f32 v[176:177], v[194:195], v[154:155], v[176:177]
	v_cvt_pk_f32_fp8_e32 v[184:185], v27
	v_cvt_pk_f32_fp8_e32 v[192:193], v23
	v_cvt_pk_f32_fp8_sdwa v[186:187], v27 src0_sel:WORD_1
	v_cvt_pk_f32_fp8_sdwa v[194:195], v23 src0_sel:WORD_1
	v_pk_fma_f32 v[188:189], v[184:185], v[156:157], v[188:189]
	v_pk_fma_f32 v[222:223], v[192:193], v[156:157], v[222:223]
	v_pk_fma_f32 v[190:191], v[186:187], v[158:159], v[190:191]
	v_pk_fma_f32 v[176:177], v[194:195], v[158:159], v[176:177]
	v_pk_add_f32 v[188:189], v[188:189], v[190:191]
	v_pk_add_f32 v[222:223], v[222:223], v[176:177]
	v_add_f32_e32 v172, v188, v189
	v_add_f32_e32 v174, v222, v223
.Lp6a1_dotdone:
	s_nop 4
	buffer_load_dwordx4 v[72:75], v181, s[8:11], s44 offen
	buffer_load_dwordx4 v[52:55], v181, s[8:11], s45 offen
	buffer_load_dwordx4 v[44:47], v181, s[8:11], s46 offen
	buffer_load_dwordx4 v[40:43], v181, s[8:11], s47 offen
	buffer_load_dwordx4 v[36:39], v181, s[8:11], s48 offen
	buffer_load_dwordx4 v[28:31], v181, s[8:11], s49 offen
	buffer_load_dwordx4 v[24:27], v181, s[8:11], s50 offen
	buffer_load_dwordx4 v[20:23], v181, s[8:11], s51 offen
	v_permlane32_swap_b32_e32 v160, v168
	v_permlane32_swap_b32_e32 v162, v170
	v_permlane32_swap_b32_e32 v164, v172
	v_permlane32_swap_b32_e32 v166, v174
	v_add_f32_e32 v1, v160, v168
	v_add_f32_e32 v2, v162, v170
	v_add_f32_e32 v160, v164, v172
	v_add_f32_e32 v161, v166, v174
	s_nop 0
	v_permlane16_swap_b32_e32 v1, v160
	v_permlane16_swap_b32_e32 v2, v161
	v_add_f32_e32 v1, v1, v160
	v_add_f32_e32 v2, v2, v161
	v_cndmask_b32_e64 v160, v1, v2, s[4:5]
	v_cndmask_b32_e64 v1, v2, v1, s[4:5]
	s_bfe_u32 s14, s26, 0x4000a
	v_cmp_gt_u32_e32 vcc, s14, v180
	v_add_f32_dpp v1, v160, v1 row_ror:8 row_mask:0xf bank_mask:0xf bound_ctrl:1
	s_nop 1
	v_add_f32_dpp v1, v1, v1 row_half_mirror row_mask:0xf bank_mask:0xf bound_ctrl:1
	s_nop 1
	v_add_f32_dpp v2, v1, v1 quad_perm:[1,0,3,2] row_mask:0xf bank_mask:0xf bound_ctrl:1
	v_mov_b32_e32 v1, 0
	s_nop 0
	v_mov_b32_dpp v160, v2 quad_perm:[2,3,0,1] row_mask:0xf bank_mask:0xf bound_ctrl:1
	s_and_saveexec_b64 s[14:15], vcc
	s_cbranch_execz .Lp6a1_958
	s_and_b32 s26, s26, 0x3ff
	v_add_u32_e32 v1, s26, v180
	v_lshl_add_u32 v1, v1, 2, s85
	v_mov_b32_e32 v185, v1
	v_add_f32_e32 v2, v2, v160
	ds_read2st64_b32 v[160:161], v1 offset1:48
	s_mov_b32 s26, 0x3e6d3388
	s_waitcnt lgkmcnt(0)
	v_mul_f32_e32 v1, v2, v160
	v_fma_f32 v2, |v1|, s26, 1.0
	v_rcp_f32_e32 v2, v2
	v_mov_b32_e32 v160, 0xbf3a00e3
	v_cmp_gt_f32_e32 vcc, 0, v1
	v_fmamk_f32 v160, v2, 0x3f07dc22, v160
	v_fmaak_f32 v160, v2, v160, 0x3f35f0e3
	v_fmaak_f32 v160, v2, v160, 0xbe11a98e
	v_fmaak_f32 v160, v2, v160, 0x3e027906
	v_mul_f32_e32 v2, v2, v160
	v_mul_f32_e32 v160, v1, v1
	v_mul_f32_e32 v160, 0xbf38aa3b, v160
	v_exp_f32_e32 v160, v160
	s_nop 0
	v_mul_f32_e32 v2, v160, v2
	v_mul_f32_e32 v160, v1, v2
	v_fma_f32 v1, -v1, v2, v1
	v_cndmask_b32_e32 v1, v1, v160, vcc
	v_mul_f32_e32 v1, v161, v1
	ds_write_b32 v185, v1 offset:12288

.Lp6a2_956:
	s_bfe_u32 s36, s26, 0x4000a
	v_cvt_pk_f32_fp8_e32 v[184:185], v224
	v_cvt_pk_f32_fp8_e32 v[192:193], v228
	v_cvt_pk_f32_fp8_sdwa v[186:187], v224 src0_sel:WORD_1
	v_cvt_pk_f32_fp8_sdwa v[194:195], v228 src0_sel:WORD_1
	v_pk_mul_f32 v[188:189], v[184:185], v[144:145]
	v_pk_mul_f32 v[222:223], v[192:193], v[144:145]
	v_pk_mul_f32 v[190:191], v[186:187], v[146:147]
	v_pk_mul_f32 v[176:177], v[194:195], v[146:147]
	v_cvt_pk_f32_fp8_e32 v[184:185], v225
	v_cvt_pk_f32_fp8_e32 v[192:193], v229
	v_cvt_pk_f32_fp8_sdwa v[186:187], v225 src0_sel:WORD_1
	v_cvt_pk_f32_fp8_sdwa v[194:195], v229 src0_sel:WORD_1
	v_pk_fma_f32 v[188:189], v[184:185], v[148:149], v[188:189]
	v_pk_fma_f32 v[222:223], v[192:193], v[148:149], v[222:223]
	v_pk_fma_f32 v[190:191], v[186:187], v[150:151], v[190:191]
	v_pk_fma_f32 v[176:177], v[194:195], v[150:151], v[176:177]
	v_cvt_pk_f32_fp8_e32 v[184:185], v226
	v_cvt_pk_f32_fp8_e32 v[192:193], v230
	v_cvt_pk_f32_fp8_sdwa v[186:187], v226 src0_sel:WORD_1
	v_cvt_pk_f32_fp8_sdwa v[194:195], v230 src0_sel:WORD_1
	v_pk_fma_f32 v[188:189], v[184:185], v[152:153], v[188:189]
	v_pk_fma_f32 v[222:223], v[192:193], v[152:153], v[222:223]
	v_pk_fma_f32 v[190:191], v[186:187], v[154:155], v[190:191]
	v_pk_fma_f32 v[176:177], v[194:195], v[154:155], v[176:177]
	v_cvt_pk_f32_fp8_e32 v[184:185], v227
	v_cvt_pk_f32_fp8_e32 v[192:193], v231
	v_cvt_pk_f32_fp8_sdwa v[186:187], v227 src0_sel:WORD_1
	v_cvt_pk_f32_fp8_sdwa v[194:195], v231 src0_sel:WORD_1
	v_pk_fma_f32 v[188:189], v[184:185], v[156:157], v[188:189]
	v_pk_fma_f32 v[222:223], v[192:193], v[156:157], v[222:223]
	v_pk_fma_f32 v[190:191], v[186:187], v[158:159], v[190:191]
	v_pk_fma_f32 v[176:177], v[194:195], v[158:159], v[176:177]
	v_pk_add_f32 v[188:189], v[188:189], v[190:191]
	v_pk_add_f32 v[222:223], v[222:223], v[176:177]
	v_add_f32_e32 v160, v188, v189
	v_add_f32_e32 v162, v222, v223
	s_cmp_le_u32 s36, 2
	s_cbranch_scc1 .Lp6a2_dotdone
	v_cvt_pk_f32_fp8_e32 v[184:185], v232
	v_cvt_pk_f32_fp8_e32 v[192:193], v236
	v_cvt_pk_f32_fp8_sdwa v[186:187], v232 src0_sel:WORD_1
	v_cvt_pk_f32_fp8_sdwa v[194:195], v236 src0_sel:WORD_1
	v_pk_mul_f32 v[188:189], v[184:185], v[144:145]
	v_pk_mul_f32 v[222:223], v[192:193], v[144:145]
	v_pk_mul_f32 v[190:191], v[186:187], v[146:147]
	v_pk_mul_f32 v[176:177], v[194:195], v[146:147]
	v_cvt_pk_f32_fp8_e32 v[184:185], v233
	v_cvt_pk_f32_fp8_e32 v[192:193], v237
	v_cvt_pk_f32_fp8_sdwa v[186:187], v233 src0_sel:WORD_1
	v_cvt_pk_f32_fp8_sdwa v[194:195], v237 src0_sel:WORD_1
	v_pk_fma_f32 v[188:189], v[184:185], v[148:149], v[188:189]
	v_pk_fma_f32 v[222:223], v[192:193], v[148:149], v[222:223]
	v_pk_fma_f32 v[190:191], v[186:187], v[150:151], v[190:191]
	v_pk_fma_f32 v[176:177], v[194:195], v[150:151], v[176:177]
	v_cvt_pk_f32_fp8_e32 v[184:185], v234
	v_cvt_pk_f32_fp8_e32 v[192:193], v238
	v_cvt_pk_f32_fp8_sdwa v[186:187], v234 src0_sel:WORD_1
	v_cvt_pk_f32_fp8_sdwa v[194:195], v238 src0_sel:WORD_1
	v_pk_fma_f32 v[188:189], v[184:185], v[152:153], v[188:189]
	v_pk_fma_f32 v[222:223], v[192:193], v[152:153], v[222:223]
	v_pk_fma_f32 v[190:191], v[186:187], v[154:155], v[190:191]
	v_pk_fma_f32 v[176:177], v[194:195], v[154:155], v[176:177]
	v_cvt_pk_f32_fp8_e32 v[184:185], v235
	v_cvt_pk_f32_fp8_e32 v[192:193], v239
	v_cvt_pk_f32_fp8_sdwa v[186:187], v235 src0_sel:WORD_1
	v_cvt_pk_f32_fp8_sdwa v[194:195], v239 src0_sel:WORD_1
	v_pk_fma_f32 v[188:189], v[184:185], v[156:157], v[188:189]
	v_pk_fma_f32 v[222:223], v[192:193], v[156:157], v[222:223]
	v_pk_fma_f32 v[190:191], v[186:187], v[158:159], v[190:191]
	v_pk_fma_f32 v[176:177], v[194:195], v[158:159], v[176:177]
	v_pk_add_f32 v[188:189], v[188:189], v[190:191]
	v_pk_add_f32 v[222:223], v[222:223], v[176:177]
	v_add_f32_e32 v164, v188, v189
	v_add_f32_e32 v166, v222, v223
	s_cmp_le_u32 s36, 4
	s_cbranch_scc1 .Lp6a2_dotdone
	v_cvt_pk_f32_fp8_e32 v[184:185], v240
	v_cvt_pk_f32_fp8_e32 v[192:193], v244
	v_cvt_pk_f32_fp8_sdwa v[186:187], v240 src0_sel:WORD_1
	v_cvt_pk_f32_fp8_sdwa v[194:195], v244 src0_sel:WORD_1
	v_pk_mul_f32 v[188:189], v[184:185], v[144:145]
	v_pk_mul_f32 v[222:223], v[192:193], v[144:145]
	v_pk_mul_f32 v[190:191], v[186:187], v[146:147]
	v_pk_mul_f32 v[176:177], v[194:195], v[146:147]
	v_cvt_pk_f32_fp8_e32 v[184:185], v241
	v_cvt_pk_f32_fp8_e32 v[192:193], v245
	v_cvt_pk_f32_fp8_sdwa v[186:187], v241 src0_sel:WORD_1
	v_cvt_pk_f32_fp8_sdwa v[194:195], v245 src0_sel:WORD_1
	v_pk_fma_f32 v[188:189], v[184:185], v[148:149], v[188:189]
	v_pk_fma_f32 v[222:223], v[192:193], v[148:149], v[222:223]
	v_pk_fma_f32 v[190:191], v[186:187], v[150:151], v[190:191]
	v_pk_fma_f32 v[176:177], v[194:195], v[150:151], v[176:177]
	v_cvt_pk_f32_fp8_e32 v[184:185], v242
	v_cvt_pk_f32_fp8_e32 v[192:193], v246
	v_cvt_pk_f32_fp8_sdwa v[186:187], v242 src0_sel:WORD_1
	v_cvt_pk_f32_fp8_sdwa v[194:195], v246 src0_sel:WORD_1
	v_pk_fma_f32 v[188:189], v[184:185], v[152:153], v[188:189]
	v_pk_fma_f32 v[222:223], v[192:193], v[152:153], v[222:223]
	v_pk_fma_f32 v[190:191], v[186:187], v[154:155], v[190:191]
	v_pk_fma_f32 v[176:177], v[194:195], v[154:155], v[176:177]
	v_cvt_pk_f32_fp8_e32 v[184:185], v243
	v_cvt_pk_f32_fp8_e32 v[192:193], v247
	v_cvt_pk_f32_fp8_sdwa v[186:187], v243 src0_sel:WORD_1
	v_cvt_pk_f32_fp8_sdwa v[194:195], v247 src0_sel:WORD_1
	v_pk_fma_f32 v[188:189], v[184:185], v[156:157], v[188:189]
	v_pk_fma_f32 v[222:223], v[192:193], v[156:157], v[222:223]
	v_pk_fma_f32 v[190:191], v[186:187], v[158:159], v[190:191]
	v_pk_fma_f32 v[176:177], v[194:195], v[158:159], v[176:177]
	v_pk_add_f32 v[188:189], v[188:189], v[190:191]
	v_pk_add_f32 v[222:223], v[222:223], v[176:177]
	v_add_f32_e32 v168, v188, v189
	v_add_f32_e32 v170, v222, v223
	s_cmp_le_u32 s36, 6
	s_cbranch_scc1 .Lp6a2_dotdone
	v_cvt_pk_f32_fp8_e32 v[184:185], v248
	v_cvt_pk_f32_fp8_e32 v[192:193], v216
	v_cvt_pk_f32_fp8_sdwa v[186:187], v248 src0_sel:WORD_1
	v_cvt_pk_f32_fp8_sdwa v[194:195], v216 src0_sel:WORD_1
	v_pk_mul_f32 v[188:189], v[184:185], v[144:145]
	v_pk_mul_f32 v[222:223], v[192:193], v[144:145]
	v_pk_mul_f32 v[190:191], v[186:187], v[146:147]
	v_pk_mul_f32 v[176:177], v[194:195], v[146:147]
	v_cvt_pk_f32_fp8_e32 v[184:185], v249
	v_cvt_pk_f32_fp8_e32 v[192:193], v217
	v_cvt_pk_f32_fp8_sdwa v[186:187], v249 src0_sel:WORD_1
	v_cvt_pk_f32_fp8_sdwa v[194:195], v217 src0_sel:WORD_1
	v_pk_fma_f32 v[188:189], v[184:185], v[148:149], v[188:189]
	v_pk_fma_f32 v[222:223], v[192:193], v[148:149], v[222:223]
	v_pk_fma_f32 v[190:191], v[186:187], v[150:151], v[190:191]
	v_pk_fma_f32 v[176:177], v[194:195], v[150:151], v[176:177]
	v_cvt_pk_f32_fp8_e32 v[184:185], v250
	v_cvt_pk_f32_fp8_e32 v[192:193], v218
	v_cvt_pk_f32_fp8_sdwa v[186:187], v250 src0_sel:WORD_1
	v_cvt_pk_f32_fp8_sdwa v[194:195], v218 src0_sel:WORD_1
	v_pk_fma_f32 v[188:189], v[184:185], v[152:153], v[188:189]
	v_pk_fma_f32 v[222:223], v[192:193], v[152:153], v[222:223]
	v_pk_fma_f32 v[190:191], v[186:187], v[154:155], v[190:191]
	v_pk_fma_f32 v[176:177], v[194:195], v[154:155], v[176:177]
	v_cvt_pk_f32_fp8_e32 v[184:185], v251
	v_cvt_pk_f32_fp8_e32 v[192:193], v219
	v_cvt_pk_f32_fp8_sdwa v[186:187], v251 src0_sel:WORD_1
	v_cvt_pk_f32_fp8_sdwa v[194:195], v219 src0_sel:WORD_1
	v_pk_fma_f32 v[188:189], v[184:185], v[156:157], v[188:189]
	v_pk_fma_f32 v[222:223], v[192:193], v[156:157], v[222:223]
	v_pk_fma_f32 v[190:191], v[186:187], v[158:159], v[190:191]
	v_pk_fma_f32 v[176:177], v[194:195], v[158:159], v[176:177]
	v_pk_add_f32 v[188:189], v[188:189], v[190:191]
	v_pk_add_f32 v[222:223], v[222:223], v[176:177]
	v_add_f32_e32 v172, v188, v189
	v_add_f32_e32 v174, v222, v223
.Lp6a2_dotdone:
	s_nop 4
	buffer_load_dwordx4 v[224:227], v181, s[8:11], s44 offen
	buffer_load_dwordx4 v[228:231], v181, s[8:11], s45 offen
	buffer_load_dwordx4 v[232:235], v181, s[8:11], s46 offen
	buffer_load_dwordx4 v[236:239], v181, s[8:11], s47 offen
	buffer_load_dwordx4 v[240:243], v181, s[8:11], s48 offen
	buffer_load_dwordx4 v[244:247], v181, s[8:11], s49 offen
	buffer_load_dwordx4 v[248:251], v181, s[8:11], s50 offen
	buffer_load_dwordx4 v[216:219], v181, s[8:11], s51 offen
	v_permlane32_swap_b32_e32 v160, v168
	v_permlane32_swap_b32_e32 v162, v170
	v_permlane32_swap_b32_e32 v164, v172
	v_permlane32_swap_b32_e32 v166, v174
	v_add_f32_e32 v1, v160, v168
	v_add_f32_e32 v2, v162, v170
	v_add_f32_e32 v160, v164, v172
	v_add_f32_e32 v161, v166, v174
	s_nop 0
	v_permlane16_swap_b32_e32 v1, v160
	v_permlane16_swap_b32_e32 v2, v161
	v_add_f32_e32 v1, v1, v160
	v_add_f32_e32 v2, v2, v161
	v_cndmask_b32_e64 v160, v1, v2, s[4:5]
	v_cndmask_b32_e64 v1, v2, v1, s[4:5]
	s_bfe_u32 s14, s26, 0x4000a
	v_cmp_gt_u32_e32 vcc, s14, v180
	v_add_f32_dpp v1, v160, v1 row_ror:8 row_mask:0xf bank_mask:0xf bound_ctrl:1
	s_nop 1
	v_add_f32_dpp v1, v1, v1 row_half_mirror row_mask:0xf bank_mask:0xf bound_ctrl:1
	s_nop 1
	v_add_f32_dpp v2, v1, v1 quad_perm:[1,0,3,2] row_mask:0xf bank_mask:0xf bound_ctrl:1
	v_mov_b32_e32 v1, 0
	s_nop 0
	v_mov_b32_dpp v160, v2 quad_perm:[2,3,0,1] row_mask:0xf bank_mask:0xf bound_ctrl:1
	s_and_saveexec_b64 s[14:15], vcc
	s_cbranch_execz .Lp6a2_958
	s_and_b32 s26, s26, 0x3ff
	v_add_u32_e32 v1, s26, v180
	v_lshl_add_u32 v1, v1, 2, s85
	v_mov_b32_e32 v185, v1
	v_add_f32_e32 v2, v2, v160
	ds_read2st64_b32 v[160:161], v1 offset1:48
	s_mov_b32 s26, 0x3e6d3388
	s_waitcnt lgkmcnt(0)
	v_mul_f32_e32 v1, v2, v160
	v_fma_f32 v2, |v1|, s26, 1.0
	v_rcp_f32_e32 v2, v2
	v_mov_b32_e32 v160, 0xbf3a00e3
	v_cmp_gt_f32_e32 vcc, 0, v1
	v_fmamk_f32 v160, v2, 0x3f07dc22, v160
	v_fmaak_f32 v160, v2, v160, 0x3f35f0e3
	v_fmaak_f32 v160, v2, v160, 0xbe11a98e
	v_fmaak_f32 v160, v2, v160, 0x3e027906
	v_mul_f32_e32 v2, v2, v160
	v_mul_f32_e32 v160, v1, v1
	v_mul_f32_e32 v160, 0xbf38aa3b, v160
	v_exp_f32_e32 v160, v160
	s_nop 0
	v_mul_f32_e32 v2, v160, v2
	v_mul_f32_e32 v160, v1, v2
	v_fma_f32 v1, -v1, v2, v1
	v_cndmask_b32_e32 v1, v1, v160, vcc
	v_mul_f32_e32 v1, v161, v1
	ds_write_b32 v185, v1 offset:12288
.Lp6a2_958:
	s_or_b64 exec, exec, s[14:15]
	s_mov_b32 s26, s86
	s_mov_b32 s86, s27
	s_mov_b32 s27, s32
	s_cmp_eq_u32 s22, s23
	s_cbranch_scc1 .Lp6_Adone
	s_branch .Lp6a0_top
.Lp6_Adone:
	s_waitcnt vmcnt(0)
	s_add_i32 s3, s22, -1
	s_min_i32 s2, s3, 0
	s_max_i32 s2, s2, 0
	s_lshl_b32 s2, s2, 2
	s_add_i32 s2, s85, s2
	v_mov_b32_e32 v1, s2
	ds_read_b32 v1, v1 offset:4864
	s_waitcnt lgkmcnt(0)
	v_readfirstlane_b32 s26, v1
	s_and_b32 s2, s26, 0x3ff
	s_bfe_u32 s3, s26, 0x4000a
	v_cmp_gt_u32_e32 vcc, s3, v182
	s_lshl_b32 s2, s2, 2
	s_add_i32 s2, s2, s85
	v_cndmask_b32_e32 v1, 0, v182, vcc
	v_lshl_add_u32 v1, v1, 2, s2
	ds_read_b32 v1, v1 offset:8192
	s_waitcnt lgkmcnt(0)
	v_lshlrev_b32_e32 v1, 10, v1
	v_and_b32_e32 v1, 0x3fffc00, v1
	s_nop 0
	v_readlane_b32 s44, v1, 0
	v_readlane_b32 s45, v1, 1
	v_readlane_b32 s46, v1, 2
	v_readlane_b32 s47, v1, 3
	v_readlane_b32 s48, v1, 4
	v_readlane_b32 s49, v1, 5
	v_readlane_b32 s50, v1, 6
	v_readlane_b32 s51, v1, 7
	s_nop 4
	buffer_load_dwordx4 v[68:71], v181, s[92:95], s44 offen
	buffer_load_dwordx4 v[64:67], v181, s[92:95], s45 offen
	buffer_load_dwordx4 v[60:63], v181, s[92:95], s46 offen
	buffer_load_dwordx4 v[56:59], v181, s[92:95], s47 offen
	buffer_load_dwordx4 v[48:51], v181, s[92:95], s48 offen
	buffer_load_dwordx4 v[32:35], v181, s[92:95], s49 offen
	buffer_load_dwordx4 v[16:19], v181, s[92:95], s50 offen
	buffer_load_dwordx4 v[12:15], v181, s[92:95], s51 offen
	s_add_i32 s3, s22, -1
	s_min_i32 s2, s3, 1
	s_max_i32 s2, s2, 0
	s_lshl_b32 s2, s2, 2
	s_add_i32 s2, s85, s2
	v_mov_b32_e32 v1, s2
	ds_read_b32 v1, v1 offset:4864
	s_waitcnt lgkmcnt(0)
	v_readfirstlane_b32 s86, v1
	s_and_b32 s2, s86, 0x3ff
	s_bfe_u32 s3, s86, 0x4000a
	v_cmp_gt_u32_e32 vcc, s3, v182
	s_lshl_b32 s2, s2, 2
	s_add_i32 s2, s2, s85
	v_cndmask_b32_e32 v1, 0, v182, vcc
	v_lshl_add_u32 v1, v1, 2, s2
	ds_read_b32 v1, v1 offset:8192
	s_waitcnt lgkmcnt(0)
	v_lshlrev_b32_e32 v1, 10, v1
	v_and_b32_e32 v1, 0x3fffc00, v1
	s_nop 0
	v_readlane_b32 s44, v1, 0
	v_readlane_b32 s45, v1, 1
	v_readlane_b32 s46, v1, 2
	v_readlane_b32 s47, v1, 3
	v_readlane_b32 s48, v1, 4
	v_readlane_b32 s49, v1, 5
	v_readlane_b32 s50, v1, 6
	v_readlane_b32 s51, v1, 7
	s_nop 4
	buffer_load_dwordx4 v[72:75], v181, s[92:95], s44 offen
	buffer_load_dwordx4 v[52:55], v181, s[92:95], s45 offen
	buffer_load_dwordx4 v[44:47], v181, s[92:95], s46 offen
	buffer_load_dwordx4 v[40:43], v181, s[92:95], s47 offen
	buffer_load_dwordx4 v[36:39], v181, s[92:95], s48 offen
	buffer_load_dwordx4 v[28:31], v181, s[92:95], s49 offen
	buffer_load_dwordx4 v[24:27], v181, s[92:95], s50 offen
	buffer_load_dwordx4 v[20:23], v181, s[92:95], s51 offen
	s_add_i32 s3, s22, -1
	s_min_i32 s2, s3, 2
	s_max_i32 s2, s2, 0
	s_lshl_b32 s2, s2, 2
	s_add_i32 s2, s85, s2
	v_mov_b32_e32 v1, s2
	ds_read_b32 v1, v1 offset:4864
	s_waitcnt lgkmcnt(0)
	v_readfirstlane_b32 s27, v1
	s_and_b32 s2, s27, 0x3ff
	s_bfe_u32 s3, s27, 0x4000a
	v_cmp_gt_u32_e32 vcc, s3, v182
	s_lshl_b32 s2, s2, 2
	s_add_i32 s2, s2, s85
	v_cndmask_b32_e32 v1, 0, v182, vcc
	v_lshl_add_u32 v1, v1, 2, s2
	ds_read_b32 v1, v1 offset:8192
	s_waitcnt lgkmcnt(0)
	v_lshlrev_b32_e32 v1, 10, v1
	v_and_b32_e32 v1, 0x3fffc00, v1
	s_nop 0
	v_readlane_b32 s44, v1, 0
	v_readlane_b32 s45, v1, 1
	v_readlane_b32 s46, v1, 2
	v_readlane_b32 s47, v1, 3
	v_readlane_b32 s48, v1, 4
	v_readlane_b32 s49, v1, 5
	v_readlane_b32 s50, v1, 6
	v_readlane_b32 s51, v1, 7
	s_nop 4
	buffer_load_dwordx4 v[224:227], v181, s[92:95], s44 offen
	buffer_load_dwordx4 v[228:231], v181, s[92:95], s45 offen
	buffer_load_dwordx4 v[232:235], v181, s[92:95], s46 offen
	buffer_load_dwordx4 v[236:239], v181, s[92:95], s47 offen
	buffer_load_dwordx4 v[240:243], v181, s[92:95], s48 offen
	buffer_load_dwordx4 v[244:247], v181, s[92:95], s49 offen
	buffer_load_dwordx4 v[248:251], v181, s[92:95], s50 offen
	buffer_load_dwordx4 v[216:219], v181, s[92:95], s51 offen
	s_mov_b32 s23, 0
.Lp6b0_top:
	s_add_i32 s23, s23, 1
	s_add_i32 s2, s23, 2
	s_add_i32 s3, s22, -1
	s_min_i32 s2, s2, s3
	s_lshl_b32 s2, s2, 2
	s_add_i32 s2, s85, s2
	v_mov_b32_e32 v1, s2
	ds_read_b32 v1, v1 offset:4864
	s_waitcnt lgkmcnt(0)
	v_readfirstlane_b32 s32, v1
	s_and_b32 s2, s32, 0x3ff
	s_bfe_u32 s3, s32, 0x4000a
	v_cmp_gt_u32_e32 vcc, s3, v182
	s_lshl_b32 s2, s2, 2
	s_add_i32 s2, s2, s85
	v_cndmask_b32_e32 v1, 0, v182, vcc
	v_lshl_add_u32 v1, v1, 2, s2
	ds_read_b32 v1, v1 offset:8192
	s_waitcnt lgkmcnt(0)
	v_lshlrev_b32_e32 v1, 10, v1
	v_and_b32_e32 v1, 0x3fffc00, v1
	s_nop 0
	v_readlane_b32 s44, v1, 0
	v_readlane_b32 s45, v1, 1
	v_readlane_b32 s46, v1, 2
	v_readlane_b32 s47, v1, 3
	v_readlane_b32 s48, v1, 4
	v_readlane_b32 s49, v1, 5
	v_readlane_b32 s50, v1, 6
	v_readlane_b32 s51, v1, 7
	s_bfe_u32 s14, s26, 0x4000a
	v_cmp_gt_u32_e32 vcc, s14, v180
	v_mov_b32_e32 v1, 0
	s_and_b32 s2, s26, 0x3ff
	s_lshr_b32 s66, s26, 14
	s_and_saveexec_b64 s[14:15], vcc
	v_add_u32_e32 v2, s2, v180
	v_lshl_add_u32 v2, v2, 2, s85
	ds_read_b32 v1, v2 offset:12288
	s_or_b64 exec, exec, s[14:15]
	s_waitcnt vmcnt(16)
	s_waitcnt lgkmcnt(0)
	s_bfe_u32 s36, s26, 0x4000a
	s_cmp_lt_i32 s66, 1
	s_cbranch_scc1 .Lp6b0_t0
	s_cmp_lt_i32 s66, 2
	s_cbranch_scc1 .Lp6b0_t1
	s_cmp_lg_u32 s66, 2
	s_cbranch_scc0 .Lp6b0_t2
	v_readlane_b32 s14, v1, 0
	v_cvt_pk_f32_fp8_e32 v[184:185], v68
	v_cvt_pk_f32_fp8_sdwa v[186:187], v68 src0_sel:WORD_1
	v_pk_fma_f32 v[78:79], v[184:185], s[14:15], v[78:79] op_sel_hi:[1,0,1]
	v_pk_fma_f32 v[80:81], v[186:187], s[14:15], v[80:81] op_sel_hi:[1,0,1]
	v_cvt_pk_f32_fp8_e32 v[188:189], v69
	v_cvt_pk_f32_fp8_sdwa v[190:191], v69 src0_sel:WORD_1
	v_pk_fma_f32 v[82:83], v[188:189], s[14:15], v[82:83] op_sel_hi:[1,0,1]
	v_pk_fma_f32 v[86:87], v[190:191], s[14:15], v[86:87] op_sel_hi:[1,0,1]
	v_cvt_pk_f32_fp8_e32 v[184:185], v70
	v_cvt_pk_f32_fp8_sdwa v[186:187], v70 src0_sel:WORD_1
	v_pk_fma_f32 v[88:89], v[184:185], s[14:15], v[88:89] op_sel_hi:[1,0,1]
	v_pk_fma_f32 v[90:91], v[186:187], s[14:15], v[90:91] op_sel_hi:[1,0,1]
	v_cvt_pk_f32_fp8_e32 v[188:189], v71
	v_cvt_pk_f32_fp8_sdwa v[190:191], v71 src0_sel:WORD_1
	v_pk_fma_f32 v[92:93], v[188:189], s[14:15], v[92:93] op_sel_hi:[1,0,1]
	v_pk_fma_f32 v[84:85], v[190:191], s[14:15], v[84:85] op_sel_hi:[1,0,1]
	v_readlane_b32 s14, v1, 8
	v_cvt_pk_f32_fp8_e32 v[184:185], v64
	v_cvt_pk_f32_fp8_sdwa v[186:187], v64 src0_sel:WORD_1
	v_pk_fma_f32 v[78:79], v[184:185], s[14:15], v[78:79] op_sel_hi:[1,0,1]
	v_pk_fma_f32 v[80:81], v[186:187], s[14:15], v[80:81] op_sel_hi:[1,0,1]
	v_cvt_pk_f32_fp8_e32 v[188:189], v65
	v_cvt_pk_f32_fp8_sdwa v[190:191], v65 src0_sel:WORD_1
	v_pk_fma_f32 v[82:83], v[188:189], s[14:15], v[82:83] op_sel_hi:[1,0,1]
	v_pk_fma_f32 v[86:87], v[190:191], s[14:15], v[86:87] op_sel_hi:[1,0,1]
	v_cvt_pk_f32_fp8_e32 v[184:185], v66
	v_cvt_pk_f32_fp8_sdwa v[186:187], v66 src0_sel:WORD_1
	v_pk_fma_f32 v[88:89], v[184:185], s[14:15], v[88:89] op_sel_hi:[1,0,1]
	v_pk_fma_f32 v[90:91], v[186:187], s[14:15], v[90:91] op_sel_hi:[1,0,1]
	v_cvt_pk_f32_fp8_e32 v[188:189], v67
	v_cvt_pk_f32_fp8_sdwa v[190:191], v67 src0_sel:WORD_1
	v_pk_fma_f32 v[92:93], v[188:189], s[14:15], v[92:93] op_sel_hi:[1,0,1]
	v_pk_fma_f32 v[84:85], v[190:191], s[14:15], v[84:85] op_sel_hi:[1,0,1]
	s_cmp_le_u32 s36, 2
	s_cbranch_scc1 .Lp6b0_axdone
	v_readlane_b32 s14, v1, 16
	v_cvt_pk_f32_fp8_e32 v[184:185], v60
	v_cvt_pk_f32_fp8_sdwa v[186:187], v60 src0_sel:WORD_1
	v_pk_fma_f32 v[78:79], v[184:185], s[14:15], v[78:79] op_sel_hi:[1,0,1]
	v_pk_fma_f32 v[80:81], v[186:187], s[14:15], v[80:81] op_sel_hi:[1,0,1]
	v_cvt_pk_f32_fp8_e32 v[188:189], v61
	v_cvt_pk_f32_fp8_sdwa v[190:191], v61 src0_sel:WORD_1
	v_pk_fma_f32 v[82:83], v[188:189], s[14:15], v[82:83] op_sel_hi:[1,0,1]
	v_pk_fma_f32 v[86:87], v[190:191], s[14:15], v[86:87] op_sel_hi:[1,0,1]
	v_cvt_pk_f32_fp8_e32 v[184:185], v62
	v_cvt_pk_f32_fp8_sdwa v[186:187], v62 src0_sel:WORD_1
	v_pk_fma_f32 v[88:89], v[184:185], s[14:15], v[88:89] op_sel_hi:[1,0,1]
	v_pk_fma_f32 v[90:91], v[186:187], s[14:15], v[90:91] op_sel_hi:[1,0,1]
	v_cvt_pk_f32_fp8_e32 v[188:189], v63
	v_cvt_pk_f32_fp8_sdwa v[190:191], v63 src0_sel:WORD_1
	v_pk_fma_f32 v[92:93], v[188:189], s[14:15], v[92:93] op_sel_hi:[1,0,1]
	v_pk_fma_f32 v[84:85], v[190:191], s[14:15], v[84:85] op_sel_hi:[1,0,1]
	v_readlane_b32 s14, v1, 24
	v_cvt_pk_f32_fp8_e32 v[184:185], v56
	v_cvt_pk_f32_fp8_sdwa v[186:187], v56 src0_sel:WORD_1
	v_pk_fma_f32 v[78:79], v[184:185], s[14:15], v[78:79] op_sel_hi:[1,0,1]
	v_pk_fma_f32 v[80:81], v[186:187], s[14:15], v[80:81] op_sel_hi:[1,0,1]
	v_cvt_pk_f32_fp8_e32 v[188:189], v57
	v_cvt_pk_f32_fp8_sdwa v[190:191], v57 src0_sel:WORD_1
	v_pk_fma_f32 v[82:83], v[188:189], s[14:15], v[82:83] op_sel_hi:[1,0,1]
	v_pk_fma_f32 v[86:87], v[190:191], s[14:15], v[86:87] op_sel_hi:[1,0,1]
	v_cvt_pk_f32_fp8_e32 v[184:185], v58
	v_cvt_pk_f32_fp8_sdwa v[186:187], v58 src0_sel:WORD_1
	v_pk_fma_f32 v[88:89], v[184:185], s[14:15], v[88:89] op_sel_hi:[1,0,1]
	v_pk_fma_f32 v[90:91], v[186:187], s[14:15], v[90:91] op_sel_hi:[1,0,1]
	v_cvt_pk_f32_fp8_e32 v[188:189], v59
	v_cvt_pk_f32_fp8_sdwa v[190:191], v59 src0_sel:WORD_1
	v_pk_fma_f32 v[92:93], v[188:189], s[14:15], v[92:93] op_sel_hi:[1,0,1]
	v_pk_fma_f32 v[84:85], v[190:191], s[14:15], v[84:85] op_sel_hi:[1,0,1]
	s_cmp_le_u32 s36, 4
	s_cbranch_scc1 .Lp6b0_axdone
	v_readlane_b32 s14, v1, 32
	v_cvt_pk_f32_fp8_e32 v[184:185], v48
	v_cvt_pk_f32_fp8_sdwa v[186:187], v48 src0_sel:WORD_1
	v_pk_fma_f32 v[78:79], v[184:185], s[14:15], v[78:79] op_sel_hi:[1,0,1]
	v_pk_fma_f32 v[80:81], v[186:187], s[14:15], v[80:81] op_sel_hi:[1,0,1]
	v_cvt_pk_f32_fp8_e32 v[188:189], v49
	v_cvt_pk_f32_fp8_sdwa v[190:191], v49 src0_sel:WORD_1
	v_pk_fma_f32 v[82:83], v[188:189], s[14:15], v[82:83] op_sel_hi:[1,0,1]
	v_pk_fma_f32 v[86:87], v[190:191], s[14:15], v[86:87] op_sel_hi:[1,0,1]
	v_cvt_pk_f32_fp8_e32 v[184:185], v50
	v_cvt_pk_f32_fp8_sdwa v[186:187], v50 src0_sel:WORD_1
	v_pk_fma_f32 v[88:89], v[184:185], s[14:15], v[88:89] op_sel_hi:[1,0,1]
	v_pk_fma_f32 v[90:91], v[186:187], s[14:15], v[90:91] op_sel_hi:[1,0,1]
	v_cvt_pk_f32_fp8_e32 v[188:189], v51
	v_cvt_pk_f32_fp8_sdwa v[190:191], v51 src0_sel:WORD_1
	v_pk_fma_f32 v[92:93], v[188:189], s[14:15], v[92:93] op_sel_hi:[1,0,1]
	v_pk_fma_f32 v[84:85], v[190:191], s[14:15], v[84:85] op_sel_hi:[1,0,1]
	v_readlane_b32 s14, v1, 40
	v_cvt_pk_f32_fp8_e32 v[184:185], v32
	v_cvt_pk_f32_fp8_sdwa v[186:187], v32 src0_sel:WORD_1
	v_pk_fma_f32 v[78:79], v[184:185], s[14:15], v[78:79] op_sel_hi:[1,0,1]
	v_pk_fma_f32 v[80:81], v[186:187], s[14:15], v[80:81] op_sel_hi:[1,0,1]
	v_cvt_pk_f32_fp8_e32 v[188:189], v33
	v_cvt_pk_f32_fp8_sdwa v[190:191], v33 src0_sel:WORD_1
	v_pk_fma_f32 v[82:83], v[188:189], s[14:15], v[82:83] op_sel_hi:[1,0,1]
	v_pk_fma_f32 v[86:87], v[190:191], s[14:15], v[86:87] op_sel_hi:[1,0,1]
	v_cvt_pk_f32_fp8_e32 v[184:185], v34
	v_cvt_pk_f32_fp8_sdwa v[186:187], v34 src0_sel:WORD_1
	v_pk_fma_f32 v[88:89], v[184:185], s[14:15], v[88:89] op_sel_hi:[1,0,1]
	v_pk_fma_f32 v[90:91], v[186:187], s[14:15], v[90:91] op_sel_hi:[1,0,1]
	v_cvt_pk_f32_fp8_e32 v[188:189], v35
	v_cvt_pk_f32_fp8_sdwa v[190:191], v35 src0_sel:WORD_1
	v_pk_fma_f32 v[92:93], v[188:189], s[14:15], v[92:93] op_sel_hi:[1,0,1]
	v_pk_fma_f32 v[84:85], v[190:191], s[14:15], v[84:85] op_sel_hi:[1,0,1]
	s_cmp_le_u32 s36, 6
	s_cbranch_scc1 .Lp6b0_axdone
	v_readlane_b32 s14, v1, 48
	v_cvt_pk_f32_fp8_e32 v[184:185], v16
	v_cvt_pk_f32_fp8_sdwa v[186:187], v16 src0_sel:WORD_1
	v_pk_fma_f32 v[78:79], v[184:185], s[14:15], v[78:79] op_sel_hi:[1,0,1]
	v_pk_fma_f32 v[80:81], v[186:187], s[14:15], v[80:81] op_sel_hi:[1,0,1]
	v_cvt_pk_f32_fp8_e32 v[188:189], v17
	v_cvt_pk_f32_fp8_sdwa v[190:191], v17 src0_sel:WORD_1
	v_pk_fma_f32 v[82:83], v[188:189], s[14:15], v[82:83] op_sel_hi:[1,0,1]
	v_pk_fma_f32 v[86:87], v[190:191], s[14:15], v[86:87] op_sel_hi:[1,0,1]
	v_cvt_pk_f32_fp8_e32 v[184:185], v18
	v_cvt_pk_f32_fp8_sdwa v[186:187], v18 src0_sel:WORD_1
	v_pk_fma_f32 v[88:89], v[184:185], s[14:15], v[88:89] op_sel_hi:[1,0,1]
	v_pk_fma_f32 v[90:91], v[186:187], s[14:15], v[90:91] op_sel_hi:[1,0,1]
	v_cvt_pk_f32_fp8_e32 v[188:189], v19
	v_cvt_pk_f32_fp8_sdwa v[190:191], v19 src0_sel:WORD_1
	v_pk_fma_f32 v[92:93], v[188:189], s[14:15], v[92:93] op_sel_hi:[1,0,1]
	v_pk_fma_f32 v[84:85], v[190:191], s[14:15], v[84:85] op_sel_hi:[1,0,1]
	v_readlane_b32 s14, v1, 56
	v_cvt_pk_f32_fp8_e32 v[184:185], v12
	v_cvt_pk_f32_fp8_sdwa v[186:187], v12 src0_sel:WORD_1
	v_pk_fma_f32 v[78:79], v[184:185], s[14:15], v[78:79] op_sel_hi:[1,0,1]
	v_pk_fma_f32 v[80:81], v[186:187], s[14:15], v[80:81] op_sel_hi:[1,0,1]
	v_cvt_pk_f32_fp8_e32 v[188:189], v13
	v_cvt_pk_f32_fp8_sdwa v[190:191], v13 src0_sel:WORD_1
	v_pk_fma_f32 v[82:83], v[188:189], s[14:15], v[82:83] op_sel_hi:[1,0,1]
	v_pk_fma_f32 v[86:87], v[190:191], s[14:15], v[86:87] op_sel_hi:[1,0,1]
	v_cvt_pk_f32_fp8_e32 v[184:185], v14
	v_cvt_pk_f32_fp8_sdwa v[186:187], v14 src0_sel:WORD_1
	v_pk_fma_f32 v[88:89], v[184:185], s[14:15], v[88:89] op_sel_hi:[1,0,1]
	v_pk_fma_f32 v[90:91], v[186:187], s[14:15], v[90:91] op_sel_hi:[1,0,1]
	v_cvt_pk_f32_fp8_e32 v[188:189], v15
	v_cvt_pk_f32_fp8_sdwa v[190:191], v15 src0_sel:WORD_1
	v_pk_fma_f32 v[92:93], v[188:189], s[14:15], v[92:93] op_sel_hi:[1,0,1]
	v_pk_fma_f32 v[84:85], v[190:191], s[14:15], v[84:85] op_sel_hi:[1,0,1]
	s_branch .Lp6b0_axdone
.Lp6b0_t2:
	v_readlane_b32 s14, v1, 0
	v_cvt_pk_f32_fp8_e32 v[184:185], v68
	v_cvt_pk_f32_fp8_sdwa v[186:187], v68 src0_sel:WORD_1
	v_pk_fma_f32 v[94:95], v[184:185], s[14:15], v[94:95] op_sel_hi:[1,0,1]
	v_pk_fma_f32 v[96:97], v[186:187], s[14:15], v[96:97] op_sel_hi:[1,0,1]
	v_cvt_pk_f32_fp8_e32 v[188:189], v69
	v_cvt_pk_f32_fp8_sdwa v[190:191], v69 src0_sel:WORD_1
	v_pk_fma_f32 v[98:99], v[188:189], s[14:15], v[98:99] op_sel_hi:[1,0,1]
	v_pk_fma_f32 v[100:101], v[190:191], s[14:15], v[100:101] op_sel_hi:[1,0,1]
	v_cvt_pk_f32_fp8_e32 v[184:185], v70
	v_cvt_pk_f32_fp8_sdwa v[186:187], v70 src0_sel:WORD_1
	v_pk_fma_f32 v[102:103], v[184:185], s[14:15], v[102:103] op_sel_hi:[1,0,1]
	v_pk_fma_f32 v[104:105], v[186:187], s[14:15], v[104:105] op_sel_hi:[1,0,1]
	v_cvt_pk_f32_fp8_e32 v[188:189], v71
	v_cvt_pk_f32_fp8_sdwa v[190:191], v71 src0_sel:WORD_1
	v_pk_fma_f32 v[106:107], v[188:189], s[14:15], v[106:107] op_sel_hi:[1,0,1]
	v_pk_fma_f32 v[108:109], v[190:191], s[14:15], v[108:109] op_sel_hi:[1,0,1]
	v_readlane_b32 s14, v1, 8
	v_cvt_pk_f32_fp8_e32 v[184:185], v64
	v_cvt_pk_f32_fp8_sdwa v[186:187], v64 src0_sel:WORD_1
	v_pk_fma_f32 v[94:95], v[184:185], s[14:15], v[94:95] op_sel_hi:[1,0,1]
	v_pk_fma_f32 v[96:97], v[186:187], s[14:15], v[96:97] op_sel_hi:[1,0,1]
	v_cvt_pk_f32_fp8_e32 v[188:189], v65
	v_cvt_pk_f32_fp8_sdwa v[190:191], v65 src0_sel:WORD_1
	v_pk_fma_f32 v[98:99], v[188:189], s[14:15], v[98:99] op_sel_hi:[1,0,1]
	v_pk_fma_f32 v[100:101], v[190:191], s[14:15], v[100:101] op_sel_hi:[1,0,1]
	v_cvt_pk_f32_fp8_e32 v[184:185], v66
	v_cvt_pk_f32_fp8_sdwa v[186:187], v66 src0_sel:WORD_1
	v_pk_fma_f32 v[102:103], v[184:185], s[14:15], v[102:103] op_sel_hi:[1,0,1]
	v_pk_fma_f32 v[104:105], v[186:187], s[14:15], v[104:105] op_sel_hi:[1,0,1]
	v_cvt_pk_f32_fp8_e32 v[188:189], v67
	v_cvt_pk_f32_fp8_sdwa v[190:191], v67 src0_sel:WORD_1
	v_pk_fma_f32 v[106:107], v[188:189], s[14:15], v[106:107] op_sel_hi:[1,0,1]
	v_pk_fma_f32 v[108:109], v[190:191], s[14:15], v[108:109] op_sel_hi:[1,0,1]
	s_cmp_le_u32 s36, 2
	s_cbranch_scc1 .Lp6b0_axdone
	v_readlane_b32 s14, v1, 16
	v_cvt_pk_f32_fp8_e32 v[184:185], v60
	v_cvt_pk_f32_fp8_sdwa v[186:187], v60 src0_sel:WORD_1
	v_pk_fma_f32 v[94:95], v[184:185], s[14:15], v[94:95] op_sel_hi:[1,0,1]
	v_pk_fma_f32 v[96:97], v[186:187], s[14:15], v[96:97] op_sel_hi:[1,0,1]
	v_cvt_pk_f32_fp8_e32 v[188:189], v61
	v_cvt_pk_f32_fp8_sdwa v[190:191], v61 src0_sel:WORD_1
	v_pk_fma_f32 v[98:99], v[188:189], s[14:15], v[98:99] op_sel_hi:[1,0,1]
	v_pk_fma_f32 v[100:101], v[190:191], s[14:15], v[100:101] op_sel_hi:[1,0,1]
	v_cvt_pk_f32_fp8_e32 v[184:185], v62
	v_cvt_pk_f32_fp8_sdwa v[186:187], v62 src0_sel:WORD_1
	v_pk_fma_f32 v[102:103], v[184:185], s[14:15], v[102:103] op_sel_hi:[1,0,1]
	v_pk_fma_f32 v[104:105], v[186:187], s[14:15], v[104:105] op_sel_hi:[1,0,1]
	v_cvt_pk_f32_fp8_e32 v[188:189], v63
	v_cvt_pk_f32_fp8_sdwa v[190:191], v63 src0_sel:WORD_1
	v_pk_fma_f32 v[106:107], v[188:189], s[14:15], v[106:107] op_sel_hi:[1,0,1]
	v_pk_fma_f32 v[108:109], v[190:191], s[14:15], v[108:109] op_sel_hi:[1,0,1]
	v_readlane_b32 s14, v1, 24
	v_cvt_pk_f32_fp8_e32 v[184:185], v56
	v_cvt_pk_f32_fp8_sdwa v[186:187], v56 src0_sel:WORD_1
	v_pk_fma_f32 v[94:95], v[184:185], s[14:15], v[94:95] op_sel_hi:[1,0,1]
	v_pk_fma_f32 v[96:97], v[186:187], s[14:15], v[96:97] op_sel_hi:[1,0,1]
	v_cvt_pk_f32_fp8_e32 v[188:189], v57
	v_cvt_pk_f32_fp8_sdwa v[190:191], v57 src0_sel:WORD_1
	v_pk_fma_f32 v[98:99], v[188:189], s[14:15], v[98:99] op_sel_hi:[1,0,1]
	v_pk_fma_f32 v[100:101], v[190:191], s[14:15], v[100:101] op_sel_hi:[1,0,1]
	v_cvt_pk_f32_fp8_e32 v[184:185], v58
	v_cvt_pk_f32_fp8_sdwa v[186:187], v58 src0_sel:WORD_1
	v_pk_fma_f32 v[102:103], v[184:185], s[14:15], v[102:103] op_sel_hi:[1,0,1]
	v_pk_fma_f32 v[104:105], v[186:187], s[14:15], v[104:105] op_sel_hi:[1,0,1]
	v_cvt_pk_f32_fp8_e32 v[188:189], v59
	v_cvt_pk_f32_fp8_sdwa v[190:191], v59 src0_sel:WORD_1
	v_pk_fma_f32 v[106:107], v[188:189], s[14:15], v[106:107] op_sel_hi:[1,0,1]
	v_pk_fma_f32 v[108:109], v[190:191], s[14:15], v[108:109] op_sel_hi:[1,0,1]
	s_cmp_le_u32 s36, 4
	s_cbranch_scc1 .Lp6b0_axdone
	v_readlane_b32 s14, v1, 32
	v_cvt_pk_f32_fp8_e32 v[184:185], v48
	v_cvt_pk_f32_fp8_sdwa v[186:187], v48 src0_sel:WORD_1
	v_pk_fma_f32 v[94:95], v[184:185], s[14:15], v[94:95] op_sel_hi:[1,0,1]
	v_pk_fma_f32 v[96:97], v[186:187], s[14:15], v[96:97] op_sel_hi:[1,0,1]
	v_cvt_pk_f32_fp8_e32 v[188:189], v49
	v_cvt_pk_f32_fp8_sdwa v[190:191], v49 src0_sel:WORD_1
	v_pk_fma_f32 v[98:99], v[188:189], s[14:15], v[98:99] op_sel_hi:[1,0,1]
	v_pk_fma_f32 v[100:101], v[190:191], s[14:15], v[100:101] op_sel_hi:[1,0,1]
	v_cvt_pk_f32_fp8_e32 v[184:185], v50
	v_cvt_pk_f32_fp8_sdwa v[186:187], v50 src0_sel:WORD_1
	v_pk_fma_f32 v[102:103], v[184:185], s[14:15], v[102:103] op_sel_hi:[1,0,1]
	v_pk_fma_f32 v[104:105], v[186:187], s[14:15], v[104:105] op_sel_hi:[1,0,1]
	v_cvt_pk_f32_fp8_e32 v[188:189], v51
	v_cvt_pk_f32_fp8_sdwa v[190:191], v51 src0_sel:WORD_1
	v_pk_fma_f32 v[106:107], v[188:189], s[14:15], v[106:107] op_sel_hi:[1,0,1]
	v_pk_fma_f32 v[108:109], v[190:191], s[14:15], v[108:109] op_sel_hi:[1,0,1]
	v_readlane_b32 s14, v1, 40
	v_cvt_pk_f32_fp8_e32 v[184:185], v32
	v_cvt_pk_f32_fp8_sdwa v[186:187], v32 src0_sel:WORD_1
	v_pk_fma_f32 v[94:95], v[184:185], s[14:15], v[94:95] op_sel_hi:[1,0,1]
	v_pk_fma_f32 v[96:97], v[186:187], s[14:15], v[96:97] op_sel_hi:[1,0,1]
	v_cvt_pk_f32_fp8_e32 v[188:189], v33
	v_cvt_pk_f32_fp8_sdwa v[190:191], v33 src0_sel:WORD_1
	v_pk_fma_f32 v[98:99], v[188:189], s[14:15], v[98:99] op_sel_hi:[1,0,1]
	v_pk_fma_f32 v[100:101], v[190:191], s[14:15], v[100:101] op_sel_hi:[1,0,1]
	v_cvt_pk_f32_fp8_e32 v[184:185], v34
	v_cvt_pk_f32_fp8_sdwa v[186:187], v34 src0_sel:WORD_1
	v_pk_fma_f32 v[102:103], v[184:185], s[14:15], v[102:103] op_sel_hi:[1,0,1]
	v_pk_fma_f32 v[104:105], v[186:187], s[14:15], v[104:105] op_sel_hi:[1,0,1]
	v_cvt_pk_f32_fp8_e32 v[188:189], v35
	v_cvt_pk_f32_fp8_sdwa v[190:191], v35 src0_sel:WORD_1
	v_pk_fma_f32 v[106:107], v[188:189], s[14:15], v[106:107] op_sel_hi:[1,0,1]
	v_pk_fma_f32 v[108:109], v[190:191], s[14:15], v[108:109] op_sel_hi:[1,0,1]
	s_cmp_le_u32 s36, 6
	s_cbranch_scc1 .Lp6b0_axdone
	v_readlane_b32 s14, v1, 48
	v_cvt_pk_f32_fp8_e32 v[184:185], v16
	v_cvt_pk_f32_fp8_sdwa v[186:187], v16 src0_sel:WORD_1
	v_pk_fma_f32 v[94:95], v[184:185], s[14:15], v[94:95] op_sel_hi:[1,0,1]
	v_pk_fma_f32 v[96:97], v[186:187], s[14:15], v[96:97] op_sel_hi:[1,0,1]
	v_cvt_pk_f32_fp8_e32 v[188:189], v17
	v_cvt_pk_f32_fp8_sdwa v[190:191], v17 src0_sel:WORD_1
	v_pk_fma_f32 v[98:99], v[188:189], s[14:15], v[98:99] op_sel_hi:[1,0,1]
	v_pk_fma_f32 v[100:101], v[190:191], s[14:15], v[100:101] op_sel_hi:[1,0,1]
	v_cvt_pk_f32_fp8_e32 v[184:185], v18
	v_cvt_pk_f32_fp8_sdwa v[186:187], v18 src0_sel:WORD_1
	v_pk_fma_f32 v[102:103], v[184:185], s[14:15], v[102:103] op_sel_hi:[1,0,1]
	v_pk_fma_f32 v[104:105], v[186:187], s[14:15], v[104:105] op_sel_hi:[1,0,1]
	v_cvt_pk_f32_fp8_e32 v[188:189], v19
	v_cvt_pk_f32_fp8_sdwa v[190:191], v19 src0_sel:WORD_1
	v_pk_fma_f32 v[106:107], v[188:189], s[14:15], v[106:107] op_sel_hi:[1,0,1]
	v_pk_fma_f32 v[108:109], v[190:191], s[14:15], v[108:109] op_sel_hi:[1,0,1]
	v_readlane_b32 s14, v1, 56
	v_cvt_pk_f32_fp8_e32 v[184:185], v12
	v_cvt_pk_f32_fp8_sdwa v[186:187], v12 src0_sel:WORD_1
	v_pk_fma_f32 v[94:95], v[184:185], s[14:15], v[94:95] op_sel_hi:[1,0,1]
	v_pk_fma_f32 v[96:97], v[186:187], s[14:15], v[96:97] op_sel_hi:[1,0,1]
	v_cvt_pk_f32_fp8_e32 v[188:189], v13
	v_cvt_pk_f32_fp8_sdwa v[190:191], v13 src0_sel:WORD_1
	v_pk_fma_f32 v[98:99], v[188:189], s[14:15], v[98:99] op_sel_hi:[1,0,1]
	v_pk_fma_f32 v[100:101], v[190:191], s[14:15], v[100:101] op_sel_hi:[1,0,1]
	v_cvt_pk_f32_fp8_e32 v[184:185], v14
	v_cvt_pk_f32_fp8_sdwa v[186:187], v14 src0_sel:WORD_1
	v_pk_fma_f32 v[102:103], v[184:185], s[14:15], v[102:103] op_sel_hi:[1,0,1]
	v_pk_fma_f32 v[104:105], v[186:187], s[14:15], v[104:105] op_sel_hi:[1,0,1]
	v_cvt_pk_f32_fp8_e32 v[188:189], v15
	v_cvt_pk_f32_fp8_sdwa v[190:191], v15 src0_sel:WORD_1
	v_pk_fma_f32 v[106:107], v[188:189], s[14:15], v[106:107] op_sel_hi:[1,0,1]
	v_pk_fma_f32 v[108:109], v[190:191], s[14:15], v[108:109] op_sel_hi:[1,0,1]
	s_branch .Lp6b0_axdone
.Lp6b0_t1:
	v_readlane_b32 s14, v1, 0
	v_cvt_pk_f32_fp8_e32 v[184:185], v68
	v_cvt_pk_f32_fp8_sdwa v[186:187], v68 src0_sel:WORD_1
	v_pk_fma_f32 v[110:111], v[184:185], s[14:15], v[110:111] op_sel_hi:[1,0,1]
	v_pk_fma_f32 v[112:113], v[186:187], s[14:15], v[112:113] op_sel_hi:[1,0,1]
	v_cvt_pk_f32_fp8_e32 v[188:189], v69
	v_cvt_pk_f32_fp8_sdwa v[190:191], v69 src0_sel:WORD_1
	v_pk_fma_f32 v[114:115], v[188:189], s[14:15], v[114:115] op_sel_hi:[1,0,1]
	v_pk_fma_f32 v[116:117], v[190:191], s[14:15], v[116:117] op_sel_hi:[1,0,1]
	v_cvt_pk_f32_fp8_e32 v[184:185], v70
	v_cvt_pk_f32_fp8_sdwa v[186:187], v70 src0_sel:WORD_1
	v_pk_fma_f32 v[118:119], v[184:185], s[14:15], v[118:119] op_sel_hi:[1,0,1]
	v_pk_fma_f32 v[120:121], v[186:187], s[14:15], v[120:121] op_sel_hi:[1,0,1]
	v_cvt_pk_f32_fp8_e32 v[188:189], v71
	v_cvt_pk_f32_fp8_sdwa v[190:191], v71 src0_sel:WORD_1
	v_pk_fma_f32 v[122:123], v[188:189], s[14:15], v[122:123] op_sel_hi:[1,0,1]
	v_pk_fma_f32 v[124:125], v[190:191], s[14:15], v[124:125] op_sel_hi:[1,0,1]
	v_readlane_b32 s14, v1, 8
	v_cvt_pk_f32_fp8_e32 v[184:185], v64
	v_cvt_pk_f32_fp8_sdwa v[186:187], v64 src0_sel:WORD_1
	v_pk_fma_f32 v[110:111], v[184:185], s[14:15], v[110:111] op_sel_hi:[1,0,1]
	v_pk_fma_f32 v[112:113], v[186:187], s[14:15], v[112:113] op_sel_hi:[1,0,1]
	v_cvt_pk_f32_fp8_e32 v[188:189], v65
	v_cvt_pk_f32_fp8_sdwa v[190:191], v65 src0_sel:WORD_1
	v_pk_fma_f32 v[114:115], v[188:189], s[14:15], v[114:115] op_sel_hi:[1,0,1]
	v_pk_fma_f32 v[116:117], v[190:191], s[14:15], v[116:117] op_sel_hi:[1,0,1]
	v_cvt_pk_f32_fp8_e32 v[184:185], v66
	v_cvt_pk_f32_fp8_sdwa v[186:187], v66 src0_sel:WORD_1
	v_pk_fma_f32 v[118:119], v[184:185], s[14:15], v[118:119] op_sel_hi:[1,0,1]
	v_pk_fma_f32 v[120:121], v[186:187], s[14:15], v[120:121] op_sel_hi:[1,0,1]
	v_cvt_pk_f32_fp8_e32 v[188:189], v67
	v_cvt_pk_f32_fp8_sdwa v[190:191], v67 src0_sel:WORD_1
	v_pk_fma_f32 v[122:123], v[188:189], s[14:15], v[122:123] op_sel_hi:[1,0,1]
	v_pk_fma_f32 v[124:125], v[190:191], s[14:15], v[124:125] op_sel_hi:[1,0,1]
	s_cmp_le_u32 s36, 2
	s_cbranch_scc1 .Lp6b0_axdone
	v_readlane_b32 s14, v1, 16
	v_cvt_pk_f32_fp8_e32 v[184:185], v60
	v_cvt_pk_f32_fp8_sdwa v[186:187], v60 src0_sel:WORD_1
	v_pk_fma_f32 v[110:111], v[184:185], s[14:15], v[110:111] op_sel_hi:[1,0,1]
	v_pk_fma_f32 v[112:113], v[186:187], s[14:15], v[112:113] op_sel_hi:[1,0,1]
	v_cvt_pk_f32_fp8_e32 v[188:189], v61
	v_cvt_pk_f32_fp8_sdwa v[190:191], v61 src0_sel:WORD_1
	v_pk_fma_f32 v[114:115], v[188:189], s[14:15], v[114:115] op_sel_hi:[1,0,1]
	v_pk_fma_f32 v[116:117], v[190:191], s[14:15], v[116:117] op_sel_hi:[1,0,1]
	v_cvt_pk_f32_fp8_e32 v[184:185], v62
	v_cvt_pk_f32_fp8_sdwa v[186:187], v62 src0_sel:WORD_1
	v_pk_fma_f32 v[118:119], v[184:185], s[14:15], v[118:119] op_sel_hi:[1,0,1]
	v_pk_fma_f32 v[120:121], v[186:187], s[14:15], v[120:121] op_sel_hi:[1,0,1]
	v_cvt_pk_f32_fp8_e32 v[188:189], v63
	v_cvt_pk_f32_fp8_sdwa v[190:191], v63 src0_sel:WORD_1
	v_pk_fma_f32 v[122:123], v[188:189], s[14:15], v[122:123] op_sel_hi:[1,0,1]
	v_pk_fma_f32 v[124:125], v[190:191], s[14:15], v[124:125] op_sel_hi:[1,0,1]
	v_readlane_b32 s14, v1, 24
	v_cvt_pk_f32_fp8_e32 v[184:185], v56
	v_cvt_pk_f32_fp8_sdwa v[186:187], v56 src0_sel:WORD_1
	v_pk_fma_f32 v[110:111], v[184:185], s[14:15], v[110:111] op_sel_hi:[1,0,1]
	v_pk_fma_f32 v[112:113], v[186:187], s[14:15], v[112:113] op_sel_hi:[1,0,1]
	v_cvt_pk_f32_fp8_e32 v[188:189], v57
	v_cvt_pk_f32_fp8_sdwa v[190:191], v57 src0_sel:WORD_1
	v_pk_fma_f32 v[114:115], v[188:189], s[14:15], v[114:115] op_sel_hi:[1,0,1]
	v_pk_fma_f32 v[116:117], v[190:191], s[14:15], v[116:117] op_sel_hi:[1,0,1]
	v_cvt_pk_f32_fp8_e32 v[184:185], v58
	v_cvt_pk_f32_fp8_sdwa v[186:187], v58 src0_sel:WORD_1
	v_pk_fma_f32 v[118:119], v[184:185], s[14:15], v[118:119] op_sel_hi:[1,0,1]
	v_pk_fma_f32 v[120:121], v[186:187], s[14:15], v[120:121] op_sel_hi:[1,0,1]
	v_cvt_pk_f32_fp8_e32 v[188:189], v59
	v_cvt_pk_f32_fp8_sdwa v[190:191], v59 src0_sel:WORD_1
	v_pk_fma_f32 v[122:123], v[188:189], s[14:15], v[122:123] op_sel_hi:[1,0,1]
	v_pk_fma_f32 v[124:125], v[190:191], s[14:15], v[124:125] op_sel_hi:[1,0,1]
	s_cmp_le_u32 s36, 4
	s_cbranch_scc1 .Lp6b0_axdone
	v_readlane_b32 s14, v1, 32
	v_cvt_pk_f32_fp8_e32 v[184:185], v48
	v_cvt_pk_f32_fp8_sdwa v[186:187], v48 src0_sel:WORD_1
	v_pk_fma_f32 v[110:111], v[184:185], s[14:15], v[110:111] op_sel_hi:[1,0,1]
	v_pk_fma_f32 v[112:113], v[186:187], s[14:15], v[112:113] op_sel_hi:[1,0,1]
	v_cvt_pk_f32_fp8_e32 v[188:189], v49
	v_cvt_pk_f32_fp8_sdwa v[190:191], v49 src0_sel:WORD_1
	v_pk_fma_f32 v[114:115], v[188:189], s[14:15], v[114:115] op_sel_hi:[1,0,1]
	v_pk_fma_f32 v[116:117], v[190:191], s[14:15], v[116:117] op_sel_hi:[1,0,1]
	v_cvt_pk_f32_fp8_e32 v[184:185], v50
	v_cvt_pk_f32_fp8_sdwa v[186:187], v50 src0_sel:WORD_1
	v_pk_fma_f32 v[118:119], v[184:185], s[14:15], v[118:119] op_sel_hi:[1,0,1]
	v_pk_fma_f32 v[120:121], v[186:187], s[14:15], v[120:121] op_sel_hi:[1,0,1]
	v_cvt_pk_f32_fp8_e32 v[188:189], v51
	v_cvt_pk_f32_fp8_sdwa v[190:191], v51 src0_sel:WORD_1
	v_pk_fma_f32 v[122:123], v[188:189], s[14:15], v[122:123] op_sel_hi:[1,0,1]
	v_pk_fma_f32 v[124:125], v[190:191], s[14:15], v[124:125] op_sel_hi:[1,0,1]
	v_readlane_b32 s14, v1, 40
	v_cvt_pk_f32_fp8_e32 v[184:185], v32
	v_cvt_pk_f32_fp8_sdwa v[186:187], v32 src0_sel:WORD_1
	v_pk_fma_f32 v[110:111], v[184:185], s[14:15], v[110:111] op_sel_hi:[1,0,1]
	v_pk_fma_f32 v[112:113], v[186:187], s[14:15], v[112:113] op_sel_hi:[1,0,1]
	v_cvt_pk_f32_fp8_e32 v[188:189], v33
	v_cvt_pk_f32_fp8_sdwa v[190:191], v33 src0_sel:WORD_1
	v_pk_fma_f32 v[114:115], v[188:189], s[14:15], v[114:115] op_sel_hi:[1,0,1]
	v_pk_fma_f32 v[116:117], v[190:191], s[14:15], v[116:117] op_sel_hi:[1,0,1]
	v_cvt_pk_f32_fp8_e32 v[184:185], v34
	v_cvt_pk_f32_fp8_sdwa v[186:187], v34 src0_sel:WORD_1
	v_pk_fma_f32 v[118:119], v[184:185], s[14:15], v[118:119] op_sel_hi:[1,0,1]
	v_pk_fma_f32 v[120:121], v[186:187], s[14:15], v[120:121] op_sel_hi:[1,0,1]
	v_cvt_pk_f32_fp8_e32 v[188:189], v35
	v_cvt_pk_f32_fp8_sdwa v[190:191], v35 src0_sel:WORD_1
	v_pk_fma_f32 v[122:123], v[188:189], s[14:15], v[122:123] op_sel_hi:[1,0,1]
	v_pk_fma_f32 v[124:125], v[190:191], s[14:15], v[124:125] op_sel_hi:[1,0,1]
	s_cmp_le_u32 s36, 6
	s_cbranch_scc1 .Lp6b0_axdone
	v_readlane_b32 s14, v1, 48
	v_cvt_pk_f32_fp8_e32 v[184:185], v16
	v_cvt_pk_f32_fp8_sdwa v[186:187], v16 src0_sel:WORD_1
	v_pk_fma_f32 v[110:111], v[184:185], s[14:15], v[110:111] op_sel_hi:[1,0,1]
	v_pk_fma_f32 v[112:113], v[186:187], s[14:15], v[112:113] op_sel_hi:[1,0,1]
	v_cvt_pk_f32_fp8_e32 v[188:189], v17
	v_cvt_pk_f32_fp8_sdwa v[190:191], v17 src0_sel:WORD_1
	v_pk_fma_f32 v[114:115], v[188:189], s[14:15], v[114:115] op_sel_hi:[1,0,1]
	v_pk_fma_f32 v[116:117], v[190:191], s[14:15], v[116:117] op_sel_hi:[1,0,1]
	v_cvt_pk_f32_fp8_e32 v[184:185], v18
	v_cvt_pk_f32_fp8_sdwa v[186:187], v18 src0_sel:WORD_1
	v_pk_fma_f32 v[118:119], v[184:185], s[14:15], v[118:119] op_sel_hi:[1,0,1]
	v_pk_fma_f32 v[120:121], v[186:187], s[14:15], v[120:121] op_sel_hi:[1,0,1]
	v_cvt_pk_f32_fp8_e32 v[188:189], v19
	v_cvt_pk_f32_fp8_sdwa v[190:191], v19 src0_sel:WORD_1
	v_pk_fma_f32 v[122:123], v[188:189], s[14:15], v[122:123] op_sel_hi:[1,0,1]
	v_pk_fma_f32 v[124:125], v[190:191], s[14:15], v[124:125] op_sel_hi:[1,0,1]
	v_readlane_b32 s14, v1, 56
	v_cvt_pk_f32_fp8_e32 v[184:185], v12
	v_cvt_pk_f32_fp8_sdwa v[186:187], v12 src0_sel:WORD_1
	v_pk_fma_f32 v[110:111], v[184:185], s[14:15], v[110:111] op_sel_hi:[1,0,1]
	v_pk_fma_f32 v[112:113], v[186:187], s[14:15], v[112:113] op_sel_hi:[1,0,1]
	v_cvt_pk_f32_fp8_e32 v[188:189], v13
	v_cvt_pk_f32_fp8_sdwa v[190:191], v13 src0_sel:WORD_1
	v_pk_fma_f32 v[114:115], v[188:189], s[14:15], v[114:115] op_sel_hi:[1,0,1]
	v_pk_fma_f32 v[116:117], v[190:191], s[14:15], v[116:117] op_sel_hi:[1,0,1]
	v_cvt_pk_f32_fp8_e32 v[184:185], v14
	v_cvt_pk_f32_fp8_sdwa v[186:187], v14 src0_sel:WORD_1
	v_pk_fma_f32 v[118:119], v[184:185], s[14:15], v[118:119] op_sel_hi:[1,0,1]
	v_pk_fma_f32 v[120:121], v[186:187], s[14:15], v[120:121] op_sel_hi:[1,0,1]
	v_cvt_pk_f32_fp8_e32 v[188:189], v15
	v_cvt_pk_f32_fp8_sdwa v[190:191], v15 src0_sel:WORD_1
	v_pk_fma_f32 v[122:123], v[188:189], s[14:15], v[122:123] op_sel_hi:[1,0,1]
	v_pk_fma_f32 v[124:125], v[190:191], s[14:15], v[124:125] op_sel_hi:[1,0,1]
	s_branch .Lp6b0_axdone
.Lp6b0_t0:
	v_readlane_b32 s14, v1, 0
	v_cvt_pk_f32_fp8_e32 v[184:185], v68
	v_cvt_pk_f32_fp8_sdwa v[186:187], v68 src0_sel:WORD_1
	v_pk_fma_f32 v[126:127], v[184:185], s[14:15], v[126:127] op_sel_hi:[1,0,1]
	v_pk_fma_f32 v[128:129], v[186:187], s[14:15], v[128:129] op_sel_hi:[1,0,1]
	v_cvt_pk_f32_fp8_e32 v[188:189], v69
	v_cvt_pk_f32_fp8_sdwa v[190:191], v69 src0_sel:WORD_1
	v_pk_fma_f32 v[130:131], v[188:189], s[14:15], v[130:131] op_sel_hi:[1,0,1]
	v_pk_fma_f32 v[132:133], v[190:191], s[14:15], v[132:133] op_sel_hi:[1,0,1]
	v_cvt_pk_f32_fp8_e32 v[184:185], v70
	v_cvt_pk_f32_fp8_sdwa v[186:187], v70 src0_sel:WORD_1
	v_pk_fma_f32 v[134:135], v[184:185], s[14:15], v[134:135] op_sel_hi:[1,0,1]
	v_pk_fma_f32 v[136:137], v[186:187], s[14:15], v[136:137] op_sel_hi:[1,0,1]
	v_cvt_pk_f32_fp8_e32 v[188:189], v71
	v_cvt_pk_f32_fp8_sdwa v[190:191], v71 src0_sel:WORD_1
	v_pk_fma_f32 v[138:139], v[188:189], s[14:15], v[138:139] op_sel_hi:[1,0,1]
	v_pk_fma_f32 v[140:141], v[190:191], s[14:15], v[140:141] op_sel_hi:[1,0,1]
	v_readlane_b32 s14, v1, 8
	v_cvt_pk_f32_fp8_e32 v[184:185], v64
	v_cvt_pk_f32_fp8_sdwa v[186:187], v64 src0_sel:WORD_1
	v_pk_fma_f32 v[126:127], v[184:185], s[14:15], v[126:127] op_sel_hi:[1,0,1]
	v_pk_fma_f32 v[128:129], v[186:187], s[14:15], v[128:129] op_sel_hi:[1,0,1]
	v_cvt_pk_f32_fp8_e32 v[188:189], v65
	v_cvt_pk_f32_fp8_sdwa v[190:191], v65 src0_sel:WORD_1
	v_pk_fma_f32 v[130:131], v[188:189], s[14:15], v[130:131] op_sel_hi:[1,0,1]
	v_pk_fma_f32 v[132:133], v[190:191], s[14:15], v[132:133] op_sel_hi:[1,0,1]
	v_cvt_pk_f32_fp8_e32 v[184:185], v66
	v_cvt_pk_f32_fp8_sdwa v[186:187], v66 src0_sel:WORD_1
	v_pk_fma_f32 v[134:135], v[184:185], s[14:15], v[134:135] op_sel_hi:[1,0,1]
	v_pk_fma_f32 v[136:137], v[186:187], s[14:15], v[136:137] op_sel_hi:[1,0,1]
	v_cvt_pk_f32_fp8_e32 v[188:189], v67
	v_cvt_pk_f32_fp8_sdwa v[190:191], v67 src0_sel:WORD_1
	v_pk_fma_f32 v[138:139], v[188:189], s[14:15], v[138:139] op_sel_hi:[1,0,1]
	v_pk_fma_f32 v[140:141], v[190:191], s[14:15], v[140:141] op_sel_hi:[1,0,1]
	s_cmp_le_u32 s36, 2
	s_cbranch_scc1 .Lp6b0_axdone
	v_readlane_b32 s14, v1, 16
	v_cvt_pk_f32_fp8_e32 v[184:185], v60
	v_cvt_pk_f32_fp8_sdwa v[186:187], v60 src0_sel:WORD_1
	v_pk_fma_f32 v[126:127], v[184:185], s[14:15], v[126:127] op_sel_hi:[1,0,1]
	v_pk_fma_f32 v[128:129], v[186:187], s[14:15], v[128:129] op_sel_hi:[1,0,1]
	v_cvt_pk_f32_fp8_e32 v[188:189], v61
	v_cvt_pk_f32_fp8_sdwa v[190:191], v61 src0_sel:WORD_1
	v_pk_fma_f32 v[130:131], v[188:189], s[14:15], v[130:131] op_sel_hi:[1,0,1]
	v_pk_fma_f32 v[132:133], v[190:191], s[14:15], v[132:133] op_sel_hi:[1,0,1]
	v_cvt_pk_f32_fp8_e32 v[184:185], v62
	v_cvt_pk_f32_fp8_sdwa v[186:187], v62 src0_sel:WORD_1
	v_pk_fma_f32 v[134:135], v[184:185], s[14:15], v[134:135] op_sel_hi:[1,0,1]
	v_pk_fma_f32 v[136:137], v[186:187], s[14:15], v[136:137] op_sel_hi:[1,0,1]
	v_cvt_pk_f32_fp8_e32 v[188:189], v63
	v_cvt_pk_f32_fp8_sdwa v[190:191], v63 src0_sel:WORD_1
	v_pk_fma_f32 v[138:139], v[188:189], s[14:15], v[138:139] op_sel_hi:[1,0,1]
	v_pk_fma_f32 v[140:141], v[190:191], s[14:15], v[140:141] op_sel_hi:[1,0,1]
	v_readlane_b32 s14, v1, 24
	v_cvt_pk_f32_fp8_e32 v[184:185], v56
	v_cvt_pk_f32_fp8_sdwa v[186:187], v56 src0_sel:WORD_1
	v_pk_fma_f32 v[126:127], v[184:185], s[14:15], v[126:127] op_sel_hi:[1,0,1]
	v_pk_fma_f32 v[128:129], v[186:187], s[14:15], v[128:129] op_sel_hi:[1,0,1]
	v_cvt_pk_f32_fp8_e32 v[188:189], v57
	v_cvt_pk_f32_fp8_sdwa v[190:191], v57 src0_sel:WORD_1
	v_pk_fma_f32 v[130:131], v[188:189], s[14:15], v[130:131] op_sel_hi:[1,0,1]
	v_pk_fma_f32 v[132:133], v[190:191], s[14:15], v[132:133] op_sel_hi:[1,0,1]
	v_cvt_pk_f32_fp8_e32 v[184:185], v58
	v_cvt_pk_f32_fp8_sdwa v[186:187], v58 src0_sel:WORD_1
	v_pk_fma_f32 v[134:135], v[184:185], s[14:15], v[134:135] op_sel_hi:[1,0,1]
	v_pk_fma_f32 v[136:137], v[186:187], s[14:15], v[136:137] op_sel_hi:[1,0,1]
	v_cvt_pk_f32_fp8_e32 v[188:189], v59
	v_cvt_pk_f32_fp8_sdwa v[190:191], v59 src0_sel:WORD_1
	v_pk_fma_f32 v[138:139], v[188:189], s[14:15], v[138:139] op_sel_hi:[1,0,1]
	v_pk_fma_f32 v[140:141], v[190:191], s[14:15], v[140:141] op_sel_hi:[1,0,1]
	s_cmp_le_u32 s36, 4
	s_cbranch_scc1 .Lp6b0_axdone
	v_readlane_b32 s14, v1, 32
	v_cvt_pk_f32_fp8_e32 v[184:185], v48
	v_cvt_pk_f32_fp8_sdwa v[186:187], v48 src0_sel:WORD_1
	v_pk_fma_f32 v[126:127], v[184:185], s[14:15], v[126:127] op_sel_hi:[1,0,1]
	v_pk_fma_f32 v[128:129], v[186:187], s[14:15], v[128:129] op_sel_hi:[1,0,1]
	v_cvt_pk_f32_fp8_e32 v[188:189], v49
	v_cvt_pk_f32_fp8_sdwa v[190:191], v49 src0_sel:WORD_1
	v_pk_fma_f32 v[130:131], v[188:189], s[14:15], v[130:131] op_sel_hi:[1,0,1]
	v_pk_fma_f32 v[132:133], v[190:191], s[14:15], v[132:133] op_sel_hi:[1,0,1]
	v_cvt_pk_f32_fp8_e32 v[184:185], v50
	v_cvt_pk_f32_fp8_sdwa v[186:187], v50 src0_sel:WORD_1
	v_pk_fma_f32 v[134:135], v[184:185], s[14:15], v[134:135] op_sel_hi:[1,0,1]
	v_pk_fma_f32 v[136:137], v[186:187], s[14:15], v[136:137] op_sel_hi:[1,0,1]
	v_cvt_pk_f32_fp8_e32 v[188:189], v51
	v_cvt_pk_f32_fp8_sdwa v[190:191], v51 src0_sel:WORD_1
	v_pk_fma_f32 v[138:139], v[188:189], s[14:15], v[138:139] op_sel_hi:[1,0,1]
	v_pk_fma_f32 v[140:141], v[190:191], s[14:15], v[140:141] op_sel_hi:[1,0,1]
	v_readlane_b32 s14, v1, 40
	v_cvt_pk_f32_fp8_e32 v[184:185], v32
	v_cvt_pk_f32_fp8_sdwa v[186:187], v32 src0_sel:WORD_1
	v_pk_fma_f32 v[126:127], v[184:185], s[14:15], v[126:127] op_sel_hi:[1,0,1]
	v_pk_fma_f32 v[128:129], v[186:187], s[14:15], v[128:129] op_sel_hi:[1,0,1]
	v_cvt_pk_f32_fp8_e32 v[188:189], v33
	v_cvt_pk_f32_fp8_sdwa v[190:191], v33 src0_sel:WORD_1
	v_pk_fma_f32 v[130:131], v[188:189], s[14:15], v[130:131] op_sel_hi:[1,0,1]
	v_pk_fma_f32 v[132:133], v[190:191], s[14:15], v[132:133] op_sel_hi:[1,0,1]
	v_cvt_pk_f32_fp8_e32 v[184:185], v34
	v_cvt_pk_f32_fp8_sdwa v[186:187], v34 src0_sel:WORD_1
	v_pk_fma_f32 v[134:135], v[184:185], s[14:15], v[134:135] op_sel_hi:[1,0,1]
	v_pk_fma_f32 v[136:137], v[186:187], s[14:15], v[136:137] op_sel_hi:[1,0,1]
	v_cvt_pk_f32_fp8_e32 v[188:189], v35
	v_cvt_pk_f32_fp8_sdwa v[190:191], v35 src0_sel:WORD_1
	v_pk_fma_f32 v[138:139], v[188:189], s[14:15], v[138:139] op_sel_hi:[1,0,1]
	v_pk_fma_f32 v[140:141], v[190:191], s[14:15], v[140:141] op_sel_hi:[1,0,1]
	s_cmp_le_u32 s36, 6
	s_cbranch_scc1 .Lp6b0_axdone
	v_readlane_b32 s14, v1, 48
	v_cvt_pk_f32_fp8_e32 v[184:185], v16
	v_cvt_pk_f32_fp8_sdwa v[186:187], v16 src0_sel:WORD_1
	v_pk_fma_f32 v[126:127], v[184:185], s[14:15], v[126:127] op_sel_hi:[1,0,1]
	v_pk_fma_f32 v[128:129], v[186:187], s[14:15], v[128:129] op_sel_hi:[1,0,1]
	v_cvt_pk_f32_fp8_e32 v[188:189], v17
	v_cvt_pk_f32_fp8_sdwa v[190:191], v17 src0_sel:WORD_1
	v_pk_fma_f32 v[130:131], v[188:189], s[14:15], v[130:131] op_sel_hi:[1,0,1]
	v_pk_fma_f32 v[132:133], v[190:191], s[14:15], v[132:133] op_sel_hi:[1,0,1]
	v_cvt_pk_f32_fp8_e32 v[184:185], v18
	v_cvt_pk_f32_fp8_sdwa v[186:187], v18 src0_sel:WORD_1
	v_pk_fma_f32 v[134:135], v[184:185], s[14:15], v[134:135] op_sel_hi:[1,0,1]
	v_pk_fma_f32 v[136:137], v[186:187], s[14:15], v[136:137] op_sel_hi:[1,0,1]
	v_cvt_pk_f32_fp8_e32 v[188:189], v19
	v_cvt_pk_f32_fp8_sdwa v[190:191], v19 src0_sel:WORD_1
	v_pk_fma_f32 v[138:139], v[188:189], s[14:15], v[138:139] op_sel_hi:[1,0,1]
	v_pk_fma_f32 v[140:141], v[190:191], s[14:15], v[140:141] op_sel_hi:[1,0,1]
	v_readlane_b32 s14, v1, 56
	v_cvt_pk_f32_fp8_e32 v[184:185], v12
	v_cvt_pk_f32_fp8_sdwa v[186:187], v12 src0_sel:WORD_1
	v_pk_fma_f32 v[126:127], v[184:185], s[14:15], v[126:127] op_sel_hi:[1,0,1]
	v_pk_fma_f32 v[128:129], v[186:187], s[14:15], v[128:129] op_sel_hi:[1,0,1]
	v_cvt_pk_f32_fp8_e32 v[188:189], v13
	v_cvt_pk_f32_fp8_sdwa v[190:191], v13 src0_sel:WORD_1
	v_pk_fma_f32 v[130:131], v[188:189], s[14:15], v[130:131] op_sel_hi:[1,0,1]
	v_pk_fma_f32 v[132:133], v[190:191], s[14:15], v[132:133] op_sel_hi:[1,0,1]
	v_cvt_pk_f32_fp8_e32 v[184:185], v14
	v_cvt_pk_f32_fp8_sdwa v[186:187], v14 src0_sel:WORD_1
	v_pk_fma_f32 v[134:135], v[184:185], s[14:15], v[134:135] op_sel_hi:[1,0,1]
	v_pk_fma_f32 v[136:137], v[186:187], s[14:15], v[136:137] op_sel_hi:[1,0,1]
	v_cvt_pk_f32_fp8_e32 v[188:189], v15
	v_cvt_pk_f32_fp8_sdwa v[190:191], v15 src0_sel:WORD_1
	v_pk_fma_f32 v[138:139], v[188:189], s[14:15], v[138:139] op_sel_hi:[1,0,1]
	v_pk_fma_f32 v[140:141], v[190:191], s[14:15], v[140:141] op_sel_hi:[1,0,1]
.Lp6b0_axdone:
	s_nop 4
	buffer_load_dwordx4 v[68:71], v181, s[92:95], s44 offen
	buffer_load_dwordx4 v[64:67], v181, s[92:95], s45 offen
	buffer_load_dwordx4 v[60:63], v181, s[92:95], s46 offen
	buffer_load_dwordx4 v[56:59], v181, s[92:95], s47 offen
	buffer_load_dwordx4 v[48:51], v181, s[92:95], s48 offen
	buffer_load_dwordx4 v[32:35], v181, s[92:95], s49 offen
	buffer_load_dwordx4 v[16:19], v181, s[92:95], s50 offen
	buffer_load_dwordx4 v[12:15], v181, s[92:95], s51 offen
	s_mov_b32 s26, s86
	s_mov_b32 s86, s27
	s_mov_b32 s27, s32
	s_cmp_eq_u32 s22, s23
	s_cbranch_scc1 .LBB0_973
.Lp6b1_top:
	s_add_i32 s23, s23, 1
	s_add_i32 s2, s23, 2
	s_add_i32 s3, s22, -1
	s_min_i32 s2, s2, s3
	s_lshl_b32 s2, s2, 2
	s_add_i32 s2, s85, s2
	v_mov_b32_e32 v1, s2
	ds_read_b32 v1, v1 offset:4864
	s_waitcnt lgkmcnt(0)
	v_readfirstlane_b32 s32, v1
	s_and_b32 s2, s32, 0x3ff
	s_bfe_u32 s3, s32, 0x4000a
	v_cmp_gt_u32_e32 vcc, s3, v182
	s_lshl_b32 s2, s2, 2
	s_add_i32 s2, s2, s85
	v_cndmask_b32_e32 v1, 0, v182, vcc
	v_lshl_add_u32 v1, v1, 2, s2
	ds_read_b32 v1, v1 offset:8192
	s_waitcnt lgkmcnt(0)
	v_lshlrev_b32_e32 v1, 10, v1
	v_and_b32_e32 v1, 0x3fffc00, v1
	s_nop 0
	v_readlane_b32 s44, v1, 0
	v_readlane_b32 s45, v1, 1
	v_readlane_b32 s46, v1, 2
	v_readlane_b32 s47, v1, 3
	v_readlane_b32 s48, v1, 4
	v_readlane_b32 s49, v1, 5
	v_readlane_b32 s50, v1, 6
	v_readlane_b32 s51, v1, 7
	s_bfe_u32 s14, s26, 0x4000a
	v_cmp_gt_u32_e32 vcc, s14, v180
	v_mov_b32_e32 v1, 0
	s_and_b32 s2, s26, 0x3ff
	s_lshr_b32 s66, s26, 14
	s_and_saveexec_b64 s[14:15], vcc
	v_add_u32_e32 v2, s2, v180
	v_lshl_add_u32 v2, v2, 2, s85
	ds_read_b32 v1, v2 offset:12288
	s_or_b64 exec, exec, s[14:15]
	s_waitcnt vmcnt(16)
	s_waitcnt lgkmcnt(0)
	s_bfe_u32 s36, s26, 0x4000a
	s_cmp_lt_i32 s66, 1
	s_cbranch_scc1 .Lp6b1_t0
	s_cmp_lt_i32 s66, 2
	s_cbranch_scc1 .Lp6b1_t1
	s_cmp_lg_u32 s66, 2
	s_cbranch_scc0 .Lp6b1_t2
	v_readlane_b32 s14, v1, 0
	v_cvt_pk_f32_fp8_e32 v[184:185], v72
	v_cvt_pk_f32_fp8_sdwa v[186:187], v72 src0_sel:WORD_1
	v_pk_fma_f32 v[78:79], v[184:185], s[14:15], v[78:79] op_sel_hi:[1,0,1]
	v_pk_fma_f32 v[80:81], v[186:187], s[14:15], v[80:81] op_sel_hi:[1,0,1]
	v_cvt_pk_f32_fp8_e32 v[188:189], v73
	v_cvt_pk_f32_fp8_sdwa v[190:191], v73 src0_sel:WORD_1
	v_pk_fma_f32 v[82:83], v[188:189], s[14:15], v[82:83] op_sel_hi:[1,0,1]
	v_pk_fma_f32 v[86:87], v[190:191], s[14:15], v[86:87] op_sel_hi:[1,0,1]
	v_cvt_pk_f32_fp8_e32 v[184:185], v74
	v_cvt_pk_f32_fp8_sdwa v[186:187], v74 src0_sel:WORD_1
	v_pk_fma_f32 v[88:89], v[184:185], s[14:15], v[88:89] op_sel_hi:[1,0,1]
	v_pk_fma_f32 v[90:91], v[186:187], s[14:15], v[90:91] op_sel_hi:[1,0,1]
	v_cvt_pk_f32_fp8_e32 v[188:189], v75
	v_cvt_pk_f32_fp8_sdwa v[190:191], v75 src0_sel:WORD_1
	v_pk_fma_f32 v[92:93], v[188:189], s[14:15], v[92:93] op_sel_hi:[1,0,1]
	v_pk_fma_f32 v[84:85], v[190:191], s[14:15], v[84:85] op_sel_hi:[1,0,1]
	v_readlane_b32 s14, v1, 8
	v_cvt_pk_f32_fp8_e32 v[184:185], v52
	v_cvt_pk_f32_fp8_sdwa v[186:187], v52 src0_sel:WORD_1
	v_pk_fma_f32 v[78:79], v[184:185], s[14:15], v[78:79] op_sel_hi:[1,0,1]
	v_pk_fma_f32 v[80:81], v[186:187], s[14:15], v[80:81] op_sel_hi:[1,0,1]
	v_cvt_pk_f32_fp8_e32 v[188:189], v53
	v_cvt_pk_f32_fp8_sdwa v[190:191], v53 src0_sel:WORD_1
	v_pk_fma_f32 v[82:83], v[188:189], s[14:15], v[82:83] op_sel_hi:[1,0,1]
	v_pk_fma_f32 v[86:87], v[190:191], s[14:15], v[86:87] op_sel_hi:[1,0,1]
	v_cvt_pk_f32_fp8_e32 v[184:185], v54
	v_cvt_pk_f32_fp8_sdwa v[186:187], v54 src0_sel:WORD_1
	v_pk_fma_f32 v[88:89], v[184:185], s[14:15], v[88:89] op_sel_hi:[1,0,1]
	v_pk_fma_f32 v[90:91], v[186:187], s[14:15], v[90:91] op_sel_hi:[1,0,1]
	v_cvt_pk_f32_fp8_e32 v[188:189], v55
	v_cvt_pk_f32_fp8_sdwa v[190:191], v55 src0_sel:WORD_1
	v_pk_fma_f32 v[92:93], v[188:189], s[14:15], v[92:93] op_sel_hi:[1,0,1]
	v_pk_fma_f32 v[84:85], v[190:191], s[14:15], v[84:85] op_sel_hi:[1,0,1]
	s_cmp_le_u32 s36, 2
	s_cbranch_scc1 .Lp6b1_axdone
	v_readlane_b32 s14, v1, 16
	v_cvt_pk_f32_fp8_e32 v[184:185], v44
	v_cvt_pk_f32_fp8_sdwa v[186:187], v44 src0_sel:WORD_1
	v_pk_fma_f32 v[78:79], v[184:185], s[14:15], v[78:79] op_sel_hi:[1,0,1]
	v_pk_fma_f32 v[80:81], v[186:187], s[14:15], v[80:81] op_sel_hi:[1,0,1]
	v_cvt_pk_f32_fp8_e32 v[188:189], v45
	v_cvt_pk_f32_fp8_sdwa v[190:191], v45 src0_sel:WORD_1
	v_pk_fma_f32 v[82:83], v[188:189], s[14:15], v[82:83] op_sel_hi:[1,0,1]
	v_pk_fma_f32 v[86:87], v[190:191], s[14:15], v[86:87] op_sel_hi:[1,0,1]
	v_cvt_pk_f32_fp8_e32 v[184:185], v46
	v_cvt_pk_f32_fp8_sdwa v[186:187], v46 src0_sel:WORD_1
	v_pk_fma_f32 v[88:89], v[184:185], s[14:15], v[88:89] op_sel_hi:[1,0,1]
	v_pk_fma_f32 v[90:91], v[186:187], s[14:15], v[90:91] op_sel_hi:[1,0,1]
	v_cvt_pk_f32_fp8_e32 v[188:189], v47
	v_cvt_pk_f32_fp8_sdwa v[190:191], v47 src0_sel:WORD_1
	v_pk_fma_f32 v[92:93], v[188:189], s[14:15], v[92:93] op_sel_hi:[1,0,1]
	v_pk_fma_f32 v[84:85], v[190:191], s[14:15], v[84:85] op_sel_hi:[1,0,1]
	v_readlane_b32 s14, v1, 24
	v_cvt_pk_f32_fp8_e32 v[184:185], v40
	v_cvt_pk_f32_fp8_sdwa v[186:187], v40 src0_sel:WORD_1
	v_pk_fma_f32 v[78:79], v[184:185], s[14:15], v[78:79] op_sel_hi:[1,0,1]
	v_pk_fma_f32 v[80:81], v[186:187], s[14:15], v[80:81] op_sel_hi:[1,0,1]
	v_cvt_pk_f32_fp8_e32 v[188:189], v41
	v_cvt_pk_f32_fp8_sdwa v[190:191], v41 src0_sel:WORD_1
	v_pk_fma_f32 v[82:83], v[188:189], s[14:15], v[82:83] op_sel_hi:[1,0,1]
	v_pk_fma_f32 v[86:87], v[190:191], s[14:15], v[86:87] op_sel_hi:[1,0,1]
	v_cvt_pk_f32_fp8_e32 v[184:185], v42
	v_cvt_pk_f32_fp8_sdwa v[186:187], v42 src0_sel:WORD_1
	v_pk_fma_f32 v[88:89], v[184:185], s[14:15], v[88:89] op_sel_hi:[1,0,1]
	v_pk_fma_f32 v[90:91], v[186:187], s[14:15], v[90:91] op_sel_hi:[1,0,1]
	v_cvt_pk_f32_fp8_e32 v[188:189], v43
	v_cvt_pk_f32_fp8_sdwa v[190:191], v43 src0_sel:WORD_1
	v_pk_fma_f32 v[92:93], v[188:189], s[14:15], v[92:93] op_sel_hi:[1,0,1]
	v_pk_fma_f32 v[84:85], v[190:191], s[14:15], v[84:85] op_sel_hi:[1,0,1]
	s_cmp_le_u32 s36, 4
	s_cbranch_scc1 .Lp6b1_axdone
	v_readlane_b32 s14, v1, 32
	v_cvt_pk_f32_fp8_e32 v[184:185], v36
	v_cvt_pk_f32_fp8_sdwa v[186:187], v36 src0_sel:WORD_1
	v_pk_fma_f32 v[78:79], v[184:185], s[14:15], v[78:79] op_sel_hi:[1,0,1]
	v_pk_fma_f32 v[80:81], v[186:187], s[14:15], v[80:81] op_sel_hi:[1,0,1]
	v_cvt_pk_f32_fp8_e32 v[188:189], v37
	v_cvt_pk_f32_fp8_sdwa v[190:191], v37 src0_sel:WORD_1
	v_pk_fma_f32 v[82:83], v[188:189], s[14:15], v[82:83] op_sel_hi:[1,0,1]
	v_pk_fma_f32 v[86:87], v[190:191], s[14:15], v[86:87] op_sel_hi:[1,0,1]
	v_cvt_pk_f32_fp8_e32 v[184:185], v38
	v_cvt_pk_f32_fp8_sdwa v[186:187], v38 src0_sel:WORD_1
	v_pk_fma_f32 v[88:89], v[184:185], s[14:15], v[88:89] op_sel_hi:[1,0,1]
	v_pk_fma_f32 v[90:91], v[186:187], s[14:15], v[90:91] op_sel_hi:[1,0,1]
	v_cvt_pk_f32_fp8_e32 v[188:189], v39
	v_cvt_pk_f32_fp8_sdwa v[190:191], v39 src0_sel:WORD_1
	v_pk_fma_f32 v[92:93], v[188:189], s[14:15], v[92:93] op_sel_hi:[1,0,1]
	v_pk_fma_f32 v[84:85], v[190:191], s[14:15], v[84:85] op_sel_hi:[1,0,1]
	v_readlane_b32 s14, v1, 40
	v_cvt_pk_f32_fp8_e32 v[184:185], v28
	v_cvt_pk_f32_fp8_sdwa v[186:187], v28 src0_sel:WORD_1
	v_pk_fma_f32 v[78:79], v[184:185], s[14:15], v[78:79] op_sel_hi:[1,0,1]
	v_pk_fma_f32 v[80:81], v[186:187], s[14:15], v[80:81] op_sel_hi:[1,0,1]
	v_cvt_pk_f32_fp8_e32 v[188:189], v29
	v_cvt_pk_f32_fp8_sdwa v[190:191], v29 src0_sel:WORD_1
	v_pk_fma_f32 v[82:83], v[188:189], s[14:15], v[82:83] op_sel_hi:[1,0,1]
	v_pk_fma_f32 v[86:87], v[190:191], s[14:15], v[86:87] op_sel_hi:[1,0,1]
	v_cvt_pk_f32_fp8_e32 v[184:185], v30
	v_cvt_pk_f32_fp8_sdwa v[186:187], v30 src0_sel:WORD_1
	v_pk_fma_f32 v[88:89], v[184:185], s[14:15], v[88:89] op_sel_hi:[1,0,1]
	v_pk_fma_f32 v[90:91], v[186:187], s[14:15], v[90:91] op_sel_hi:[1,0,1]
	v_cvt_pk_f32_fp8_e32 v[188:189], v31
	v_cvt_pk_f32_fp8_sdwa v[190:191], v31 src0_sel:WORD_1
	v_pk_fma_f32 v[92:93], v[188:189], s[14:15], v[92:93] op_sel_hi:[1,0,1]
	v_pk_fma_f32 v[84:85], v[190:191], s[14:15], v[84:85] op_sel_hi:[1,0,1]
	s_cmp_le_u32 s36, 6
	s_cbranch_scc1 .Lp6b1_axdone
	v_readlane_b32 s14, v1, 48
	v_cvt_pk_f32_fp8_e32 v[184:185], v24
	v_cvt_pk_f32_fp8_sdwa v[186:187], v24 src0_sel:WORD_1
	v_pk_fma_f32 v[78:79], v[184:185], s[14:15], v[78:79] op_sel_hi:[1,0,1]
	v_pk_fma_f32 v[80:81], v[186:187], s[14:15], v[80:81] op_sel_hi:[1,0,1]
	v_cvt_pk_f32_fp8_e32 v[188:189], v25
	v_cvt_pk_f32_fp8_sdwa v[190:191], v25 src0_sel:WORD_1
	v_pk_fma_f32 v[82:83], v[188:189], s[14:15], v[82:83] op_sel_hi:[1,0,1]
	v_pk_fma_f32 v[86:87], v[190:191], s[14:15], v[86:87] op_sel_hi:[1,0,1]
	v_cvt_pk_f32_fp8_e32 v[184:185], v26
	v_cvt_pk_f32_fp8_sdwa v[186:187], v26 src0_sel:WORD_1
	v_pk_fma_f32 v[88:89], v[184:185], s[14:15], v[88:89] op_sel_hi:[1,0,1]
	v_pk_fma_f32 v[90:91], v[186:187], s[14:15], v[90:91] op_sel_hi:[1,0,1]
	v_cvt_pk_f32_fp8_e32 v[188:189], v27
	v_cvt_pk_f32_fp8_sdwa v[190:191], v27 src0_sel:WORD_1
	v_pk_fma_f32 v[92:93], v[188:189], s[14:15], v[92:93] op_sel_hi:[1,0,1]
	v_pk_fma_f32 v[84:85], v[190:191], s[14:15], v[84:85] op_sel_hi:[1,0,1]
	v_readlane_b32 s14, v1, 56
	v_cvt_pk_f32_fp8_e32 v[184:185], v20
	v_cvt_pk_f32_fp8_sdwa v[186:187], v20 src0_sel:WORD_1
	v_pk_fma_f32 v[78:79], v[184:185], s[14:15], v[78:79] op_sel_hi:[1,0,1]
	v_pk_fma_f32 v[80:81], v[186:187], s[14:15], v[80:81] op_sel_hi:[1,0,1]
	v_cvt_pk_f32_fp8_e32 v[188:189], v21
	v_cvt_pk_f32_fp8_sdwa v[190:191], v21 src0_sel:WORD_1
	v_pk_fma_f32 v[82:83], v[188:189], s[14:15], v[82:83] op_sel_hi:[1,0,1]
	v_pk_fma_f32 v[86:87], v[190:191], s[14:15], v[86:87] op_sel_hi:[1,0,1]
	v_cvt_pk_f32_fp8_e32 v[184:185], v22
	v_cvt_pk_f32_fp8_sdwa v[186:187], v22 src0_sel:WORD_1
	v_pk_fma_f32 v[88:89], v[184:185], s[14:15], v[88:89] op_sel_hi:[1,0,1]
	v_pk_fma_f32 v[90:91], v[186:187], s[14:15], v[90:91] op_sel_hi:[1,0,1]
	v_cvt_pk_f32_fp8_e32 v[188:189], v23
	v_cvt_pk_f32_fp8_sdwa v[190:191], v23 src0_sel:WORD_1
	v_pk_fma_f32 v[92:93], v[188:189], s[14:15], v[92:93] op_sel_hi:[1,0,1]
	v_pk_fma_f32 v[84:85], v[190:191], s[14:15], v[84:85] op_sel_hi:[1,0,1]
	s_branch .Lp6b1_axdone
.Lp6b1_t2:
	v_readlane_b32 s14, v1, 0
	v_cvt_pk_f32_fp8_e32 v[184:185], v72
	v_cvt_pk_f32_fp8_sdwa v[186:187], v72 src0_sel:WORD_1
	v_pk_fma_f32 v[94:95], v[184:185], s[14:15], v[94:95] op_sel_hi:[1,0,1]
	v_pk_fma_f32 v[96:97], v[186:187], s[14:15], v[96:97] op_sel_hi:[1,0,1]
	v_cvt_pk_f32_fp8_e32 v[188:189], v73
	v_cvt_pk_f32_fp8_sdwa v[190:191], v73 src0_sel:WORD_1
	v_pk_fma_f32 v[98:99], v[188:189], s[14:15], v[98:99] op_sel_hi:[1,0,1]
	v_pk_fma_f32 v[100:101], v[190:191], s[14:15], v[100:101] op_sel_hi:[1,0,1]
	v_cvt_pk_f32_fp8_e32 v[184:185], v74
	v_cvt_pk_f32_fp8_sdwa v[186:187], v74 src0_sel:WORD_1
	v_pk_fma_f32 v[102:103], v[184:185], s[14:15], v[102:103] op_sel_hi:[1,0,1]
	v_pk_fma_f32 v[104:105], v[186:187], s[14:15], v[104:105] op_sel_hi:[1,0,1]
	v_cvt_pk_f32_fp8_e32 v[188:189], v75
	v_cvt_pk_f32_fp8_sdwa v[190:191], v75 src0_sel:WORD_1
	v_pk_fma_f32 v[106:107], v[188:189], s[14:15], v[106:107] op_sel_hi:[1,0,1]
	v_pk_fma_f32 v[108:109], v[190:191], s[14:15], v[108:109] op_sel_hi:[1,0,1]
	v_readlane_b32 s14, v1, 8
	v_cvt_pk_f32_fp8_e32 v[184:185], v52
	v_cvt_pk_f32_fp8_sdwa v[186:187], v52 src0_sel:WORD_1
	v_pk_fma_f32 v[94:95], v[184:185], s[14:15], v[94:95] op_sel_hi:[1,0,1]
	v_pk_fma_f32 v[96:97], v[186:187], s[14:15], v[96:97] op_sel_hi:[1,0,1]
	v_cvt_pk_f32_fp8_e32 v[188:189], v53
	v_cvt_pk_f32_fp8_sdwa v[190:191], v53 src0_sel:WORD_1
	v_pk_fma_f32 v[98:99], v[188:189], s[14:15], v[98:99] op_sel_hi:[1,0,1]
	v_pk_fma_f32 v[100:101], v[190:191], s[14:15], v[100:101] op_sel_hi:[1,0,1]
	v_cvt_pk_f32_fp8_e32 v[184:185], v54
	v_cvt_pk_f32_fp8_sdwa v[186:187], v54 src0_sel:WORD_1
	v_pk_fma_f32 v[102:103], v[184:185], s[14:15], v[102:103] op_sel_hi:[1,0,1]
	v_pk_fma_f32 v[104:105], v[186:187], s[14:15], v[104:105] op_sel_hi:[1,0,1]
	v_cvt_pk_f32_fp8_e32 v[188:189], v55
	v_cvt_pk_f32_fp8_sdwa v[190:191], v55 src0_sel:WORD_1
	v_pk_fma_f32 v[106:107], v[188:189], s[14:15], v[106:107] op_sel_hi:[1,0,1]
	v_pk_fma_f32 v[108:109], v[190:191], s[14:15], v[108:109] op_sel_hi:[1,0,1]
	s_cmp_le_u32 s36, 2
	s_cbranch_scc1 .Lp6b1_axdone
	v_readlane_b32 s14, v1, 16
	v_cvt_pk_f32_fp8_e32 v[184:185], v44
	v_cvt_pk_f32_fp8_sdwa v[186:187], v44 src0_sel:WORD_1
	v_pk_fma_f32 v[94:95], v[184:185], s[14:15], v[94:95] op_sel_hi:[1,0,1]
	v_pk_fma_f32 v[96:97], v[186:187], s[14:15], v[96:97] op_sel_hi:[1,0,1]
	v_cvt_pk_f32_fp8_e32 v[188:189], v45
	v_cvt_pk_f32_fp8_sdwa v[190:191], v45 src0_sel:WORD_1
	v_pk_fma_f32 v[98:99], v[188:189], s[14:15], v[98:99] op_sel_hi:[1,0,1]
	v_pk_fma_f32 v[100:101], v[190:191], s[14:15], v[100:101] op_sel_hi:[1,0,1]
	v_cvt_pk_f32_fp8_e32 v[184:185], v46
	v_cvt_pk_f32_fp8_sdwa v[186:187], v46 src0_sel:WORD_1
	v_pk_fma_f32 v[102:103], v[184:185], s[14:15], v[102:103] op_sel_hi:[1,0,1]
	v_pk_fma_f32 v[104:105], v[186:187], s[14:15], v[104:105] op_sel_hi:[1,0,1]
	v_cvt_pk_f32_fp8_e32 v[188:189], v47
	v_cvt_pk_f32_fp8_sdwa v[190:191], v47 src0_sel:WORD_1
	v_pk_fma_f32 v[106:107], v[188:189], s[14:15], v[106:107] op_sel_hi:[1,0,1]
	v_pk_fma_f32 v[108:109], v[190:191], s[14:15], v[108:109] op_sel_hi:[1,0,1]
	v_readlane_b32 s14, v1, 24
	v_cvt_pk_f32_fp8_e32 v[184:185], v40
	v_cvt_pk_f32_fp8_sdwa v[186:187], v40 src0_sel:WORD_1
	v_pk_fma_f32 v[94:95], v[184:185], s[14:15], v[94:95] op_sel_hi:[1,0,1]
	v_pk_fma_f32 v[96:97], v[186:187], s[14:15], v[96:97] op_sel_hi:[1,0,1]
	v_cvt_pk_f32_fp8_e32 v[188:189], v41
	v_cvt_pk_f32_fp8_sdwa v[190:191], v41 src0_sel:WORD_1
	v_pk_fma_f32 v[98:99], v[188:189], s[14:15], v[98:99] op_sel_hi:[1,0,1]
	v_pk_fma_f32 v[100:101], v[190:191], s[14:15], v[100:101] op_sel_hi:[1,0,1]
	v_cvt_pk_f32_fp8_e32 v[184:185], v42
	v_cvt_pk_f32_fp8_sdwa v[186:187], v42 src0_sel:WORD_1
	v_pk_fma_f32 v[102:103], v[184:185], s[14:15], v[102:103] op_sel_hi:[1,0,1]
	v_pk_fma_f32 v[104:105], v[186:187], s[14:15], v[104:105] op_sel_hi:[1,0,1]
	v_cvt_pk_f32_fp8_e32 v[188:189], v43
	v_cvt_pk_f32_fp8_sdwa v[190:191], v43 src0_sel:WORD_1
	v_pk_fma_f32 v[106:107], v[188:189], s[14:15], v[106:107] op_sel_hi:[1,0,1]
	v_pk_fma_f32 v[108:109], v[190:191], s[14:15], v[108:109] op_sel_hi:[1,0,1]
	s_cmp_le_u32 s36, 4
	s_cbranch_scc1 .Lp6b1_axdone
	v_readlane_b32 s14, v1, 32
	v_cvt_pk_f32_fp8_e32 v[184:185], v36
	v_cvt_pk_f32_fp8_sdwa v[186:187], v36 src0_sel:WORD_1
	v_pk_fma_f32 v[94:95], v[184:185], s[14:15], v[94:95] op_sel_hi:[1,0,1]
	v_pk_fma_f32 v[96:97], v[186:187], s[14:15], v[96:97] op_sel_hi:[1,0,1]
	v_cvt_pk_f32_fp8_e32 v[188:189], v37
	v_cvt_pk_f32_fp8_sdwa v[190:191], v37 src0_sel:WORD_1
	v_pk_fma_f32 v[98:99], v[188:189], s[14:15], v[98:99] op_sel_hi:[1,0,1]
	v_pk_fma_f32 v[100:101], v[190:191], s[14:15], v[100:101] op_sel_hi:[1,0,1]
	v_cvt_pk_f32_fp8_e32 v[184:185], v38
	v_cvt_pk_f32_fp8_sdwa v[186:187], v38 src0_sel:WORD_1
	v_pk_fma_f32 v[102:103], v[184:185], s[14:15], v[102:103] op_sel_hi:[1,0,1]
	v_pk_fma_f32 v[104:105], v[186:187], s[14:15], v[104:105] op_sel_hi:[1,0,1]
	v_cvt_pk_f32_fp8_e32 v[188:189], v39
	v_cvt_pk_f32_fp8_sdwa v[190:191], v39 src0_sel:WORD_1
	v_pk_fma_f32 v[106:107], v[188:189], s[14:15], v[106:107] op_sel_hi:[1,0,1]
	v_pk_fma_f32 v[108:109], v[190:191], s[14:15], v[108:109] op_sel_hi:[1,0,1]
	v_readlane_b32 s14, v1, 40
	v_cvt_pk_f32_fp8_e32 v[184:185], v28
	v_cvt_pk_f32_fp8_sdwa v[186:187], v28 src0_sel:WORD_1
	v_pk_fma_f32 v[94:95], v[184:185], s[14:15], v[94:95] op_sel_hi:[1,0,1]
	v_pk_fma_f32 v[96:97], v[186:187], s[14:15], v[96:97] op_sel_hi:[1,0,1]
	v_cvt_pk_f32_fp8_e32 v[188:189], v29
	v_cvt_pk_f32_fp8_sdwa v[190:191], v29 src0_sel:WORD_1
	v_pk_fma_f32 v[98:99], v[188:189], s[14:15], v[98:99] op_sel_hi:[1,0,1]
	v_pk_fma_f32 v[100:101], v[190:191], s[14:15], v[100:101] op_sel_hi:[1,0,1]
	v_cvt_pk_f32_fp8_e32 v[184:185], v30
	v_cvt_pk_f32_fp8_sdwa v[186:187], v30 src0_sel:WORD_1
	v_pk_fma_f32 v[102:103], v[184:185], s[14:15], v[102:103] op_sel_hi:[1,0,1]
	v_pk_fma_f32 v[104:105], v[186:187], s[14:15], v[104:105] op_sel_hi:[1,0,1]
	v_cvt_pk_f32_fp8_e32 v[188:189], v31
	v_cvt_pk_f32_fp8_sdwa v[190:191], v31 src0_sel:WORD_1
	v_pk_fma_f32 v[106:107], v[188:189], s[14:15], v[106:107] op_sel_hi:[1,0,1]
	v_pk_fma_f32 v[108:109], v[190:191], s[14:15], v[108:109] op_sel_hi:[1,0,1]
	s_cmp_le_u32 s36, 6
	s_cbranch_scc1 .Lp6b1_axdone
	v_readlane_b32 s14, v1, 48
	v_cvt_pk_f32_fp8_e32 v[184:185], v24
	v_cvt_pk_f32_fp8_sdwa v[186:187], v24 src0_sel:WORD_1
	v_pk_fma_f32 v[94:95], v[184:185], s[14:15], v[94:95] op_sel_hi:[1,0,1]
	v_pk_fma_f32 v[96:97], v[186:187], s[14:15], v[96:97] op_sel_hi:[1,0,1]
	v_cvt_pk_f32_fp8_e32 v[188:189], v25
	v_cvt_pk_f32_fp8_sdwa v[190:191], v25 src0_sel:WORD_1
	v_pk_fma_f32 v[98:99], v[188:189], s[14:15], v[98:99] op_sel_hi:[1,0,1]
	v_pk_fma_f32 v[100:101], v[190:191], s[14:15], v[100:101] op_sel_hi:[1,0,1]
	v_cvt_pk_f32_fp8_e32 v[184:185], v26
	v_cvt_pk_f32_fp8_sdwa v[186:187], v26 src0_sel:WORD_1
	v_pk_fma_f32 v[102:103], v[184:185], s[14:15], v[102:103] op_sel_hi:[1,0,1]
	v_pk_fma_f32 v[104:105], v[186:187], s[14:15], v[104:105] op_sel_hi:[1,0,1]
	v_cvt_pk_f32_fp8_e32 v[188:189], v27
	v_cvt_pk_f32_fp8_sdwa v[190:191], v27 src0_sel:WORD_1
	v_pk_fma_f32 v[106:107], v[188:189], s[14:15], v[106:107] op_sel_hi:[1,0,1]
	v_pk_fma_f32 v[108:109], v[190:191], s[14:15], v[108:109] op_sel_hi:[1,0,1]
	v_readlane_b32 s14, v1, 56
	v_cvt_pk_f32_fp8_e32 v[184:185], v20
	v_cvt_pk_f32_fp8_sdwa v[186:187], v20 src0_sel:WORD_1
	v_pk_fma_f32 v[94:95], v[184:185], s[14:15], v[94:95] op_sel_hi:[1,0,1]
	v_pk_fma_f32 v[96:97], v[186:187], s[14:15], v[96:97] op_sel_hi:[1,0,1]
	v_cvt_pk_f32_fp8_e32 v[188:189], v21
	v_cvt_pk_f32_fp8_sdwa v[190:191], v21 src0_sel:WORD_1
	v_pk_fma_f32 v[98:99], v[188:189], s[14:15], v[98:99] op_sel_hi:[1,0,1]
	v_pk_fma_f32 v[100:101], v[190:191], s[14:15], v[100:101] op_sel_hi:[1,0,1]
	v_cvt_pk_f32_fp8_e32 v[184:185], v22
	v_cvt_pk_f32_fp8_sdwa v[186:187], v22 src0_sel:WORD_1
	v_pk_fma_f32 v[102:103], v[184:185], s[14:15], v[102:103] op_sel_hi:[1,0,1]
	v_pk_fma_f32 v[104:105], v[186:187], s[14:15], v[104:105] op_sel_hi:[1,0,1]
	v_cvt_pk_f32_fp8_e32 v[188:189], v23
	v_cvt_pk_f32_fp8_sdwa v[190:191], v23 src0_sel:WORD_1
	v_pk_fma_f32 v[106:107], v[188:189], s[14:15], v[106:107] op_sel_hi:[1,0,1]
	v_pk_fma_f32 v[108:109], v[190:191], s[14:15], v[108:109] op_sel_hi:[1,0,1]
	s_branch .Lp6b1_axdone
.Lp6b1_t1:
	v_readlane_b32 s14, v1, 0
	v_cvt_pk_f32_fp8_e32 v[184:185], v72
	v_cvt_pk_f32_fp8_sdwa v[186:187], v72 src0_sel:WORD_1
	v_pk_fma_f32 v[110:111], v[184:185], s[14:15], v[110:111] op_sel_hi:[1,0,1]
	v_pk_fma_f32 v[112:113], v[186:187], s[14:15], v[112:113] op_sel_hi:[1,0,1]
	v_cvt_pk_f32_fp8_e32 v[188:189], v73
	v_cvt_pk_f32_fp8_sdwa v[190:191], v73 src0_sel:WORD_1
	v_pk_fma_f32 v[114:115], v[188:189], s[14:15], v[114:115] op_sel_hi:[1,0,1]
	v_pk_fma_f32 v[116:117], v[190:191], s[14:15], v[116:117] op_sel_hi:[1,0,1]
	v_cvt_pk_f32_fp8_e32 v[184:185], v74
	v_cvt_pk_f32_fp8_sdwa v[186:187], v74 src0_sel:WORD_1
	v_pk_fma_f32 v[118:119], v[184:185], s[14:15], v[118:119] op_sel_hi:[1,0,1]
	v_pk_fma_f32 v[120:121], v[186:187], s[14:15], v[120:121] op_sel_hi:[1,0,1]
	v_cvt_pk_f32_fp8_e32 v[188:189], v75
	v_cvt_pk_f32_fp8_sdwa v[190:191], v75 src0_sel:WORD_1
	v_pk_fma_f32 v[122:123], v[188:189], s[14:15], v[122:123] op_sel_hi:[1,0,1]
	v_pk_fma_f32 v[124:125], v[190:191], s[14:15], v[124:125] op_sel_hi:[1,0,1]
	v_readlane_b32 s14, v1, 8
	v_cvt_pk_f32_fp8_e32 v[184:185], v52
	v_cvt_pk_f32_fp8_sdwa v[186:187], v52 src0_sel:WORD_1
	v_pk_fma_f32 v[110:111], v[184:185], s[14:15], v[110:111] op_sel_hi:[1,0,1]
	v_pk_fma_f32 v[112:113], v[186:187], s[14:15], v[112:113] op_sel_hi:[1,0,1]
	v_cvt_pk_f32_fp8_e32 v[188:189], v53
	v_cvt_pk_f32_fp8_sdwa v[190:191], v53 src0_sel:WORD_1
	v_pk_fma_f32 v[114:115], v[188:189], s[14:15], v[114:115] op_sel_hi:[1,0,1]
	v_pk_fma_f32 v[116:117], v[190:191], s[14:15], v[116:117] op_sel_hi:[1,0,1]
	v_cvt_pk_f32_fp8_e32 v[184:185], v54
	v_cvt_pk_f32_fp8_sdwa v[186:187], v54 src0_sel:WORD_1
	v_pk_fma_f32 v[118:119], v[184:185], s[14:15], v[118:119] op_sel_hi:[1,0,1]
	v_pk_fma_f32 v[120:121], v[186:187], s[14:15], v[120:121] op_sel_hi:[1,0,1]
	v_cvt_pk_f32_fp8_e32 v[188:189], v55
	v_cvt_pk_f32_fp8_sdwa v[190:191], v55 src0_sel:WORD_1
	v_pk_fma_f32 v[122:123], v[188:189], s[14:15], v[122:123] op_sel_hi:[1,0,1]
	v_pk_fma_f32 v[124:125], v[190:191], s[14:15], v[124:125] op_sel_hi:[1,0,1]
	s_cmp_le_u32 s36, 2
	s_cbranch_scc1 .Lp6b1_axdone
	v_readlane_b32 s14, v1, 16
	v_cvt_pk_f32_fp8_e32 v[184:185], v44
	v_cvt_pk_f32_fp8_sdwa v[186:187], v44 src0_sel:WORD_1
	v_pk_fma_f32 v[110:111], v[184:185], s[14:15], v[110:111] op_sel_hi:[1,0,1]
	v_pk_fma_f32 v[112:113], v[186:187], s[14:15], v[112:113] op_sel_hi:[1,0,1]
	v_cvt_pk_f32_fp8_e32 v[188:189], v45
	v_cvt_pk_f32_fp8_sdwa v[190:191], v45 src0_sel:WORD_1
	v_pk_fma_f32 v[114:115], v[188:189], s[14:15], v[114:115] op_sel_hi:[1,0,1]
	v_pk_fma_f32 v[116:117], v[190:191], s[14:15], v[116:117] op_sel_hi:[1,0,1]
	v_cvt_pk_f32_fp8_e32 v[184:185], v46
	v_cvt_pk_f32_fp8_sdwa v[186:187], v46 src0_sel:WORD_1
	v_pk_fma_f32 v[118:119], v[184:185], s[14:15], v[118:119] op_sel_hi:[1,0,1]
	v_pk_fma_f32 v[120:121], v[186:187], s[14:15], v[120:121] op_sel_hi:[1,0,1]
	v_cvt_pk_f32_fp8_e32 v[188:189], v47
	v_cvt_pk_f32_fp8_sdwa v[190:191], v47 src0_sel:WORD_1
	v_pk_fma_f32 v[122:123], v[188:189], s[14:15], v[122:123] op_sel_hi:[1,0,1]
	v_pk_fma_f32 v[124:125], v[190:191], s[14:15], v[124:125] op_sel_hi:[1,0,1]
	v_readlane_b32 s14, v1, 24
	v_cvt_pk_f32_fp8_e32 v[184:185], v40
	v_cvt_pk_f32_fp8_sdwa v[186:187], v40 src0_sel:WORD_1
	v_pk_fma_f32 v[110:111], v[184:185], s[14:15], v[110:111] op_sel_hi:[1,0,1]
	v_pk_fma_f32 v[112:113], v[186:187], s[14:15], v[112:113] op_sel_hi:[1,0,1]
	v_cvt_pk_f32_fp8_e32 v[188:189], v41
	v_cvt_pk_f32_fp8_sdwa v[190:191], v41 src0_sel:WORD_1
	v_pk_fma_f32 v[114:115], v[188:189], s[14:15], v[114:115] op_sel_hi:[1,0,1]
	v_pk_fma_f32 v[116:117], v[190:191], s[14:15], v[116:117] op_sel_hi:[1,0,1]
	v_cvt_pk_f32_fp8_e32 v[184:185], v42
	v_cvt_pk_f32_fp8_sdwa v[186:187], v42 src0_sel:WORD_1
	v_pk_fma_f32 v[118:119], v[184:185], s[14:15], v[118:119] op_sel_hi:[1,0,1]
	v_pk_fma_f32 v[120:121], v[186:187], s[14:15], v[120:121] op_sel_hi:[1,0,1]
	v_cvt_pk_f32_fp8_e32 v[188:189], v43
	v_cvt_pk_f32_fp8_sdwa v[190:191], v43 src0_sel:WORD_1
	v_pk_fma_f32 v[122:123], v[188:189], s[14:15], v[122:123] op_sel_hi:[1,0,1]
	v_pk_fma_f32 v[124:125], v[190:191], s[14:15], v[124:125] op_sel_hi:[1,0,1]
	s_cmp_le_u32 s36, 4
	s_cbranch_scc1 .Lp6b1_axdone
	v_readlane_b32 s14, v1, 32
	v_cvt_pk_f32_fp8_e32 v[184:185], v36
	v_cvt_pk_f32_fp8_sdwa v[186:187], v36 src0_sel:WORD_1
	v_pk_fma_f32 v[110:111], v[184:185], s[14:15], v[110:111] op_sel_hi:[1,0,1]
	v_pk_fma_f32 v[112:113], v[186:187], s[14:15], v[112:113] op_sel_hi:[1,0,1]
	v_cvt_pk_f32_fp8_e32 v[188:189], v37
	v_cvt_pk_f32_fp8_sdwa v[190:191], v37 src0_sel:WORD_1
	v_pk_fma_f32 v[114:115], v[188:189], s[14:15], v[114:115] op_sel_hi:[1,0,1]
	v_pk_fma_f32 v[116:117], v[190:191], s[14:15], v[116:117] op_sel_hi:[1,0,1]
	v_cvt_pk_f32_fp8_e32 v[184:185], v38
	v_cvt_pk_f32_fp8_sdwa v[186:187], v38 src0_sel:WORD_1
	v_pk_fma_f32 v[118:119], v[184:185], s[14:15], v[118:119] op_sel_hi:[1,0,1]
	v_pk_fma_f32 v[120:121], v[186:187], s[14:15], v[120:121] op_sel_hi:[1,0,1]
	v_cvt_pk_f32_fp8_e32 v[188:189], v39
	v_cvt_pk_f32_fp8_sdwa v[190:191], v39 src0_sel:WORD_1
	v_pk_fma_f32 v[122:123], v[188:189], s[14:15], v[122:123] op_sel_hi:[1,0,1]
	v_pk_fma_f32 v[124:125], v[190:191], s[14:15], v[124:125] op_sel_hi:[1,0,1]
	v_readlane_b32 s14, v1, 40
	v_cvt_pk_f32_fp8_e32 v[184:185], v28
	v_cvt_pk_f32_fp8_sdwa v[186:187], v28 src0_sel:WORD_1
	v_pk_fma_f32 v[110:111], v[184:185], s[14:15], v[110:111] op_sel_hi:[1,0,1]
	v_pk_fma_f32 v[112:113], v[186:187], s[14:15], v[112:113] op_sel_hi:[1,0,1]
	v_cvt_pk_f32_fp8_e32 v[188:189], v29
	v_cvt_pk_f32_fp8_sdwa v[190:191], v29 src0_sel:WORD_1
	v_pk_fma_f32 v[114:115], v[188:189], s[14:15], v[114:115] op_sel_hi:[1,0,1]
	v_pk_fma_f32 v[116:117], v[190:191], s[14:15], v[116:117] op_sel_hi:[1,0,1]
	v_cvt_pk_f32_fp8_e32 v[184:185], v30
	v_cvt_pk_f32_fp8_sdwa v[186:187], v30 src0_sel:WORD_1
	v_pk_fma_f32 v[118:119], v[184:185], s[14:15], v[118:119] op_sel_hi:[1,0,1]
	v_pk_fma_f32 v[120:121], v[186:187], s[14:15], v[120:121] op_sel_hi:[1,0,1]
	v_cvt_pk_f32_fp8_e32 v[188:189], v31
	v_cvt_pk_f32_fp8_sdwa v[190:191], v31 src0_sel:WORD_1
	v_pk_fma_f32 v[122:123], v[188:189], s[14:15], v[122:123] op_sel_hi:[1,0,1]
	v_pk_fma_f32 v[124:125], v[190:191], s[14:15], v[124:125] op_sel_hi:[1,0,1]
	s_cmp_le_u32 s36, 6
	s_cbranch_scc1 .Lp6b1_axdone
	v_readlane_b32 s14, v1, 48
	v_cvt_pk_f32_fp8_e32 v[184:185], v24
	v_cvt_pk_f32_fp8_sdwa v[186:187], v24 src0_sel:WORD_1
	v_pk_fma_f32 v[110:111], v[184:185], s[14:15], v[110:111] op_sel_hi:[1,0,1]
	v_pk_fma_f32 v[112:113], v[186:187], s[14:15], v[112:113] op_sel_hi:[1,0,1]
	v_cvt_pk_f32_fp8_e32 v[188:189], v25
	v_cvt_pk_f32_fp8_sdwa v[190:191], v25 src0_sel:WORD_1
	v_pk_fma_f32 v[114:115], v[188:189], s[14:15], v[114:115] op_sel_hi:[1,0,1]
	v_pk_fma_f32 v[116:117], v[190:191], s[14:15], v[116:117] op_sel_hi:[1,0,1]
	v_cvt_pk_f32_fp8_e32 v[184:185], v26
	v_cvt_pk_f32_fp8_sdwa v[186:187], v26 src0_sel:WORD_1
	v_pk_fma_f32 v[118:119], v[184:185], s[14:15], v[118:119] op_sel_hi:[1,0,1]
	v_pk_fma_f32 v[120:121], v[186:187], s[14:15], v[120:121] op_sel_hi:[1,0,1]
	v_cvt_pk_f32_fp8_e32 v[188:189], v27
	v_cvt_pk_f32_fp8_sdwa v[190:191], v27 src0_sel:WORD_1
	v_pk_fma_f32 v[122:123], v[188:189], s[14:15], v[122:123] op_sel_hi:[1,0,1]
	v_pk_fma_f32 v[124:125], v[190:191], s[14:15], v[124:125] op_sel_hi:[1,0,1]
	v_readlane_b32 s14, v1, 56
	v_cvt_pk_f32_fp8_e32 v[184:185], v20
	v_cvt_pk_f32_fp8_sdwa v[186:187], v20 src0_sel:WORD_1
	v_pk_fma_f32 v[110:111], v[184:185], s[14:15], v[110:111] op_sel_hi:[1,0,1]
	v_pk_fma_f32 v[112:113], v[186:187], s[14:15], v[112:113] op_sel_hi:[1,0,1]
	v_cvt_pk_f32_fp8_e32 v[188:189], v21
	v_cvt_pk_f32_fp8_sdwa v[190:191], v21 src0_sel:WORD_1
	v_pk_fma_f32 v[114:115], v[188:189], s[14:15], v[114:115] op_sel_hi:[1,0,1]
	v_pk_fma_f32 v[116:117], v[190:191], s[14:15], v[116:117] op_sel_hi:[1,0,1]
	v_cvt_pk_f32_fp8_e32 v[184:185], v22
	v_cvt_pk_f32_fp8_sdwa v[186:187], v22 src0_sel:WORD_1
	v_pk_fma_f32 v[118:119], v[184:185], s[14:15], v[118:119] op_sel_hi:[1,0,1]
	v_pk_fma_f32 v[120:121], v[186:187], s[14:15], v[120:121] op_sel_hi:[1,0,1]
	v_cvt_pk_f32_fp8_e32 v[188:189], v23
	v_cvt_pk_f32_fp8_sdwa v[190:191], v23 src0_sel:WORD_1
	v_pk_fma_f32 v[122:123], v[188:189], s[14:15], v[122:123] op_sel_hi:[1,0,1]
	v_pk_fma_f32 v[124:125], v[190:191], s[14:15], v[124:125] op_sel_hi:[1,0,1]
	s_branch .Lp6b1_axdone
.Lp6b1_t0:
	v_readlane_b32 s14, v1, 0
	v_cvt_pk_f32_fp8_e32 v[184:185], v72
	v_cvt_pk_f32_fp8_sdwa v[186:187], v72 src0_sel:WORD_1
	v_pk_fma_f32 v[126:127], v[184:185], s[14:15], v[126:127] op_sel_hi:[1,0,1]
	v_pk_fma_f32 v[128:129], v[186:187], s[14:15], v[128:129] op_sel_hi:[1,0,1]
	v_cvt_pk_f32_fp8_e32 v[188:189], v73
	v_cvt_pk_f32_fp8_sdwa v[190:191], v73 src0_sel:WORD_1
	v_pk_fma_f32 v[130:131], v[188:189], s[14:15], v[130:131] op_sel_hi:[1,0,1]
	v_pk_fma_f32 v[132:133], v[190:191], s[14:15], v[132:133] op_sel_hi:[1,0,1]
	v_cvt_pk_f32_fp8_e32 v[184:185], v74
	v_cvt_pk_f32_fp8_sdwa v[186:187], v74 src0_sel:WORD_1
	v_pk_fma_f32 v[134:135], v[184:185], s[14:15], v[134:135] op_sel_hi:[1,0,1]
	v_pk_fma_f32 v[136:137], v[186:187], s[14:15], v[136:137] op_sel_hi:[1,0,1]
	v_cvt_pk_f32_fp8_e32 v[188:189], v75
	v_cvt_pk_f32_fp8_sdwa v[190:191], v75 src0_sel:WORD_1
	v_pk_fma_f32 v[138:139], v[188:189], s[14:15], v[138:139] op_sel_hi:[1,0,1]
	v_pk_fma_f32 v[140:141], v[190:191], s[14:15], v[140:141] op_sel_hi:[1,0,1]
	v_readlane_b32 s14, v1, 8
	v_cvt_pk_f32_fp8_e32 v[184:185], v52
	v_cvt_pk_f32_fp8_sdwa v[186:187], v52 src0_sel:WORD_1
	v_pk_fma_f32 v[126:127], v[184:185], s[14:15], v[126:127] op_sel_hi:[1,0,1]
	v_pk_fma_f32 v[128:129], v[186:187], s[14:15], v[128:129] op_sel_hi:[1,0,1]
	v_cvt_pk_f32_fp8_e32 v[188:189], v53
	v_cvt_pk_f32_fp8_sdwa v[190:191], v53 src0_sel:WORD_1
	v_pk_fma_f32 v[130:131], v[188:189], s[14:15], v[130:131] op_sel_hi:[1,0,1]
	v_pk_fma_f32 v[132:133], v[190:191], s[14:15], v[132:133] op_sel_hi:[1,0,1]
	v_cvt_pk_f32_fp8_e32 v[184:185], v54
	v_cvt_pk_f32_fp8_sdwa v[186:187], v54 src0_sel:WORD_1
	v_pk_fma_f32 v[134:135], v[184:185], s[14:15], v[134:135] op_sel_hi:[1,0,1]
	v_pk_fma_f32 v[136:137], v[186:187], s[14:15], v[136:137] op_sel_hi:[1,0,1]
	v_cvt_pk_f32_fp8_e32 v[188:189], v55
	v_cvt_pk_f32_fp8_sdwa v[190:191], v55 src0_sel:WORD_1
	v_pk_fma_f32 v[138:139], v[188:189], s[14:15], v[138:139] op_sel_hi:[1,0,1]
	v_pk_fma_f32 v[140:141], v[190:191], s[14:15], v[140:141] op_sel_hi:[1,0,1]
	s_cmp_le_u32 s36, 2
	s_cbranch_scc1 .Lp6b1_axdone
	v_readlane_b32 s14, v1, 16
	v_cvt_pk_f32_fp8_e32 v[184:185], v44
	v_cvt_pk_f32_fp8_sdwa v[186:187], v44 src0_sel:WORD_1
	v_pk_fma_f32 v[126:127], v[184:185], s[14:15], v[126:127] op_sel_hi:[1,0,1]
	v_pk_fma_f32 v[128:129], v[186:187], s[14:15], v[128:129] op_sel_hi:[1,0,1]
	v_cvt_pk_f32_fp8_e32 v[188:189], v45
	v_cvt_pk_f32_fp8_sdwa v[190:191], v45 src0_sel:WORD_1
	v_pk_fma_f32 v[130:131], v[188:189], s[14:15], v[130:131] op_sel_hi:[1,0,1]
	v_pk_fma_f32 v[132:133], v[190:191], s[14:15], v[132:133] op_sel_hi:[1,0,1]
	v_cvt_pk_f32_fp8_e32 v[184:185], v46
	v_cvt_pk_f32_fp8_sdwa v[186:187], v46 src0_sel:WORD_1
	v_pk_fma_f32 v[134:135], v[184:185], s[14:15], v[134:135] op_sel_hi:[1,0,1]
	v_pk_fma_f32 v[136:137], v[186:187], s[14:15], v[136:137] op_sel_hi:[1,0,1]
	v_cvt_pk_f32_fp8_e32 v[188:189], v47
	v_cvt_pk_f32_fp8_sdwa v[190:191], v47 src0_sel:WORD_1
	v_pk_fma_f32 v[138:139], v[188:189], s[14:15], v[138:139] op_sel_hi:[1,0,1]
	v_pk_fma_f32 v[140:141], v[190:191], s[14:15], v[140:141] op_sel_hi:[1,0,1]
	v_readlane_b32 s14, v1, 24
	v_cvt_pk_f32_fp8_e32 v[184:185], v40
	v_cvt_pk_f32_fp8_sdwa v[186:187], v40 src0_sel:WORD_1
	v_pk_fma_f32 v[126:127], v[184:185], s[14:15], v[126:127] op_sel_hi:[1,0,1]
	v_pk_fma_f32 v[128:129], v[186:187], s[14:15], v[128:129] op_sel_hi:[1,0,1]
	v_cvt_pk_f32_fp8_e32 v[188:189], v41
	v_cvt_pk_f32_fp8_sdwa v[190:191], v41 src0_sel:WORD_1
	v_pk_fma_f32 v[130:131], v[188:189], s[14:15], v[130:131] op_sel_hi:[1,0,1]
	v_pk_fma_f32 v[132:133], v[190:191], s[14:15], v[132:133] op_sel_hi:[1,0,1]
	v_cvt_pk_f32_fp8_e32 v[184:185], v42
	v_cvt_pk_f32_fp8_sdwa v[186:187], v42 src0_sel:WORD_1
	v_pk_fma_f32 v[134:135], v[184:185], s[14:15], v[134:135] op_sel_hi:[1,0,1]
	v_pk_fma_f32 v[136:137], v[186:187], s[14:15], v[136:137] op_sel_hi:[1,0,1]
	v_cvt_pk_f32_fp8_e32 v[188:189], v43
	v_cvt_pk_f32_fp8_sdwa v[190:191], v43 src0_sel:WORD_1
	v_pk_fma_f32 v[138:139], v[188:189], s[14:15], v[138:139] op_sel_hi:[1,0,1]
	v_pk_fma_f32 v[140:141], v[190:191], s[14:15], v[140:141] op_sel_hi:[1,0,1]
	s_cmp_le_u32 s36, 4
	s_cbranch_scc1 .Lp6b1_axdone
	v_readlane_b32 s14, v1, 32
	v_cvt_pk_f32_fp8_e32 v[184:185], v36
	v_cvt_pk_f32_fp8_sdwa v[186:187], v36 src0_sel:WORD_1
	v_pk_fma_f32 v[126:127], v[184:185], s[14:15], v[126:127] op_sel_hi:[1,0,1]
	v_pk_fma_f32 v[128:129], v[186:187], s[14:15], v[128:129] op_sel_hi:[1,0,1]
	v_cvt_pk_f32_fp8_e32 v[188:189], v37
	v_cvt_pk_f32_fp8_sdwa v[190:191], v37 src0_sel:WORD_1
	v_pk_fma_f32 v[130:131], v[188:189], s[14:15], v[130:131] op_sel_hi:[1,0,1]
	v_pk_fma_f32 v[132:133], v[190:191], s[14:15], v[132:133] op_sel_hi:[1,0,1]
	v_cvt_pk_f32_fp8_e32 v[184:185], v38
	v_cvt_pk_f32_fp8_sdwa v[186:187], v38 src0_sel:WORD_1
	v_pk_fma_f32 v[134:135], v[184:185], s[14:15], v[134:135] op_sel_hi:[1,0,1]
	v_pk_fma_f32 v[136:137], v[186:187], s[14:15], v[136:137] op_sel_hi:[1,0,1]
	v_cvt_pk_f32_fp8_e32 v[188:189], v39
	v_cvt_pk_f32_fp8_sdwa v[190:191], v39 src0_sel:WORD_1
	v_pk_fma_f32 v[138:139], v[188:189], s[14:15], v[138:139] op_sel_hi:[1,0,1]
	v_pk_fma_f32 v[140:141], v[190:191], s[14:15], v[140:141] op_sel_hi:[1,0,1]
	v_readlane_b32 s14, v1, 40
	v_cvt_pk_f32_fp8_e32 v[184:185], v28
	v_cvt_pk_f32_fp8_sdwa v[186:187], v28 src0_sel:WORD_1
	v_pk_fma_f32 v[126:127], v[184:185], s[14:15], v[126:127] op_sel_hi:[1,0,1]
	v_pk_fma_f32 v[128:129], v[186:187], s[14:15], v[128:129] op_sel_hi:[1,0,1]
	v_cvt_pk_f32_fp8_e32 v[188:189], v29
	v_cvt_pk_f32_fp8_sdwa v[190:191], v29 src0_sel:WORD_1
	v_pk_fma_f32 v[130:131], v[188:189], s[14:15], v[130:131] op_sel_hi:[1,0,1]
	v_pk_fma_f32 v[132:133], v[190:191], s[14:15], v[132:133] op_sel_hi:[1,0,1]
	v_cvt_pk_f32_fp8_e32 v[184:185], v30
	v_cvt_pk_f32_fp8_sdwa v[186:187], v30 src0_sel:WORD_1
	v_pk_fma_f32 v[134:135], v[184:185], s[14:15], v[134:135] op_sel_hi:[1,0,1]
	v_pk_fma_f32 v[136:137], v[186:187], s[14:15], v[136:137] op_sel_hi:[1,0,1]
	v_cvt_pk_f32_fp8_e32 v[188:189], v31
	v_cvt_pk_f32_fp8_sdwa v[190:191], v31 src0_sel:WORD_1
	v_pk_fma_f32 v[138:139], v[188:189], s[14:15], v[138:139] op_sel_hi:[1,0,1]
	v_pk_fma_f32 v[140:141], v[190:191], s[14:15], v[140:141] op_sel_hi:[1,0,1]
	s_cmp_le_u32 s36, 6
	s_cbranch_scc1 .Lp6b1_axdone
	v_readlane_b32 s14, v1, 48
	v_cvt_pk_f32_fp8_e32 v[184:185], v24
	v_cvt_pk_f32_fp8_sdwa v[186:187], v24 src0_sel:WORD_1
	v_pk_fma_f32 v[126:127], v[184:185], s[14:15], v[126:127] op_sel_hi:[1,0,1]
	v_pk_fma_f32 v[128:129], v[186:187], s[14:15], v[128:129] op_sel_hi:[1,0,1]
	v_cvt_pk_f32_fp8_e32 v[188:189], v25
	v_cvt_pk_f32_fp8_sdwa v[190:191], v25 src0_sel:WORD_1
	v_pk_fma_f32 v[130:131], v[188:189], s[14:15], v[130:131] op_sel_hi:[1,0,1]
	v_pk_fma_f32 v[132:133], v[190:191], s[14:15], v[132:133] op_sel_hi:[1,0,1]
	v_cvt_pk_f32_fp8_e32 v[184:185], v26
	v_cvt_pk_f32_fp8_sdwa v[186:187], v26 src0_sel:WORD_1
	v_pk_fma_f32 v[134:135], v[184:185], s[14:15], v[134:135] op_sel_hi:[1,0,1]
	v_pk_fma_f32 v[136:137], v[186:187], s[14:15], v[136:137] op_sel_hi:[1,0,1]
	v_cvt_pk_f32_fp8_e32 v[188:189], v27
	v_cvt_pk_f32_fp8_sdwa v[190:191], v27 src0_sel:WORD_1
	v_pk_fma_f32 v[138:139], v[188:189], s[14:15], v[138:139] op_sel_hi:[1,0,1]
	v_pk_fma_f32 v[140:141], v[190:191], s[14:15], v[140:141] op_sel_hi:[1,0,1]
	v_readlane_b32 s14, v1, 56
	v_cvt_pk_f32_fp8_e32 v[184:185], v20
	v_cvt_pk_f32_fp8_sdwa v[186:187], v20 src0_sel:WORD_1
	v_pk_fma_f32 v[126:127], v[184:185], s[14:15], v[126:127] op_sel_hi:[1,0,1]
	v_pk_fma_f32 v[128:129], v[186:187], s[14:15], v[128:129] op_sel_hi:[1,0,1]
	v_cvt_pk_f32_fp8_e32 v[188:189], v21
	v_cvt_pk_f32_fp8_sdwa v[190:191], v21 src0_sel:WORD_1
	v_pk_fma_f32 v[130:131], v[188:189], s[14:15], v[130:131] op_sel_hi:[1,0,1]
	v_pk_fma_f32 v[132:133], v[190:191], s[14:15], v[132:133] op_sel_hi:[1,0,1]
	v_cvt_pk_f32_fp8_e32 v[184:185], v22
	v_cvt_pk_f32_fp8_sdwa v[186:187], v22 src0_sel:WORD_1
	v_pk_fma_f32 v[134:135], v[184:185], s[14:15], v[134:135] op_sel_hi:[1,0,1]
	v_pk_fma_f32 v[136:137], v[186:187], s[14:15], v[136:137] op_sel_hi:[1,0,1]
	v_cvt_pk_f32_fp8_e32 v[188:189], v23
	v_cvt_pk_f32_fp8_sdwa v[190:191], v23 src0_sel:WORD_1
	v_pk_fma_f32 v[138:139], v[188:189], s[14:15], v[138:139] op_sel_hi:[1,0,1]
	v_pk_fma_f32 v[140:141], v[190:191], s[14:15], v[140:141] op_sel_hi:[1,0,1]
.Lp6b1_axdone:
	s_nop 4
	buffer_load_dwordx4 v[72:75], v181, s[92:95], s44 offen
	buffer_load_dwordx4 v[52:55], v181, s[92:95], s45 offen
	buffer_load_dwordx4 v[44:47], v181, s[92:95], s46 offen
	buffer_load_dwordx4 v[40:43], v181, s[92:95], s47 offen
	buffer_load_dwordx4 v[36:39], v181, s[92:95], s48 offen
	buffer_load_dwordx4 v[28:31], v181, s[92:95], s49 offen
	buffer_load_dwordx4 v[24:27], v181, s[92:95], s50 offen
	buffer_load_dwordx4 v[20:23], v181, s[92:95], s51 offen
	s_mov_b32 s26, s86
	s_mov_b32 s86, s27
	s_mov_b32 s27, s32
	s_cmp_eq_u32 s22, s23
	s_cbranch_scc1 .LBB0_973
.Lp6b2_top:
	s_add_i32 s23, s23, 1
	s_add_i32 s2, s23, 2
	s_add_i32 s3, s22, -1
	s_min_i32 s2, s2, s3
	s_lshl_b32 s2, s2, 2
	s_add_i32 s2, s85, s2
	v_mov_b32_e32 v1, s2
	ds_read_b32 v1, v1 offset:4864
	s_waitcnt lgkmcnt(0)
	v_readfirstlane_b32 s32, v1
	s_and_b32 s2, s32, 0x3ff
	s_bfe_u32 s3, s32, 0x4000a
	v_cmp_gt_u32_e32 vcc, s3, v182
	s_lshl_b32 s2, s2, 2
	s_add_i32 s2, s2, s85
	v_cndmask_b32_e32 v1, 0, v182, vcc
	v_lshl_add_u32 v1, v1, 2, s2
	ds_read_b32 v1, v1 offset:8192
	s_waitcnt lgkmcnt(0)
	v_lshlrev_b32_e32 v1, 10, v1
	v_and_b32_e32 v1, 0x3fffc00, v1
	s_nop 0
	v_readlane_b32 s44, v1, 0
	v_readlane_b32 s45, v1, 1
	v_readlane_b32 s46, v1, 2
	v_readlane_b32 s47, v1, 3
	v_readlane_b32 s48, v1, 4
	v_readlane_b32 s49, v1, 5
	v_readlane_b32 s50, v1, 6
	v_readlane_b32 s51, v1, 7
	s_bfe_u32 s14, s26, 0x4000a
	v_cmp_gt_u32_e32 vcc, s14, v180
	v_mov_b32_e32 v1, 0
	s_and_b32 s2, s26, 0x3ff
	s_lshr_b32 s66, s26, 14
	s_and_saveexec_b64 s[14:15], vcc
	v_add_u32_e32 v2, s2, v180
	v_lshl_add_u32 v2, v2, 2, s85
	ds_read_b32 v1, v2 offset:12288
	s_or_b64 exec, exec, s[14:15]
	s_waitcnt vmcnt(16)
	s_waitcnt lgkmcnt(0)
	s_bfe_u32 s36, s26, 0x4000a
	s_cmp_lt_i32 s66, 1
	s_cbranch_scc1 .Lp6b2_t0
	s_cmp_lt_i32 s66, 2
	s_cbranch_scc1 .Lp6b2_t1
	s_cmp_lg_u32 s66, 2
	s_cbranch_scc0 .Lp6b2_t2
	v_readlane_b32 s14, v1, 0
	v_cvt_pk_f32_fp8_e32 v[184:185], v224
	v_cvt_pk_f32_fp8_sdwa v[186:187], v224 src0_sel:WORD_1
	v_pk_fma_f32 v[78:79], v[184:185], s[14:15], v[78:79] op_sel_hi:[1,0,1]
	v_pk_fma_f32 v[80:81], v[186:187], s[14:15], v[80:81] op_sel_hi:[1,0,1]
	v_cvt_pk_f32_fp8_e32 v[188:189], v225
	v_cvt_pk_f32_fp8_sdwa v[190:191], v225 src0_sel:WORD_1
	v_pk_fma_f32 v[82:83], v[188:189], s[14:15], v[82:83] op_sel_hi:[1,0,1]
	v_pk_fma_f32 v[86:87], v[190:191], s[14:15], v[86:87] op_sel_hi:[1,0,1]
	v_cvt_pk_f32_fp8_e32 v[184:185], v226
	v_cvt_pk_f32_fp8_sdwa v[186:187], v226 src0_sel:WORD_1
	v_pk_fma_f32 v[88:89], v[184:185], s[14:15], v[88:89] op_sel_hi:[1,0,1]
	v_pk_fma_f32 v[90:91], v[186:187], s[14:15], v[90:91] op_sel_hi:[1,0,1]
	v_cvt_pk_f32_fp8_e32 v[188:189], v227
	v_cvt_pk_f32_fp8_sdwa v[190:191], v227 src0_sel:WORD_1
	v_pk_fma_f32 v[92:93], v[188:189], s[14:15], v[92:93] op_sel_hi:[1,0,1]
	v_pk_fma_f32 v[84:85], v[190:191], s[14:15], v[84:85] op_sel_hi:[1,0,1]
	v_readlane_b32 s14, v1, 8
	v_cvt_pk_f32_fp8_e32 v[184:185], v228
	v_cvt_pk_f32_fp8_sdwa v[186:187], v228 src0_sel:WORD_1
	v_pk_fma_f32 v[78:79], v[184:185], s[14:15], v[78:79] op_sel_hi:[1,0,1]
	v_pk_fma_f32 v[80:81], v[186:187], s[14:15], v[80:81] op_sel_hi:[1,0,1]
	v_cvt_pk_f32_fp8_e32 v[188:189], v229
	v_cvt_pk_f32_fp8_sdwa v[190:191], v229 src0_sel:WORD_1
	v_pk_fma_f32 v[82:83], v[188:189], s[14:15], v[82:83] op_sel_hi:[1,0,1]
	v_pk_fma_f32 v[86:87], v[190:191], s[14:15], v[86:87] op_sel_hi:[1,0,1]
	v_cvt_pk_f32_fp8_e32 v[184:185], v230
	v_cvt_pk_f32_fp8_sdwa v[186:187], v230 src0_sel:WORD_1
	v_pk_fma_f32 v[88:89], v[184:185], s[14:15], v[88:89] op_sel_hi:[1,0,1]
	v_pk_fma_f32 v[90:91], v[186:187], s[14:15], v[90:91] op_sel_hi:[1,0,1]
	v_cvt_pk_f32_fp8_e32 v[188:189], v231
	v_cvt_pk_f32_fp8_sdwa v[190:191], v231 src0_sel:WORD_1
	v_pk_fma_f32 v[92:93], v[188:189], s[14:15], v[92:93] op_sel_hi:[1,0,1]
	v_pk_fma_f32 v[84:85], v[190:191], s[14:15], v[84:85] op_sel_hi:[1,0,1]
	s_cmp_le_u32 s36, 2
	s_cbranch_scc1 .Lp6b2_axdone
	v_readlane_b32 s14, v1, 16
	v_cvt_pk_f32_fp8_e32 v[184:185], v232
	v_cvt_pk_f32_fp8_sdwa v[186:187], v232 src0_sel:WORD_1
	v_pk_fma_f32 v[78:79], v[184:185], s[14:15], v[78:79] op_sel_hi:[1,0,1]
	v_pk_fma_f32 v[80:81], v[186:187], s[14:15], v[80:81] op_sel_hi:[1,0,1]
	v_cvt_pk_f32_fp8_e32 v[188:189], v233
	v_cvt_pk_f32_fp8_sdwa v[190:191], v233 src0_sel:WORD_1
	v_pk_fma_f32 v[82:83], v[188:189], s[14:15], v[82:83] op_sel_hi:[1,0,1]
	v_pk_fma_f32 v[86:87], v[190:191], s[14:15], v[86:87] op_sel_hi:[1,0,1]
	v_cvt_pk_f32_fp8_e32 v[184:185], v234
	v_cvt_pk_f32_fp8_sdwa v[186:187], v234 src0_sel:WORD_1
	v_pk_fma_f32 v[88:89], v[184:185], s[14:15], v[88:89] op_sel_hi:[1,0,1]
	v_pk_fma_f32 v[90:91], v[186:187], s[14:15], v[90:91] op_sel_hi:[1,0,1]
	v_cvt_pk_f32_fp8_e32 v[188:189], v235
	v_cvt_pk_f32_fp8_sdwa v[190:191], v235 src0_sel:WORD_1
	v_pk_fma_f32 v[92:93], v[188:189], s[14:15], v[92:93] op_sel_hi:[1,0,1]
	v_pk_fma_f32 v[84:85], v[190:191], s[14:15], v[84:85] op_sel_hi:[1,0,1]
	v_readlane_b32 s14, v1, 24
	v_cvt_pk_f32_fp8_e32 v[184:185], v236
	v_cvt_pk_f32_fp8_sdwa v[186:187], v236 src0_sel:WORD_1
	v_pk_fma_f32 v[78:79], v[184:185], s[14:15], v[78:79] op_sel_hi:[1,0,1]
	v_pk_fma_f32 v[80:81], v[186:187], s[14:15], v[80:81] op_sel_hi:[1,0,1]
	v_cvt_pk_f32_fp8_e32 v[188:189], v237
	v_cvt_pk_f32_fp8_sdwa v[190:191], v237 src0_sel:WORD_1
	v_pk_fma_f32 v[82:83], v[188:189], s[14:15], v[82:83] op_sel_hi:[1,0,1]
	v_pk_fma_f32 v[86:87], v[190:191], s[14:15], v[86:87] op_sel_hi:[1,0,1]
	v_cvt_pk_f32_fp8_e32 v[184:185], v238
	v_cvt_pk_f32_fp8_sdwa v[186:187], v238 src0_sel:WORD_1
	v_pk_fma_f32 v[88:89], v[184:185], s[14:15], v[88:89] op_sel_hi:[1,0,1]
	v_pk_fma_f32 v[90:91], v[186:187], s[14:15], v[90:91] op_sel_hi:[1,0,1]
	v_cvt_pk_f32_fp8_e32 v[188:189], v239
	v_cvt_pk_f32_fp8_sdwa v[190:191], v239 src0_sel:WORD_1
	v_pk_fma_f32 v[92:93], v[188:189], s[14:15], v[92:93] op_sel_hi:[1,0,1]
	v_pk_fma_f32 v[84:85], v[190:191], s[14:15], v[84:85] op_sel_hi:[1,0,1]
	s_cmp_le_u32 s36, 4
	s_cbranch_scc1 .Lp6b2_axdone
	v_readlane_b32 s14, v1, 32
	v_cvt_pk_f32_fp8_e32 v[184:185], v240
	v_cvt_pk_f32_fp8_sdwa v[186:187], v240 src0_sel:WORD_1
	v_pk_fma_f32 v[78:79], v[184:185], s[14:15], v[78:79] op_sel_hi:[1,0,1]
	v_pk_fma_f32 v[80:81], v[186:187], s[14:15], v[80:81] op_sel_hi:[1,0,1]
	v_cvt_pk_f32_fp8_e32 v[188:189], v241
	v_cvt_pk_f32_fp8_sdwa v[190:191], v241 src0_sel:WORD_1
	v_pk_fma_f32 v[82:83], v[188:189], s[14:15], v[82:83] op_sel_hi:[1,0,1]
	v_pk_fma_f32 v[86:87], v[190:191], s[14:15], v[86:87] op_sel_hi:[1,0,1]
	v_cvt_pk_f32_fp8_e32 v[184:185], v242
	v_cvt_pk_f32_fp8_sdwa v[186:187], v242 src0_sel:WORD_1
	v_pk_fma_f32 v[88:89], v[184:185], s[14:15], v[88:89] op_sel_hi:[1,0,1]
	v_pk_fma_f32 v[90:91], v[186:187], s[14:15], v[90:91] op_sel_hi:[1,0,1]
	v_cvt_pk_f32_fp8_e32 v[188:189], v243
	v_cvt_pk_f32_fp8_sdwa v[190:191], v243 src0_sel:WORD_1
	v_pk_fma_f32 v[92:93], v[188:189], s[14:15], v[92:93] op_sel_hi:[1,0,1]
	v_pk_fma_f32 v[84:85], v[190:191], s[14:15], v[84:85] op_sel_hi:[1,0,1]
	v_readlane_b32 s14, v1, 40
	v_cvt_pk_f32_fp8_e32 v[184:185], v244
	v_cvt_pk_f32_fp8_sdwa v[186:187], v244 src0_sel:WORD_1
	v_pk_fma_f32 v[78:79], v[184:185], s[14:15], v[78:79] op_sel_hi:[1,0,1]
	v_pk_fma_f32 v[80:81], v[186:187], s[14:15], v[80:81] op_sel_hi:[1,0,1]
	v_cvt_pk_f32_fp8_e32 v[188:189], v245
	v_cvt_pk_f32_fp8_sdwa v[190:191], v245 src0_sel:WORD_1
	v_pk_fma_f32 v[82:83], v[188:189], s[14:15], v[82:83] op_sel_hi:[1,0,1]
	v_pk_fma_f32 v[86:87], v[190:191], s[14:15], v[86:87] op_sel_hi:[1,0,1]
	v_cvt_pk_f32_fp8_e32 v[184:185], v246
	v_cvt_pk_f32_fp8_sdwa v[186:187], v246 src0_sel:WORD_1
	v_pk_fma_f32 v[88:89], v[184:185], s[14:15], v[88:89] op_sel_hi:[1,0,1]
	v_pk_fma_f32 v[90:91], v[186:187], s[14:15], v[90:91] op_sel_hi:[1,0,1]
	v_cvt_pk_f32_fp8_e32 v[188:189], v247
	v_cvt_pk_f32_fp8_sdwa v[190:191], v247 src0_sel:WORD_1
	v_pk_fma_f32 v[92:93], v[188:189], s[14:15], v[92:93] op_sel_hi:[1,0,1]
	v_pk_fma_f32 v[84:85], v[190:191], s[14:15], v[84:85] op_sel_hi:[1,0,1]
	s_cmp_le_u32 s36, 6
	s_cbranch_scc1 .Lp6b2_axdone
	v_readlane_b32 s14, v1, 48
	v_cvt_pk_f32_fp8_e32 v[184:185], v248
	v_cvt_pk_f32_fp8_sdwa v[186:187], v248 src0_sel:WORD_1
	v_pk_fma_f32 v[78:79], v[184:185], s[14:15], v[78:79] op_sel_hi:[1,0,1]
	v_pk_fma_f32 v[80:81], v[186:187], s[14:15], v[80:81] op_sel_hi:[1,0,1]
	v_cvt_pk_f32_fp8_e32 v[188:189], v249
	v_cvt_pk_f32_fp8_sdwa v[190:191], v249 src0_sel:WORD_1
	v_pk_fma_f32 v[82:83], v[188:189], s[14:15], v[82:83] op_sel_hi:[1,0,1]
	v_pk_fma_f32 v[86:87], v[190:191], s[14:15], v[86:87] op_sel_hi:[1,0,1]
	v_cvt_pk_f32_fp8_e32 v[184:185], v250
	v_cvt_pk_f32_fp8_sdwa v[186:187], v250 src0_sel:WORD_1
	v_pk_fma_f32 v[88:89], v[184:185], s[14:15], v[88:89] op_sel_hi:[1,0,1]
	v_pk_fma_f32 v[90:91], v[186:187], s[14:15], v[90:91] op_sel_hi:[1,0,1]
	v_cvt_pk_f32_fp8_e32 v[188:189], v251
	v_cvt_pk_f32_fp8_sdwa v[190:191], v251 src0_sel:WORD_1
	v_pk_fma_f32 v[92:93], v[188:189], s[14:15], v[92:93] op_sel_hi:[1,0,1]
	v_pk_fma_f32 v[84:85], v[190:191], s[14:15], v[84:85] op_sel_hi:[1,0,1]
	v_readlane_b32 s14, v1, 56
	v_cvt_pk_f32_fp8_e32 v[184:185], v216
	v_cvt_pk_f32_fp8_sdwa v[186:187], v216 src0_sel:WORD_1
	v_pk_fma_f32 v[78:79], v[184:185], s[14:15], v[78:79] op_sel_hi:[1,0,1]
	v_pk_fma_f32 v[80:81], v[186:187], s[14:15], v[80:81] op_sel_hi:[1,0,1]
	v_cvt_pk_f32_fp8_e32 v[188:189], v217
	v_cvt_pk_f32_fp8_sdwa v[190:191], v217 src0_sel:WORD_1
	v_pk_fma_f32 v[82:83], v[188:189], s[14:15], v[82:83] op_sel_hi:[1,0,1]
	v_pk_fma_f32 v[86:87], v[190:191], s[14:15], v[86:87] op_sel_hi:[1,0,1]
	v_cvt_pk_f32_fp8_e32 v[184:185], v218
	v_cvt_pk_f32_fp8_sdwa v[186:187], v218 src0_sel:WORD_1
	v_pk_fma_f32 v[88:89], v[184:185], s[14:15], v[88:89] op_sel_hi:[1,0,1]
	v_pk_fma_f32 v[90:91], v[186:187], s[14:15], v[90:91] op_sel_hi:[1,0,1]
	v_cvt_pk_f32_fp8_e32 v[188:189], v219
	v_cvt_pk_f32_fp8_sdwa v[190:191], v219 src0_sel:WORD_1
	v_pk_fma_f32 v[92:93], v[188:189], s[14:15], v[92:93] op_sel_hi:[1,0,1]
	v_pk_fma_f32 v[84:85], v[190:191], s[14:15], v[84:85] op_sel_hi:[1,0,1]
	s_branch .Lp6b2_axdone
.Lp6b2_t2:
	v_readlane_b32 s14, v1, 0
	v_cvt_pk_f32_fp8_e32 v[184:185], v224
	v_cvt_pk_f32_fp8_sdwa v[186:187], v224 src0_sel:WORD_1
	v_pk_fma_f32 v[94:95], v[184:185], s[14:15], v[94:95] op_sel_hi:[1,0,1]
	v_pk_fma_f32 v[96:97], v[186:187], s[14:15], v[96:97] op_sel_hi:[1,0,1]
	v_cvt_pk_f32_fp8_e32 v[188:189], v225
	v_cvt_pk_f32_fp8_sdwa v[190:191], v225 src0_sel:WORD_1
	v_pk_fma_f32 v[98:99], v[188:189], s[14:15], v[98:99] op_sel_hi:[1,0,1]
	v_pk_fma_f32 v[100:101], v[190:191], s[14:15], v[100:101] op_sel_hi:[1,0,1]
	v_cvt_pk_f32_fp8_e32 v[184:185], v226
	v_cvt_pk_f32_fp8_sdwa v[186:187], v226 src0_sel:WORD_1
	v_pk_fma_f32 v[102:103], v[184:185], s[14:15], v[102:103] op_sel_hi:[1,0,1]
	v_pk_fma_f32 v[104:105], v[186:187], s[14:15], v[104:105] op_sel_hi:[1,0,1]
	v_cvt_pk_f32_fp8_e32 v[188:189], v227
	v_cvt_pk_f32_fp8_sdwa v[190:191], v227 src0_sel:WORD_1
	v_pk_fma_f32 v[106:107], v[188:189], s[14:15], v[106:107] op_sel_hi:[1,0,1]
	v_pk_fma_f32 v[108:109], v[190:191], s[14:15], v[108:109] op_sel_hi:[1,0,1]
	v_readlane_b32 s14, v1, 8
	v_cvt_pk_f32_fp8_e32 v[184:185], v228
	v_cvt_pk_f32_fp8_sdwa v[186:187], v228 src0_sel:WORD_1
	v_pk_fma_f32 v[94:95], v[184:185], s[14:15], v[94:95] op_sel_hi:[1,0,1]
	v_pk_fma_f32 v[96:97], v[186:187], s[14:15], v[96:97] op_sel_hi:[1,0,1]
	v_cvt_pk_f32_fp8_e32 v[188:189], v229
	v_cvt_pk_f32_fp8_sdwa v[190:191], v229 src0_sel:WORD_1
	v_pk_fma_f32 v[98:99], v[188:189], s[14:15], v[98:99] op_sel_hi:[1,0,1]
	v_pk_fma_f32 v[100:101], v[190:191], s[14:15], v[100:101] op_sel_hi:[1,0,1]
	v_cvt_pk_f32_fp8_e32 v[184:185], v230
	v_cvt_pk_f32_fp8_sdwa v[186:187], v230 src0_sel:WORD_1
	v_pk_fma_f32 v[102:103], v[184:185], s[14:15], v[102:103] op_sel_hi:[1,0,1]
	v_pk_fma_f32 v[104:105], v[186:187], s[14:15], v[104:105] op_sel_hi:[1,0,1]
	v_cvt_pk_f32_fp8_e32 v[188:189], v231
	v_cvt_pk_f32_fp8_sdwa v[190:191], v231 src0_sel:WORD_1
	v_pk_fma_f32 v[106:107], v[188:189], s[14:15], v[106:107] op_sel_hi:[1,0,1]
	v_pk_fma_f32 v[108:109], v[190:191], s[14:15], v[108:109] op_sel_hi:[1,0,1]
	s_cmp_le_u32 s36, 2
	s_cbranch_scc1 .Lp6b2_axdone
	v_readlane_b32 s14, v1, 16
	v_cvt_pk_f32_fp8_e32 v[184:185], v232
	v_cvt_pk_f32_fp8_sdwa v[186:187], v232 src0_sel:WORD_1
	v_pk_fma_f32 v[94:95], v[184:185], s[14:15], v[94:95] op_sel_hi:[1,0,1]
	v_pk_fma_f32 v[96:97], v[186:187], s[14:15], v[96:97] op_sel_hi:[1,0,1]
	v_cvt_pk_f32_fp8_e32 v[188:189], v233
	v_cvt_pk_f32_fp8_sdwa v[190:191], v233 src0_sel:WORD_1
	v_pk_fma_f32 v[98:99], v[188:189], s[14:15], v[98:99] op_sel_hi:[1,0,1]
	v_pk_fma_f32 v[100:101], v[190:191], s[14:15], v[100:101] op_sel_hi:[1,0,1]
	v_cvt_pk_f32_fp8_e32 v[184:185], v234
	v_cvt_pk_f32_fp8_sdwa v[186:187], v234 src0_sel:WORD_1
	v_pk_fma_f32 v[102:103], v[184:185], s[14:15], v[102:103] op_sel_hi:[1,0,1]
	v_pk_fma_f32 v[104:105], v[186:187], s[14:15], v[104:105] op_sel_hi:[1,0,1]
	v_cvt_pk_f32_fp8_e32 v[188:189], v235
	v_cvt_pk_f32_fp8_sdwa v[190:191], v235 src0_sel:WORD_1
	v_pk_fma_f32 v[106:107], v[188:189], s[14:15], v[106:107] op_sel_hi:[1,0,1]
	v_pk_fma_f32 v[108:109], v[190:191], s[14:15], v[108:109] op_sel_hi:[1,0,1]
	v_readlane_b32 s14, v1, 24
	v_cvt_pk_f32_fp8_e32 v[184:185], v236
	v_cvt_pk_f32_fp8_sdwa v[186:187], v236 src0_sel:WORD_1
	v_pk_fma_f32 v[94:95], v[184:185], s[14:15], v[94:95] op_sel_hi:[1,0,1]
	v_pk_fma_f32 v[96:97], v[186:187], s[14:15], v[96:97] op_sel_hi:[1,0,1]
	v_cvt_pk_f32_fp8_e32 v[188:189], v237
	v_cvt_pk_f32_fp8_sdwa v[190:191], v237 src0_sel:WORD_1
	v_pk_fma_f32 v[98:99], v[188:189], s[14:15], v[98:99] op_sel_hi:[1,0,1]
	v_pk_fma_f32 v[100:101], v[190:191], s[14:15], v[100:101] op_sel_hi:[1,0,1]
	v_cvt_pk_f32_fp8_e32 v[184:185], v238
	v_cvt_pk_f32_fp8_sdwa v[186:187], v238 src0_sel:WORD_1
	v_pk_fma_f32 v[102:103], v[184:185], s[14:15], v[102:103] op_sel_hi:[1,0,1]
	v_pk_fma_f32 v[104:105], v[186:187], s[14:15], v[104:105] op_sel_hi:[1,0,1]
	v_cvt_pk_f32_fp8_e32 v[188:189], v239
	v_cvt_pk_f32_fp8_sdwa v[190:191], v239 src0_sel:WORD_1
	v_pk_fma_f32 v[106:107], v[188:189], s[14:15], v[106:107] op_sel_hi:[1,0,1]
	v_pk_fma_f32 v[108:109], v[190:191], s[14:15], v[108:109] op_sel_hi:[1,0,1]
	s_cmp_le_u32 s36, 4
	s_cbranch_scc1 .Lp6b2_axdone
	v_readlane_b32 s14, v1, 32
	v_cvt_pk_f32_fp8_e32 v[184:185], v240
	v_cvt_pk_f32_fp8_sdwa v[186:187], v240 src0_sel:WORD_1
	v_pk_fma_f32 v[94:95], v[184:185], s[14:15], v[94:95] op_sel_hi:[1,0,1]
	v_pk_fma_f32 v[96:97], v[186:187], s[14:15], v[96:97] op_sel_hi:[1,0,1]
	v_cvt_pk_f32_fp8_e32 v[188:189], v241
	v_cvt_pk_f32_fp8_sdwa v[190:191], v241 src0_sel:WORD_1
	v_pk_fma_f32 v[98:99], v[188:189], s[14:15], v[98:99] op_sel_hi:[1,0,1]
	v_pk_fma_f32 v[100:101], v[190:191], s[14:15], v[100:101] op_sel_hi:[1,0,1]
	v_cvt_pk_f32_fp8_e32 v[184:185], v242
	v_cvt_pk_f32_fp8_sdwa v[186:187], v242 src0_sel:WORD_1
	v_pk_fma_f32 v[102:103], v[184:185], s[14:15], v[102:103] op_sel_hi:[1,0,1]
	v_pk_fma_f32 v[104:105], v[186:187], s[14:15], v[104:105] op_sel_hi:[1,0,1]
	v_cvt_pk_f32_fp8_e32 v[188:189], v243
	v_cvt_pk_f32_fp8_sdwa v[190:191], v243 src0_sel:WORD_1
	v_pk_fma_f32 v[106:107], v[188:189], s[14:15], v[106:107] op_sel_hi:[1,0,1]
	v_pk_fma_f32 v[108:109], v[190:191], s[14:15], v[108:109] op_sel_hi:[1,0,1]
	v_readlane_b32 s14, v1, 40
	v_cvt_pk_f32_fp8_e32 v[184:185], v244
	v_cvt_pk_f32_fp8_sdwa v[186:187], v244 src0_sel:WORD_1
	v_pk_fma_f32 v[94:95], v[184:185], s[14:15], v[94:95] op_sel_hi:[1,0,1]
	v_pk_fma_f32 v[96:97], v[186:187], s[14:15], v[96:97] op_sel_hi:[1,0,1]
	v_cvt_pk_f32_fp8_e32 v[188:189], v245
	v_cvt_pk_f32_fp8_sdwa v[190:191], v245 src0_sel:WORD_1
	v_pk_fma_f32 v[98:99], v[188:189], s[14:15], v[98:99] op_sel_hi:[1,0,1]
	v_pk_fma_f32 v[100:101], v[190:191], s[14:15], v[100:101] op_sel_hi:[1,0,1]
	v_cvt_pk_f32_fp8_e32 v[184:185], v246
	v_cvt_pk_f32_fp8_sdwa v[186:187], v246 src0_sel:WORD_1
	v_pk_fma_f32 v[102:103], v[184:185], s[14:15], v[102:103] op_sel_hi:[1,0,1]
	v_pk_fma_f32 v[104:105], v[186:187], s[14:15], v[104:105] op_sel_hi:[1,0,1]
	v_cvt_pk_f32_fp8_e32 v[188:189], v247
	v_cvt_pk_f32_fp8_sdwa v[190:191], v247 src0_sel:WORD_1
	v_pk_fma_f32 v[106:107], v[188:189], s[14:15], v[106:107] op_sel_hi:[1,0,1]
	v_pk_fma_f32 v[108:109], v[190:191], s[14:15], v[108:109] op_sel_hi:[1,0,1]
	s_cmp_le_u32 s36, 6
	s_cbranch_scc1 .Lp6b2_axdone
	v_readlane_b32 s14, v1, 48
	v_cvt_pk_f32_fp8_e32 v[184:185], v248
	v_cvt_pk_f32_fp8_sdwa v[186:187], v248 src0_sel:WORD_1
	v_pk_fma_f32 v[94:95], v[184:185], s[14:15], v[94:95] op_sel_hi:[1,0,1]
	v_pk_fma_f32 v[96:97], v[186:187], s[14:15], v[96:97] op_sel_hi:[1,0,1]
	v_cvt_pk_f32_fp8_e32 v[188:189], v249
	v_cvt_pk_f32_fp8_sdwa v[190:191], v249 src0_sel:WORD_1
	v_pk_fma_f32 v[98:99], v[188:189], s[14:15], v[98:99] op_sel_hi:[1,0,1]
	v_pk_fma_f32 v[100:101], v[190:191], s[14:15], v[100:101] op_sel_hi:[1,0,1]
	v_cvt_pk_f32_fp8_e32 v[184:185], v250
	v_cvt_pk_f32_fp8_sdwa v[186:187], v250 src0_sel:WORD_1
	v_pk_fma_f32 v[102:103], v[184:185], s[14:15], v[102:103] op_sel_hi:[1,0,1]
	v_pk_fma_f32 v[104:105], v[186:187], s[14:15], v[104:105] op_sel_hi:[1,0,1]
	v_cvt_pk_f32_fp8_e32 v[188:189], v251
	v_cvt_pk_f32_fp8_sdwa v[190:191], v251 src0_sel:WORD_1
	v_pk_fma_f32 v[106:107], v[188:189], s[14:15], v[106:107] op_sel_hi:[1,0,1]
	v_pk_fma_f32 v[108:109], v[190:191], s[14:15], v[108:109] op_sel_hi:[1,0,1]
	v_readlane_b32 s14, v1, 56
	v_cvt_pk_f32_fp8_e32 v[184:185], v216
	v_cvt_pk_f32_fp8_sdwa v[186:187], v216 src0_sel:WORD_1
	v_pk_fma_f32 v[94:95], v[184:185], s[14:15], v[94:95] op_sel_hi:[1,0,1]
	v_pk_fma_f32 v[96:97], v[186:187], s[14:15], v[96:97] op_sel_hi:[1,0,1]
	v_cvt_pk_f32_fp8_e32 v[188:189], v217
	v_cvt_pk_f32_fp8_sdwa v[190:191], v217 src0_sel:WORD_1
	v_pk_fma_f32 v[98:99], v[188:189], s[14:15], v[98:99] op_sel_hi:[1,0,1]
	v_pk_fma_f32 v[100:101], v[190:191], s[14:15], v[100:101] op_sel_hi:[1,0,1]
	v_cvt_pk_f32_fp8_e32 v[184:185], v218
	v_cvt_pk_f32_fp8_sdwa v[186:187], v218 src0_sel:WORD_1
	v_pk_fma_f32 v[102:103], v[184:185], s[14:15], v[102:103] op_sel_hi:[1,0,1]
	v_pk_fma_f32 v[104:105], v[186:187], s[14:15], v[104:105] op_sel_hi:[1,0,1]
	v_cvt_pk_f32_fp8_e32 v[188:189], v219
	v_cvt_pk_f32_fp8_sdwa v[190:191], v219 src0_sel:WORD_1
	v_pk_fma_f32 v[106:107], v[188:189], s[14:15], v[106:107] op_sel_hi:[1,0,1]
	v_pk_fma_f32 v[108:109], v[190:191], s[14:15], v[108:109] op_sel_hi:[1,0,1]
	s_branch .Lp6b2_axdone
.Lp6b2_t1:
	v_readlane_b32 s14, v1, 0
	v_cvt_pk_f32_fp8_e32 v[184:185], v224
	v_cvt_pk_f32_fp8_sdwa v[186:187], v224 src0_sel:WORD_1
	v_pk_fma_f32 v[110:111], v[184:185], s[14:15], v[110:111] op_sel_hi:[1,0,1]
	v_pk_fma_f32 v[112:113], v[186:187], s[14:15], v[112:113] op_sel_hi:[1,0,1]
	v_cvt_pk_f32_fp8_e32 v[188:189], v225
	v_cvt_pk_f32_fp8_sdwa v[190:191], v225 src0_sel:WORD_1
	v_pk_fma_f32 v[114:115], v[188:189], s[14:15], v[114:115] op_sel_hi:[1,0,1]
	v_pk_fma_f32 v[116:117], v[190:191], s[14:15], v[116:117] op_sel_hi:[1,0,1]
	v_cvt_pk_f32_fp8_e32 v[184:185], v226
	v_cvt_pk_f32_fp8_sdwa v[186:187], v226 src0_sel:WORD_1
	v_pk_fma_f32 v[118:119], v[184:185], s[14:15], v[118:119] op_sel_hi:[1,0,1]
	v_pk_fma_f32 v[120:121], v[186:187], s[14:15], v[120:121] op_sel_hi:[1,0,1]
	v_cvt_pk_f32_fp8_e32 v[188:189], v227
	v_cvt_pk_f32_fp8_sdwa v[190:191], v227 src0_sel:WORD_1
	v_pk_fma_f32 v[122:123], v[188:189], s[14:15], v[122:123] op_sel_hi:[1,0,1]
	v_pk_fma_f32 v[124:125], v[190:191], s[14:15], v[124:125] op_sel_hi:[1,0,1]
	v_readlane_b32 s14, v1, 8
	v_cvt_pk_f32_fp8_e32 v[184:185], v228
	v_cvt_pk_f32_fp8_sdwa v[186:187], v228 src0_sel:WORD_1
	v_pk_fma_f32 v[110:111], v[184:185], s[14:15], v[110:111] op_sel_hi:[1,0,1]
	v_pk_fma_f32 v[112:113], v[186:187], s[14:15], v[112:113] op_sel_hi:[1,0,1]
	v_cvt_pk_f32_fp8_e32 v[188:189], v229
	v_cvt_pk_f32_fp8_sdwa v[190:191], v229 src0_sel:WORD_1
	v_pk_fma_f32 v[114:115], v[188:189], s[14:15], v[114:115] op_sel_hi:[1,0,1]
	v_pk_fma_f32 v[116:117], v[190:191], s[14:15], v[116:117] op_sel_hi:[1,0,1]
	v_cvt_pk_f32_fp8_e32 v[184:185], v230
	v_cvt_pk_f32_fp8_sdwa v[186:187], v230 src0_sel:WORD_1
	v_pk_fma_f32 v[118:119], v[184:185], s[14:15], v[118:119] op_sel_hi:[1,0,1]
	v_pk_fma_f32 v[120:121], v[186:187], s[14:15], v[120:121] op_sel_hi:[1,0,1]
	v_cvt_pk_f32_fp8_e32 v[188:189], v231
	v_cvt_pk_f32_fp8_sdwa v[190:191], v231 src0_sel:WORD_1
	v_pk_fma_f32 v[122:123], v[188:189], s[14:15], v[122:123] op_sel_hi:[1,0,1]
	v_pk_fma_f32 v[124:125], v[190:191], s[14:15], v[124:125] op_sel_hi:[1,0,1]
	s_cmp_le_u32 s36, 2
	s_cbranch_scc1 .Lp6b2_axdone
	v_readlane_b32 s14, v1, 16
	v_cvt_pk_f32_fp8_e32 v[184:185], v232
	v_cvt_pk_f32_fp8_sdwa v[186:187], v232 src0_sel:WORD_1
	v_pk_fma_f32 v[110:111], v[184:185], s[14:15], v[110:111] op_sel_hi:[1,0,1]
	v_pk_fma_f32 v[112:113], v[186:187], s[14:15], v[112:113] op_sel_hi:[1,0,1]
	v_cvt_pk_f32_fp8_e32 v[188:189], v233
	v_cvt_pk_f32_fp8_sdwa v[190:191], v233 src0_sel:WORD_1
	v_pk_fma_f32 v[114:115], v[188:189], s[14:15], v[114:115] op_sel_hi:[1,0,1]
	v_pk_fma_f32 v[116:117], v[190:191], s[14:15], v[116:117] op_sel_hi:[1,0,1]
	v_cvt_pk_f32_fp8_e32 v[184:185], v234
	v_cvt_pk_f32_fp8_sdwa v[186:187], v234 src0_sel:WORD_1
	v_pk_fma_f32 v[118:119], v[184:185], s[14:15], v[118:119] op_sel_hi:[1,0,1]
	v_pk_fma_f32 v[120:121], v[186:187], s[14:15], v[120:121] op_sel_hi:[1,0,1]
	v_cvt_pk_f32_fp8_e32 v[188:189], v235
	v_cvt_pk_f32_fp8_sdwa v[190:191], v235 src0_sel:WORD_1
	v_pk_fma_f32 v[122:123], v[188:189], s[14:15], v[122:123] op_sel_hi:[1,0,1]
	v_pk_fma_f32 v[124:125], v[190:191], s[14:15], v[124:125] op_sel_hi:[1,0,1]
	v_readlane_b32 s14, v1, 24
	v_cvt_pk_f32_fp8_e32 v[184:185], v236
	v_cvt_pk_f32_fp8_sdwa v[186:187], v236 src0_sel:WORD_1
	v_pk_fma_f32 v[110:111], v[184:185], s[14:15], v[110:111] op_sel_hi:[1,0,1]
	v_pk_fma_f32 v[112:113], v[186:187], s[14:15], v[112:113] op_sel_hi:[1,0,1]
	v_cvt_pk_f32_fp8_e32 v[188:189], v237
	v_cvt_pk_f32_fp8_sdwa v[190:191], v237 src0_sel:WORD_1
	v_pk_fma_f32 v[114:115], v[188:189], s[14:15], v[114:115] op_sel_hi:[1,0,1]
	v_pk_fma_f32 v[116:117], v[190:191], s[14:15], v[116:117] op_sel_hi:[1,0,1]
	v_cvt_pk_f32_fp8_e32 v[184:185], v238
	v_cvt_pk_f32_fp8_sdwa v[186:187], v238 src0_sel:WORD_1
	v_pk_fma_f32 v[118:119], v[184:185], s[14:15], v[118:119] op_sel_hi:[1,0,1]
	v_pk_fma_f32 v[120:121], v[186:187], s[14:15], v[120:121] op_sel_hi:[1,0,1]
	v_cvt_pk_f32_fp8_e32 v[188:189], v239
	v_cvt_pk_f32_fp8_sdwa v[190:191], v239 src0_sel:WORD_1
	v_pk_fma_f32 v[122:123], v[188:189], s[14:15], v[122:123] op_sel_hi:[1,0,1]
	v_pk_fma_f32 v[124:125], v[190:191], s[14:15], v[124:125] op_sel_hi:[1,0,1]
	s_cmp_le_u32 s36, 4
	s_cbranch_scc1 .Lp6b2_axdone
	v_readlane_b32 s14, v1, 32
	v_cvt_pk_f32_fp8_e32 v[184:185], v240
	v_cvt_pk_f32_fp8_sdwa v[186:187], v240 src0_sel:WORD_1
	v_pk_fma_f32 v[110:111], v[184:185], s[14:15], v[110:111] op_sel_hi:[1,0,1]
	v_pk_fma_f32 v[112:113], v[186:187], s[14:15], v[112:113] op_sel_hi:[1,0,1]
	v_cvt_pk_f32_fp8_e32 v[188:189], v241
	v_cvt_pk_f32_fp8_sdwa v[190:191], v241 src0_sel:WORD_1
	v_pk_fma_f32 v[114:115], v[188:189], s[14:15], v[114:115] op_sel_hi:[1,0,1]
	v_pk_fma_f32 v[116:117], v[190:191], s[14:15], v[116:117] op_sel_hi:[1,0,1]
	v_cvt_pk_f32_fp8_e32 v[184:185], v242
	v_cvt_pk_f32_fp8_sdwa v[186:187], v242 src0_sel:WORD_1
	v_pk_fma_f32 v[118:119], v[184:185], s[14:15], v[118:119] op_sel_hi:[1,0,1]
	v_pk_fma_f32 v[120:121], v[186:187], s[14:15], v[120:121] op_sel_hi:[1,0,1]
	v_cvt_pk_f32_fp8_e32 v[188:189], v243
	v_cvt_pk_f32_fp8_sdwa v[190:191], v243 src0_sel:WORD_1
	v_pk_fma_f32 v[122:123], v[188:189], s[14:15], v[122:123] op_sel_hi:[1,0,1]
	v_pk_fma_f32 v[124:125], v[190:191], s[14:15], v[124:125] op_sel_hi:[1,0,1]
	v_readlane_b32 s14, v1, 40
	v_cvt_pk_f32_fp8_e32 v[184:185], v244
	v_cvt_pk_f32_fp8_sdwa v[186:187], v244 src0_sel:WORD_1
	v_pk_fma_f32 v[110:111], v[184:185], s[14:15], v[110:111] op_sel_hi:[1,0,1]
	v_pk_fma_f32 v[112:113], v[186:187], s[14:15], v[112:113] op_sel_hi:[1,0,1]
	v_cvt_pk_f32_fp8_e32 v[188:189], v245
	v_cvt_pk_f32_fp8_sdwa v[190:191], v245 src0_sel:WORD_1
	v_pk_fma_f32 v[114:115], v[188:189], s[14:15], v[114:115] op_sel_hi:[1,0,1]
	v_pk_fma_f32 v[116:117], v[190:191], s[14:15], v[116:117] op_sel_hi:[1,0,1]
	v_cvt_pk_f32_fp8_e32 v[184:185], v246
	v_cvt_pk_f32_fp8_sdwa v[186:187], v246 src0_sel:WORD_1
	v_pk_fma_f32 v[118:119], v[184:185], s[14:15], v[118:119] op_sel_hi:[1,0,1]
	v_pk_fma_f32 v[120:121], v[186:187], s[14:15], v[120:121] op_sel_hi:[1,0,1]
	v_cvt_pk_f32_fp8_e32 v[188:189], v247
	v_cvt_pk_f32_fp8_sdwa v[190:191], v247 src0_sel:WORD_1
	v_pk_fma_f32 v[122:123], v[188:189], s[14:15], v[122:123] op_sel_hi:[1,0,1]
	v_pk_fma_f32 v[124:125], v[190:191], s[14:15], v[124:125] op_sel_hi:[1,0,1]
	s_cmp_le_u32 s36, 6
	s_cbranch_scc1 .Lp6b2_axdone
	v_readlane_b32 s14, v1, 48
	v_cvt_pk_f32_fp8_e32 v[184:185], v248
	v_cvt_pk_f32_fp8_sdwa v[186:187], v248 src0_sel:WORD_1
	v_pk_fma_f32 v[110:111], v[184:185], s[14:15], v[110:111] op_sel_hi:[1,0,1]
	v_pk_fma_f32 v[112:113], v[186:187], s[14:15], v[112:113] op_sel_hi:[1,0,1]
	v_cvt_pk_f32_fp8_e32 v[188:189], v249
	v_cvt_pk_f32_fp8_sdwa v[190:191], v249 src0_sel:WORD_1
	v_pk_fma_f32 v[114:115], v[188:189], s[14:15], v[114:115] op_sel_hi:[1,0,1]
	v_pk_fma_f32 v[116:117], v[190:191], s[14:15], v[116:117] op_sel_hi:[1,0,1]
	v_cvt_pk_f32_fp8_e32 v[184:185], v250
	v_cvt_pk_f32_fp8_sdwa v[186:187], v250 src0_sel:WORD_1
	v_pk_fma_f32 v[118:119], v[184:185], s[14:15], v[118:119] op_sel_hi:[1,0,1]
	v_pk_fma_f32 v[120:121], v[186:187], s[14:15], v[120:121] op_sel_hi:[1,0,1]
	v_cvt_pk_f32_fp8_e32 v[188:189], v251
	v_cvt_pk_f32_fp8_sdwa v[190:191], v251 src0_sel:WORD_1
	v_pk_fma_f32 v[122:123], v[188:189], s[14:15], v[122:123] op_sel_hi:[1,0,1]
	v_pk_fma_f32 v[124:125], v[190:191], s[14:15], v[124:125] op_sel_hi:[1,0,1]
	v_readlane_b32 s14, v1, 56
	v_cvt_pk_f32_fp8_e32 v[184:185], v216
	v_cvt_pk_f32_fp8_sdwa v[186:187], v216 src0_sel:WORD_1
	v_pk_fma_f32 v[110:111], v[184:185], s[14:15], v[110:111] op_sel_hi:[1,0,1]
	v_pk_fma_f32 v[112:113], v[186:187], s[14:15], v[112:113] op_sel_hi:[1,0,1]
	v_cvt_pk_f32_fp8_e32 v[188:189], v217
	v_cvt_pk_f32_fp8_sdwa v[190:191], v217 src0_sel:WORD_1
	v_pk_fma_f32 v[114:115], v[188:189], s[14:15], v[114:115] op_sel_hi:[1,0,1]
	v_pk_fma_f32 v[116:117], v[190:191], s[14:15], v[116:117] op_sel_hi:[1,0,1]
	v_cvt_pk_f32_fp8_e32 v[184:185], v218
	v_cvt_pk_f32_fp8_sdwa v[186:187], v218 src0_sel:WORD_1
	v_pk_fma_f32 v[118:119], v[184:185], s[14:15], v[118:119] op_sel_hi:[1,0,1]
	v_pk_fma_f32 v[120:121], v[186:187], s[14:15], v[120:121] op_sel_hi:[1,0,1]
	v_cvt_pk_f32_fp8_e32 v[188:189], v219
	v_cvt_pk_f32_fp8_sdwa v[190:191], v219 src0_sel:WORD_1
	v_pk_fma_f32 v[122:123], v[188:189], s[14:15], v[122:123] op_sel_hi:[1,0,1]
	v_pk_fma_f32 v[124:125], v[190:191], s[14:15], v[124:125] op_sel_hi:[1,0,1]
	s_branch .Lp6b2_axdone
.Lp6b2_t0:
	v_readlane_b32 s14, v1, 0
	v_cvt_pk_f32_fp8_e32 v[184:185], v224
	v_cvt_pk_f32_fp8_sdwa v[186:187], v224 src0_sel:WORD_1
	v_pk_fma_f32 v[126:127], v[184:185], s[14:15], v[126:127] op_sel_hi:[1,0,1]
	v_pk_fma_f32 v[128:129], v[186:187], s[14:15], v[128:129] op_sel_hi:[1,0,1]
	v_cvt_pk_f32_fp8_e32 v[188:189], v225
	v_cvt_pk_f32_fp8_sdwa v[190:191], v225 src0_sel:WORD_1
	v_pk_fma_f32 v[130:131], v[188:189], s[14:15], v[130:131] op_sel_hi:[1,0,1]
	v_pk_fma_f32 v[132:133], v[190:191], s[14:15], v[132:133] op_sel_hi:[1,0,1]
	v_cvt_pk_f32_fp8_e32 v[184:185], v226
	v_cvt_pk_f32_fp8_sdwa v[186:187], v226 src0_sel:WORD_1
	v_pk_fma_f32 v[134:135], v[184:185], s[14:15], v[134:135] op_sel_hi:[1,0,1]
	v_pk_fma_f32 v[136:137], v[186:187], s[14:15], v[136:137] op_sel_hi:[1,0,1]
	v_cvt_pk_f32_fp8_e32 v[188:189], v227
	v_cvt_pk_f32_fp8_sdwa v[190:191], v227 src0_sel:WORD_1
	v_pk_fma_f32 v[138:139], v[188:189], s[14:15], v[138:139] op_sel_hi:[1,0,1]
	v_pk_fma_f32 v[140:141], v[190:191], s[14:15], v[140:141] op_sel_hi:[1,0,1]
	v_readlane_b32 s14, v1, 8
	v_cvt_pk_f32_fp8_e32 v[184:185], v228
	v_cvt_pk_f32_fp8_sdwa v[186:187], v228 src0_sel:WORD_1
	v_pk_fma_f32 v[126:127], v[184:185], s[14:15], v[126:127] op_sel_hi:[1,0,1]
	v_pk_fma_f32 v[128:129], v[186:187], s[14:15], v[128:129] op_sel_hi:[1,0,1]
	v_cvt_pk_f32_fp8_e32 v[188:189], v229
	v_cvt_pk_f32_fp8_sdwa v[190:191], v229 src0_sel:WORD_1
	v_pk_fma_f32 v[130:131], v[188:189], s[14:15], v[130:131] op_sel_hi:[1,0,1]
	v_pk_fma_f32 v[132:133], v[190:191], s[14:15], v[132:133] op_sel_hi:[1,0,1]
	v_cvt_pk_f32_fp8_e32 v[184:185], v230
	v_cvt_pk_f32_fp8_sdwa v[186:187], v230 src0_sel:WORD_1
	v_pk_fma_f32 v[134:135], v[184:185], s[14:15], v[134:135] op_sel_hi:[1,0,1]
	v_pk_fma_f32 v[136:137], v[186:187], s[14:15], v[136:137] op_sel_hi:[1,0,1]
	v_cvt_pk_f32_fp8_e32 v[188:189], v231
	v_cvt_pk_f32_fp8_sdwa v[190:191], v231 src0_sel:WORD_1
	v_pk_fma_f32 v[138:139], v[188:189], s[14:15], v[138:139] op_sel_hi:[1,0,1]
	v_pk_fma_f32 v[140:141], v[190:191], s[14:15], v[140:141] op_sel_hi:[1,0,1]
	s_cmp_le_u32 s36, 2
	s_cbranch_scc1 .Lp6b2_axdone
	v_readlane_b32 s14, v1, 16
	v_cvt_pk_f32_fp8_e32 v[184:185], v232
	v_cvt_pk_f32_fp8_sdwa v[186:187], v232 src0_sel:WORD_1
	v_pk_fma_f32 v[126:127], v[184:185], s[14:15], v[126:127] op_sel_hi:[1,0,1]
	v_pk_fma_f32 v[128:129], v[186:187], s[14:15], v[128:129] op_sel_hi:[1,0,1]
	v_cvt_pk_f32_fp8_e32 v[188:189], v233
	v_cvt_pk_f32_fp8_sdwa v[190:191], v233 src0_sel:WORD_1
	v_pk_fma_f32 v[130:131], v[188:189], s[14:15], v[130:131] op_sel_hi:[1,0,1]
	v_pk_fma_f32 v[132:133], v[190:191], s[14:15], v[132:133] op_sel_hi:[1,0,1]
	v_cvt_pk_f32_fp8_e32 v[184:185], v234
	v_cvt_pk_f32_fp8_sdwa v[186:187], v234 src0_sel:WORD_1
	v_pk_fma_f32 v[134:135], v[184:185], s[14:15], v[134:135] op_sel_hi:[1,0,1]
	v_pk_fma_f32 v[136:137], v[186:187], s[14:15], v[136:137] op_sel_hi:[1,0,1]
	v_cvt_pk_f32_fp8_e32 v[188:189], v235
	v_cvt_pk_f32_fp8_sdwa v[190:191], v235 src0_sel:WORD_1
	v_pk_fma_f32 v[138:139], v[188:189], s[14:15], v[138:139] op_sel_hi:[1,0,1]
	v_pk_fma_f32 v[140:141], v[190:191], s[14:15], v[140:141] op_sel_hi:[1,0,1]
	v_readlane_b32 s14, v1, 24
	v_cvt_pk_f32_fp8_e32 v[184:185], v236
	v_cvt_pk_f32_fp8_sdwa v[186:187], v236 src0_sel:WORD_1
	v_pk_fma_f32 v[126:127], v[184:185], s[14:15], v[126:127] op_sel_hi:[1,0,1]
	v_pk_fma_f32 v[128:129], v[186:187], s[14:15], v[128:129] op_sel_hi:[1,0,1]
	v_cvt_pk_f32_fp8_e32 v[188:189], v237
	v_cvt_pk_f32_fp8_sdwa v[190:191], v237 src0_sel:WORD_1
	v_pk_fma_f32 v[130:131], v[188:189], s[14:15], v[130:131] op_sel_hi:[1,0,1]
	v_pk_fma_f32 v[132:133], v[190:191], s[14:15], v[132:133] op_sel_hi:[1,0,1]
	v_cvt_pk_f32_fp8_e32 v[184:185], v238
	v_cvt_pk_f32_fp8_sdwa v[186:187], v238 src0_sel:WORD_1
	v_pk_fma_f32 v[134:135], v[184:185], s[14:15], v[134:135] op_sel_hi:[1,0,1]
	v_pk_fma_f32 v[136:137], v[186:187], s[14:15], v[136:137] op_sel_hi:[1,0,1]
	v_cvt_pk_f32_fp8_e32 v[188:189], v239
	v_cvt_pk_f32_fp8_sdwa v[190:191], v239 src0_sel:WORD_1
	v_pk_fma_f32 v[138:139], v[188:189], s[14:15], v[138:139] op_sel_hi:[1,0,1]
	v_pk_fma_f32 v[140:141], v[190:191], s[14:15], v[140:141] op_sel_hi:[1,0,1]
	s_cmp_le_u32 s36, 4
	s_cbranch_scc1 .Lp6b2_axdone
	v_readlane_b32 s14, v1, 32
	v_cvt_pk_f32_fp8_e32 v[184:185], v240
	v_cvt_pk_f32_fp8_sdwa v[186:187], v240 src0_sel:WORD_1
	v_pk_fma_f32 v[126:127], v[184:185], s[14:15], v[126:127] op_sel_hi:[1,0,1]
	v_pk_fma_f32 v[128:129], v[186:187], s[14:15], v[128:129] op_sel_hi:[1,0,1]
	v_cvt_pk_f32_fp8_e32 v[188:189], v241
	v_cvt_pk_f32_fp8_sdwa v[190:191], v241 src0_sel:WORD_1
	v_pk_fma_f32 v[130:131], v[188:189], s[14:15], v[130:131] op_sel_hi:[1,0,1]
	v_pk_fma_f32 v[132:133], v[190:191], s[14:15], v[132:133] op_sel_hi:[1,0,1]
	v_cvt_pk_f32_fp8_e32 v[184:185], v242
	v_cvt_pk_f32_fp8_sdwa v[186:187], v242 src0_sel:WORD_1
	v_pk_fma_f32 v[134:135], v[184:185], s[14:15], v[134:135] op_sel_hi:[1,0,1]
	v_pk_fma_f32 v[136:137], v[186:187], s[14:15], v[136:137] op_sel_hi:[1,0,1]
	v_cvt_pk_f32_fp8_e32 v[188:189], v243
	v_cvt_pk_f32_fp8_sdwa v[190:191], v243 src0_sel:WORD_1
	v_pk_fma_f32 v[138:139], v[188:189], s[14:15], v[138:139] op_sel_hi:[1,0,1]
	v_pk_fma_f32 v[140:141], v[190:191], s[14:15], v[140:141] op_sel_hi:[1,0,1]
	v_readlane_b32 s14, v1, 40
	v_cvt_pk_f32_fp8_e32 v[184:185], v244
	v_cvt_pk_f32_fp8_sdwa v[186:187], v244 src0_sel:WORD_1
	v_pk_fma_f32 v[126:127], v[184:185], s[14:15], v[126:127] op_sel_hi:[1,0,1]
	v_pk_fma_f32 v[128:129], v[186:187], s[14:15], v[128:129] op_sel_hi:[1,0,1]
	v_cvt_pk_f32_fp8_e32 v[188:189], v245
	v_cvt_pk_f32_fp8_sdwa v[190:191], v245 src0_sel:WORD_1
	v_pk_fma_f32 v[130:131], v[188:189], s[14:15], v[130:131] op_sel_hi:[1,0,1]
	v_pk_fma_f32 v[132:133], v[190:191], s[14:15], v[132:133] op_sel_hi:[1,0,1]
	v_cvt_pk_f32_fp8_e32 v[184:185], v246
	v_cvt_pk_f32_fp8_sdwa v[186:187], v246 src0_sel:WORD_1
	v_pk_fma_f32 v[134:135], v[184:185], s[14:15], v[134:135] op_sel_hi:[1,0,1]
	v_pk_fma_f32 v[136:137], v[186:187], s[14:15], v[136:137] op_sel_hi:[1,0,1]
	v_cvt_pk_f32_fp8_e32 v[188:189], v247
	v_cvt_pk_f32_fp8_sdwa v[190:191], v247 src0_sel:WORD_1
	v_pk_fma_f32 v[138:139], v[188:189], s[14:15], v[138:139] op_sel_hi:[1,0,1]
	v_pk_fma_f32 v[140:141], v[190:191], s[14:15], v[140:141] op_sel_hi:[1,0,1]
	s_cmp_le_u32 s36, 6
	s_cbranch_scc1 .Lp6b2_axdone
	v_readlane_b32 s14, v1, 48
	v_cvt_pk_f32_fp8_e32 v[184:185], v248
	v_cvt_pk_f32_fp8_sdwa v[186:187], v248 src0_sel:WORD_1
	v_pk_fma_f32 v[126:127], v[184:185], s[14:15], v[126:127] op_sel_hi:[1,0,1]
	v_pk_fma_f32 v[128:129], v[186:187], s[14:15], v[128:129] op_sel_hi:[1,0,1]
	v_cvt_pk_f32_fp8_e32 v[188:189], v249
	v_cvt_pk_f32_fp8_sdwa v[190:191], v249 src0_sel:WORD_1
	v_pk_fma_f32 v[130:131], v[188:189], s[14:15], v[130:131] op_sel_hi:[1,0,1]
	v_pk_fma_f32 v[132:133], v[190:191], s[14:15], v[132:133] op_sel_hi:[1,0,1]
	v_cvt_pk_f32_fp8_e32 v[184:185], v250
	v_cvt_pk_f32_fp8_sdwa v[186:187], v250 src0_sel:WORD_1
	v_pk_fma_f32 v[134:135], v[184:185], s[14:15], v[134:135] op_sel_hi:[1,0,1]
	v_pk_fma_f32 v[136:137], v[186:187], s[14:15], v[136:137] op_sel_hi:[1,0,1]
	v_cvt_pk_f32_fp8_e32 v[188:189], v251
	v_cvt_pk_f32_fp8_sdwa v[190:191], v251 src0_sel:WORD_1
	v_pk_fma_f32 v[138:139], v[188:189], s[14:15], v[138:139] op_sel_hi:[1,0,1]
	v_pk_fma_f32 v[140:141], v[190:191], s[14:15], v[140:141] op_sel_hi:[1,0,1]
	v_readlane_b32 s14, v1, 56
	v_cvt_pk_f32_fp8_e32 v[184:185], v216
	v_cvt_pk_f32_fp8_sdwa v[186:187], v216 src0_sel:WORD_1
	v_pk_fma_f32 v[126:127], v[184:185], s[14:15], v[126:127] op_sel_hi:[1,0,1]
	v_pk_fma_f32 v[128:129], v[186:187], s[14:15], v[128:129] op_sel_hi:[1,0,1]
	v_cvt_pk_f32_fp8_e32 v[188:189], v217
	v_cvt_pk_f32_fp8_sdwa v[190:191], v217 src0_sel:WORD_1
	v_pk_fma_f32 v[130:131], v[188:189], s[14:15], v[130:131] op_sel_hi:[1,0,1]
	v_pk_fma_f32 v[132:133], v[190:191], s[14:15], v[132:133] op_sel_hi:[1,0,1]
	v_cvt_pk_f32_fp8_e32 v[184:185], v218
	v_cvt_pk_f32_fp8_sdwa v[186:187], v218 src0_sel:WORD_1
	v_pk_fma_f32 v[134:135], v[184:185], s[14:15], v[134:135] op_sel_hi:[1,0,1]
	v_pk_fma_f32 v[136:137], v[186:187], s[14:15], v[136:137] op_sel_hi:[1,0,1]
	v_cvt_pk_f32_fp8_e32 v[188:189], v219
	v_cvt_pk_f32_fp8_sdwa v[190:191], v219 src0_sel:WORD_1
	v_pk_fma_f32 v[138:139], v[188:189], s[14:15], v[138:139] op_sel_hi:[1,0,1]
	v_pk_fma_f32 v[140:141], v[190:191], s[14:15], v[140:141] op_sel_hi:[1,0,1]
.Lp6b2_axdone:
	s_nop 4
	buffer_load_dwordx4 v[224:227], v181, s[92:95], s44 offen
	buffer_load_dwordx4 v[228:231], v181, s[92:95], s45 offen
	buffer_load_dwordx4 v[232:235], v181, s[92:95], s46 offen
	buffer_load_dwordx4 v[236:239], v181, s[92:95], s47 offen
	buffer_load_dwordx4 v[240:243], v181, s[92:95], s48 offen
	buffer_load_dwordx4 v[244:247], v181, s[92:95], s49 offen
	buffer_load_dwordx4 v[248:251], v181, s[92:95], s50 offen
	buffer_load_dwordx4 v[216:219], v181, s[92:95], s51 offen
	s_mov_b32 s26, s86
	s_mov_b32 s86, s27
	s_mov_b32 s27, s32
	s_cmp_eq_u32 s22, s23
	s_cbranch_scc1 .LBB0_973
	s_branch .Lp6b0_top
